# GEMM peel + redundant lgkmcnt(0) and setprio pairs removed from MFMA blocks
# speedup vs baseline: 1.0040x; 1.0040x over previous
.LBB0_210:
	s_ashr_i32 s49, s48, 31
	s_lshl_b64 s[4:5], s[48:49], 19
	s_add_u32 s50, s6, s4
	s_addc_u32 s51, s7, s5
	s_and_b64 s[4:5], s[38:39], exec
	s_cselect_b32 s49, s51, s41
	s_cselect_b32 s64, s50, s40
	s_ashr_i32 s45, s44, 31
	s_lshl_b64 s[4:5], s[44:45], 19
	s_add_u32 s52, s8, s4
	s_addc_u32 s53, s9, s5
	s_and_b64 s[4:5], s[38:39], exec
	s_cselect_b32 s45, s53, s43
	s_cselect_b32 s65, s52, s42
	s_add_u32 s70, s64, 0x80
	s_addc_u32 s71, s49, 0
	s_add_u32 s4, s40, 0x40080
	s_addc_u32 s5, s41, 0
	s_add_u32 s78, s42, 0x100
	v_lshl_add_u64 v[144:145], s[4:5], 0, v[140:141]
	v_lshl_add_u64 v[146:147], s[4:5], 0, v[142:143]
	s_addc_u32 s79, s43, 0
	s_mov_b32 s80, -2
	s_mov_b64 s[42:43], 0
	s_waitcnt lgkmcnt(0)
	s_add_u32 s4, s40, s42
	s_addc_u32 s5, s41, s43
	s_add_u32 s81, s4, 0x100
	s_addc_u32 s82, s5, 0
	s_add_u32 s60, s78, s42
	s_addc_u32 s61, s79, s43
	s_add_u32 s4, s4, 0x180
	s_addc_u32 s5, s5, 0
	s_add_i32 s83, 0, 0x10000
	s_add_i32 s84, 0, 0x14000
	v_add_u32_e32 v2, s83, v151
	s_waitcnt vmcnt(0)
	ds_read_b128 v[154:157], v2
	ds_read_b128 v[158:161], v2 offset:1024
	ds_read_b128 v[162:165], v2 offset:2048
	ds_read_b128 v[166:169], v2 offset:3072
	v_add_u32_e32 v2, s84, v151
	ds_read_b128 v[170:173], v2
	ds_read_b128 v[174:177], v2 offset:1024
	ds_read_b128 v[178:181], v2 offset:2048
	ds_read_b128 v[182:185], v2 offset:3072
	s_cmpk_eq_i32 s42, 0x700
	s_cselect_b32 s13, s71, s5
	s_cselect_b32 s12, s70, s4
	s_cselect_b32 s61, s45, s61
	s_cselect_b32 s60, s65, s60
	s_cselect_b32 s5, s49, s82
	s_cselect_b32 s4, s64, s81
	v_lshl_add_u64 v[148:149], v[144:145], 0, s[42:43]
	s_add_i32 m0, s17, 0xc000
	ds_read_b128 v[186:189], v153
	ds_read_b128 v[190:193], v153 offset:1024
	ds_read_b128 v[204:207], v153 offset:2048
	ds_read_b128 v[208:211], v153 offset:3072
	ds_read_b128 v[212:215], v153 offset:4096
	ds_read_b128 v[216:219], v153 offset:5120
	ds_read_b128 v[220:223], v153 offset:6144
	ds_read_b128 v[224:227], v153 offset:7168
	global_load_lds_dwordx4 v[148:149], off
	v_lshl_add_u64 v[148:149], v[146:147], 0, s[42:43]
	s_add_i32 m0, s17, 0xe000
	s_nop 0
	global_load_lds_dwordx4 v[148:149], off
	s_waitcnt vmcnt(8)
	s_waitcnt lgkmcnt(0)
	s_barrier
	s_setprio 1
	v_mfma_f32_16x16x32_bf16 v[128:131], v[154:157], v[186:189], 0
	v_mfma_f32_16x16x32_bf16 v[124:127], v[162:165], v[186:189], 0
	v_mfma_f32_16x16x32_bf16 v[112:115], v[154:157], v[204:207], 0
	v_mfma_f32_16x16x32_bf16 v[108:111], v[162:165], v[204:207], 0
	v_mfma_f32_16x16x32_bf16 v[96:99], v[154:157], v[212:215], 0
	v_mfma_f32_16x16x32_bf16 v[92:95], v[162:165], v[212:215], 0
	v_mfma_f32_16x16x32_bf16 v[80:83], v[154:157], v[220:223], 0
	v_mfma_f32_16x16x32_bf16 v[76:79], v[162:165], v[220:223], 0
	v_mfma_f32_16x16x32_bf16 v[128:131], v[158:161], v[190:193], v[128:131]
	v_mfma_f32_16x16x32_bf16 v[124:127], v[166:169], v[190:193], v[124:127]
	v_mfma_f32_16x16x32_bf16 v[112:115], v[158:161], v[208:211], v[112:115]
	v_mfma_f32_16x16x32_bf16 v[108:111], v[166:169], v[208:211], v[108:111]
	v_mfma_f32_16x16x32_bf16 v[96:99], v[158:161], v[216:219], v[96:99]
	v_mfma_f32_16x16x32_bf16 v[92:95], v[166:169], v[216:219], v[92:95]
	v_mfma_f32_16x16x32_bf16 v[80:83], v[158:161], v[224:227], v[80:83]
	v_mfma_f32_16x16x32_bf16 v[76:79], v[166:169], v[224:227], v[76:79]
	v_mfma_f32_16x16x32_bf16 v[120:123], v[170:173], v[186:189], 0
	v_mfma_f32_16x16x32_bf16 v[116:119], v[178:181], v[186:189], 0
	v_mfma_f32_16x16x32_bf16 v[104:107], v[170:173], v[204:207], 0
	v_mfma_f32_16x16x32_bf16 v[100:103], v[178:181], v[204:207], 0
	v_mfma_f32_16x16x32_bf16 v[88:91], v[170:173], v[212:215], 0
	v_mfma_f32_16x16x32_bf16 v[84:87], v[178:181], v[212:215], 0
	v_mfma_f32_16x16x32_bf16 v[72:75], v[170:173], v[220:223], 0
	v_mfma_f32_16x16x32_bf16 v[68:71], v[178:181], v[220:223], 0
	v_mfma_f32_16x16x32_bf16 v[120:123], v[174:177], v[190:193], v[120:123]
	v_mfma_f32_16x16x32_bf16 v[116:119], v[182:185], v[190:193], v[116:119]
	v_mfma_f32_16x16x32_bf16 v[104:107], v[174:177], v[208:211], v[104:107]
	v_mfma_f32_16x16x32_bf16 v[100:103], v[182:185], v[208:211], v[100:103]
	v_mfma_f32_16x16x32_bf16 v[88:91], v[174:177], v[216:219], v[88:91]
	v_mfma_f32_16x16x32_bf16 v[84:87], v[182:185], v[216:219], v[84:87]
	v_mfma_f32_16x16x32_bf16 v[72:75], v[174:177], v[224:227], v[72:75]
	v_mfma_f32_16x16x32_bf16 v[68:71], v[182:185], v[224:227], v[68:71]
	s_setprio 0
	s_barrier
	s_add_i32 s81, s83, s16
	v_lshl_add_u64 v[148:149], s[60:61], 0, v[136:137]
	s_mov_b32 m0, s81
	ds_read_b128 v[186:189], v153 offset:16384
	ds_read_b128 v[190:193], v153 offset:17408
	ds_read_b128 v[204:207], v153 offset:18432
	ds_read_b128 v[208:211], v153 offset:19456
	ds_read_b128 v[212:215], v153 offset:20480
	ds_read_b128 v[216:219], v153 offset:21504
	ds_read_b128 v[220:223], v153 offset:22528
	ds_read_b128 v[224:227], v153 offset:23552
	global_load_lds_dwordx4 v[148:149], off
	s_add_i32 m0, s81, 0x2000
	s_add_u32 s82, s60, 0x40000
	v_lshl_add_u64 v[194:195], s[60:61], 0, v[132:133]
	s_addc_u32 s83, s61, 0
	s_add_i32 s81, s84, s16
	global_load_lds_dwordx4 v[194:195], off
	v_lshl_add_u64 v[196:197], s[82:83], 0, v[136:137]
	s_mov_b32 m0, s81
	s_nop 0
	global_load_lds_dwordx4 v[196:197], off
	v_lshl_add_u64 v[196:197], s[82:83], 0, v[132:133]
	s_add_i32 m0, s81, 0x2000
	s_nop 0
	global_load_lds_dwordx4 v[196:197], off
	v_lshl_add_u64 v[196:197], s[4:5], 0, v[138:139]
	s_mov_b32 m0, s17
	s_nop 0
	global_load_lds_dwordx4 v[196:197], off
	v_lshl_add_u64 v[196:197], s[4:5], 0, v[134:135]
	s_mov_b32 m0, s46
	s_nop 0
	global_load_lds_dwordx4 v[196:197], off
	s_waitcnt vmcnt(8)
	s_waitcnt lgkmcnt(0)
	s_barrier
	s_setprio 1
	v_mfma_f32_16x16x32_bf16 v[64:67], v[154:157], v[186:189], 0
	v_mfma_f32_16x16x32_bf16 v[60:63], v[162:165], v[186:189], 0
	v_mfma_f32_16x16x32_bf16 v[48:51], v[154:157], v[204:207], 0
	v_mfma_f32_16x16x32_bf16 v[44:47], v[162:165], v[204:207], 0
	v_mfma_f32_16x16x32_bf16 v[32:35], v[154:157], v[212:215], 0
	v_mfma_f32_16x16x32_bf16 v[28:31], v[162:165], v[212:215], 0
	v_mfma_f32_16x16x32_bf16 v[16:19], v[154:157], v[220:223], 0
	v_mfma_f32_16x16x32_bf16 v[12:15], v[162:165], v[220:223], 0
	v_mfma_f32_16x16x32_bf16 v[64:67], v[158:161], v[190:193], v[64:67]
	v_mfma_f32_16x16x32_bf16 v[60:63], v[166:169], v[190:193], v[60:63]
	v_mfma_f32_16x16x32_bf16 v[48:51], v[158:161], v[208:211], v[48:51]
	v_mfma_f32_16x16x32_bf16 v[44:47], v[166:169], v[208:211], v[44:47]
	v_mfma_f32_16x16x32_bf16 v[32:35], v[158:161], v[216:219], v[32:35]
	v_mfma_f32_16x16x32_bf16 v[28:31], v[166:169], v[216:219], v[28:31]
	v_mfma_f32_16x16x32_bf16 v[16:19], v[158:161], v[224:227], v[16:19]
	v_mfma_f32_16x16x32_bf16 v[12:15], v[166:169], v[224:227], v[12:15]
	v_mfma_f32_16x16x32_bf16 v[56:59], v[170:173], v[186:189], 0
	v_mfma_f32_16x16x32_bf16 v[52:55], v[178:181], v[186:189], 0
	v_mfma_f32_16x16x32_bf16 v[40:43], v[170:173], v[204:207], 0
	v_mfma_f32_16x16x32_bf16 v[36:39], v[178:181], v[204:207], 0
	v_mfma_f32_16x16x32_bf16 v[24:27], v[170:173], v[212:215], 0
	v_mfma_f32_16x16x32_bf16 v[20:23], v[178:181], v[212:215], 0
	v_mfma_f32_16x16x32_bf16 v[8:11], v[170:173], v[220:223], 0
	v_mfma_f32_16x16x32_bf16 v[4:7], v[178:181], v[220:223], 0
	v_mfma_f32_16x16x32_bf16 v[56:59], v[174:177], v[190:193], v[56:59]
	v_mfma_f32_16x16x32_bf16 v[52:55], v[182:185], v[190:193], v[52:55]
	v_mfma_f32_16x16x32_bf16 v[40:43], v[174:177], v[208:211], v[40:43]
	v_mfma_f32_16x16x32_bf16 v[36:39], v[182:185], v[208:211], v[36:39]
	v_mfma_f32_16x16x32_bf16 v[24:27], v[174:177], v[216:219], v[24:27]
	v_mfma_f32_16x16x32_bf16 v[20:23], v[182:185], v[216:219], v[20:23]
	v_mfma_f32_16x16x32_bf16 v[8:11], v[174:177], v[224:227], v[8:11]
	v_mfma_f32_16x16x32_bf16 v[4:7], v[182:185], v[224:227], v[4:7]
	s_setprio 0
	s_barrier
	s_add_i32 s81, 0, 0x18000
	v_add_u32_e32 v2, s81, v151
	s_add_i32 s82, 0, 0x1c000
	ds_read_b128 v[154:157], v2
	ds_read_b128 v[158:161], v2 offset:1024
	ds_read_b128 v[162:165], v2 offset:2048
	ds_read_b128 v[166:169], v2 offset:3072
	v_add_u32_e32 v2, s82, v151
	ds_read_b128 v[170:173], v2
	ds_read_b128 v[174:177], v2 offset:1024
	ds_read_b128 v[178:181], v2 offset:2048
	ds_read_b128 v[182:185], v2 offset:3072
	s_add_u32 s4, s4, 0x40000
	s_addc_u32 s5, s5, 0
	s_mov_b32 m0, s47
	v_lshl_add_u64 v[196:197], s[4:5], 0, v[138:139]
	ds_read_b128 v[186:189], v153 offset:32768
	ds_read_b128 v[190:193], v153 offset:33792
	ds_read_b128 v[204:207], v153 offset:34816
	ds_read_b128 v[208:211], v153 offset:35840
	ds_read_b128 v[212:215], v153 offset:36864
	ds_read_b128 v[216:219], v153 offset:37888
	ds_read_b128 v[220:223], v153 offset:38912
	ds_read_b128 v[224:227], v153 offset:39936
	global_load_lds_dwordx4 v[196:197], off
	v_lshl_add_u64 v[196:197], s[4:5], 0, v[134:135]
	s_mov_b32 m0, s58
	s_nop 0
	global_load_lds_dwordx4 v[196:197], off
	s_waitcnt vmcnt(8)
	s_waitcnt lgkmcnt(0)
	s_barrier
	s_setprio 1
	v_mfma_f32_16x16x32_bf16 v[128:131], v[154:157], v[186:189], v[128:131]
	v_mfma_f32_16x16x32_bf16 v[124:127], v[162:165], v[186:189], v[124:127]
	v_mfma_f32_16x16x32_bf16 v[112:115], v[154:157], v[204:207], v[112:115]
	v_mfma_f32_16x16x32_bf16 v[108:111], v[162:165], v[204:207], v[108:111]
	v_mfma_f32_16x16x32_bf16 v[96:99], v[154:157], v[212:215], v[96:99]
	v_mfma_f32_16x16x32_bf16 v[92:95], v[162:165], v[212:215], v[92:95]
	v_mfma_f32_16x16x32_bf16 v[80:83], v[154:157], v[220:223], v[80:83]
	v_mfma_f32_16x16x32_bf16 v[76:79], v[162:165], v[220:223], v[76:79]
	v_mfma_f32_16x16x32_bf16 v[128:131], v[158:161], v[190:193], v[128:131]
	v_mfma_f32_16x16x32_bf16 v[124:127], v[166:169], v[190:193], v[124:127]
	v_mfma_f32_16x16x32_bf16 v[112:115], v[158:161], v[208:211], v[112:115]
	v_mfma_f32_16x16x32_bf16 v[108:111], v[166:169], v[208:211], v[108:111]
	v_mfma_f32_16x16x32_bf16 v[96:99], v[158:161], v[216:219], v[96:99]
	v_mfma_f32_16x16x32_bf16 v[92:95], v[166:169], v[216:219], v[92:95]
	v_mfma_f32_16x16x32_bf16 v[80:83], v[158:161], v[224:227], v[80:83]
	v_mfma_f32_16x16x32_bf16 v[76:79], v[166:169], v[224:227], v[76:79]
	v_mfma_f32_16x16x32_bf16 v[120:123], v[170:173], v[186:189], v[120:123]
	v_mfma_f32_16x16x32_bf16 v[116:119], v[178:181], v[186:189], v[116:119]
	v_mfma_f32_16x16x32_bf16 v[104:107], v[170:173], v[204:207], v[104:107]
	v_mfma_f32_16x16x32_bf16 v[100:103], v[178:181], v[204:207], v[100:103]
	v_mfma_f32_16x16x32_bf16 v[88:91], v[170:173], v[212:215], v[88:91]
	v_mfma_f32_16x16x32_bf16 v[84:87], v[178:181], v[212:215], v[84:87]
	v_mfma_f32_16x16x32_bf16 v[72:75], v[170:173], v[220:223], v[72:75]
	v_mfma_f32_16x16x32_bf16 v[68:71], v[178:181], v[220:223], v[68:71]
	v_mfma_f32_16x16x32_bf16 v[120:123], v[174:177], v[190:193], v[120:123]
	v_mfma_f32_16x16x32_bf16 v[116:119], v[182:185], v[190:193], v[116:119]
	v_mfma_f32_16x16x32_bf16 v[104:107], v[174:177], v[208:211], v[104:107]
	v_mfma_f32_16x16x32_bf16 v[100:103], v[182:185], v[208:211], v[100:103]
	v_mfma_f32_16x16x32_bf16 v[88:91], v[174:177], v[216:219], v[88:91]
	v_mfma_f32_16x16x32_bf16 v[84:87], v[182:185], v[216:219], v[84:87]
	v_mfma_f32_16x16x32_bf16 v[72:75], v[174:177], v[224:227], v[72:75]
	v_mfma_f32_16x16x32_bf16 v[68:71], v[182:185], v[224:227], v[68:71]
	s_setprio 0
	s_barrier
	s_add_i32 s4, s81, s16
	v_lshl_add_u64 v[148:149], v[148:149], 0, s[34:35]
	s_mov_b32 m0, s4
	ds_read_b128 v[186:189], v153 offset:49152
	ds_read_b128 v[190:193], v153 offset:50176
	ds_read_b128 v[204:207], v153 offset:51200
	ds_read_b128 v[208:211], v153 offset:52224
	ds_read_b128 v[212:215], v153 offset:53248
	ds_read_b128 v[216:219], v153 offset:54272
	ds_read_b128 v[220:223], v153 offset:55296
	ds_read_b128 v[224:227], v153 offset:56320
	global_load_lds_dwordx4 v[148:149], off
	s_add_i32 m0, s4, 0x2000
	s_add_u32 s4, s60, 0x40080
	v_lshl_add_u64 v[148:149], v[194:195], 0, s[34:35]
	s_addc_u32 s5, s61, 0
	s_add_i32 s60, s82, s16
	global_load_lds_dwordx4 v[148:149], off
	v_lshl_add_u64 v[148:149], s[4:5], 0, v[136:137]
	s_mov_b32 m0, s60
	s_nop 0
	global_load_lds_dwordx4 v[148:149], off
	v_lshl_add_u64 v[148:149], s[4:5], 0, v[132:133]
	s_add_i32 m0, s60, 0x2000
	s_nop 0
	global_load_lds_dwordx4 v[148:149], off
	v_lshl_add_u64 v[148:149], s[12:13], 0, v[138:139]
	s_mov_b32 m0, s74
	s_nop 0
	global_load_lds_dwordx4 v[148:149], off
	v_lshl_add_u64 v[148:149], s[12:13], 0, v[134:135]
	s_mov_b32 m0, s75
	s_nop 0
	global_load_lds_dwordx4 v[148:149], off
	s_waitcnt vmcnt(8)
	s_waitcnt lgkmcnt(0)
	s_barrier
	s_setprio 1
	v_mfma_f32_16x16x32_bf16 v[64:67], v[154:157], v[186:189], v[64:67]
	v_mfma_f32_16x16x32_bf16 v[60:63], v[162:165], v[186:189], v[60:63]
	v_mfma_f32_16x16x32_bf16 v[48:51], v[154:157], v[204:207], v[48:51]
	v_mfma_f32_16x16x32_bf16 v[44:47], v[162:165], v[204:207], v[44:47]
	v_mfma_f32_16x16x32_bf16 v[32:35], v[154:157], v[212:215], v[32:35]
	v_mfma_f32_16x16x32_bf16 v[28:31], v[162:165], v[212:215], v[28:31]
	v_mfma_f32_16x16x32_bf16 v[16:19], v[154:157], v[220:223], v[16:19]
	v_mfma_f32_16x16x32_bf16 v[12:15], v[162:165], v[220:223], v[12:15]
	v_mfma_f32_16x16x32_bf16 v[64:67], v[158:161], v[190:193], v[64:67]
	v_mfma_f32_16x16x32_bf16 v[60:63], v[166:169], v[190:193], v[60:63]
	v_mfma_f32_16x16x32_bf16 v[48:51], v[158:161], v[208:211], v[48:51]
	v_mfma_f32_16x16x32_bf16 v[44:47], v[166:169], v[208:211], v[44:47]
	v_mfma_f32_16x16x32_bf16 v[32:35], v[158:161], v[216:219], v[32:35]
	v_mfma_f32_16x16x32_bf16 v[28:31], v[166:169], v[216:219], v[28:31]
	v_mfma_f32_16x16x32_bf16 v[16:19], v[158:161], v[224:227], v[16:19]
	v_mfma_f32_16x16x32_bf16 v[12:15], v[166:169], v[224:227], v[12:15]
	v_mfma_f32_16x16x32_bf16 v[56:59], v[170:173], v[186:189], v[56:59]
	v_mfma_f32_16x16x32_bf16 v[52:55], v[178:181], v[186:189], v[52:55]
	v_mfma_f32_16x16x32_bf16 v[40:43], v[170:173], v[204:207], v[40:43]
	v_mfma_f32_16x16x32_bf16 v[36:39], v[178:181], v[204:207], v[36:39]
	v_mfma_f32_16x16x32_bf16 v[24:27], v[170:173], v[212:215], v[24:27]
	v_mfma_f32_16x16x32_bf16 v[20:23], v[178:181], v[212:215], v[20:23]
	v_mfma_f32_16x16x32_bf16 v[8:11], v[170:173], v[220:223], v[8:11]
	v_mfma_f32_16x16x32_bf16 v[4:7], v[178:181], v[220:223], v[4:7]
	v_mfma_f32_16x16x32_bf16 v[56:59], v[174:177], v[190:193], v[56:59]
	v_mfma_f32_16x16x32_bf16 v[52:55], v[182:185], v[190:193], v[52:55]
	v_mfma_f32_16x16x32_bf16 v[40:43], v[174:177], v[208:211], v[40:43]
	v_mfma_f32_16x16x32_bf16 v[36:39], v[182:185], v[208:211], v[36:39]
	v_mfma_f32_16x16x32_bf16 v[24:27], v[174:177], v[216:219], v[24:27]
	v_mfma_f32_16x16x32_bf16 v[20:23], v[182:185], v[216:219], v[20:23]
	v_mfma_f32_16x16x32_bf16 v[8:11], v[174:177], v[224:227], v[8:11]
	v_mfma_f32_16x16x32_bf16 v[4:7], v[182:185], v[224:227], v[4:7]
	s_setprio 0
	s_barrier
	s_add_i32 s80, s80, 2
	s_add_u32 s42, s42, 0x100
	s_addc_u32 s43, s43, 0
	s_cmp_gt_u32 s80, 13
.LBB0_211:
	s_add_u32 s4, s40, s42
	s_addc_u32 s5, s41, s43
	s_add_u32 s81, s4, 0x100
	s_addc_u32 s82, s5, 0
	s_add_u32 s60, s78, s42
	s_addc_u32 s61, s79, s43
	s_add_u32 s4, s4, 0x180
	s_addc_u32 s5, s5, 0
	s_add_i32 s83, 0, 0x10000
	s_add_i32 s84, 0, 0x14000
	v_add_u32_e32 v2, s83, v151
	s_waitcnt vmcnt(0)
	ds_read_b128 v[154:157], v2
	ds_read_b128 v[158:161], v2 offset:1024
	ds_read_b128 v[162:165], v2 offset:2048
	ds_read_b128 v[166:169], v2 offset:3072
	v_add_u32_e32 v2, s84, v151
	ds_read_b128 v[170:173], v2
	ds_read_b128 v[174:177], v2 offset:1024
	ds_read_b128 v[178:181], v2 offset:2048
	ds_read_b128 v[182:185], v2 offset:3072
	s_cmpk_eq_i32 s42, 0x700
	s_cselect_b32 s13, s71, s5
	s_cselect_b32 s12, s70, s4
	s_cselect_b32 s61, s45, s61
	s_cselect_b32 s60, s65, s60
	s_cselect_b32 s5, s49, s82
	s_cselect_b32 s4, s64, s81
	v_lshl_add_u64 v[148:149], v[144:145], 0, s[42:43]
	s_add_i32 m0, s17, 0xc000
	ds_read_b128 v[186:189], v153
	ds_read_b128 v[190:193], v153 offset:1024
	ds_read_b128 v[204:207], v153 offset:2048
	ds_read_b128 v[208:211], v153 offset:3072
	ds_read_b128 v[212:215], v153 offset:4096
	ds_read_b128 v[216:219], v153 offset:5120
	ds_read_b128 v[220:223], v153 offset:6144
	ds_read_b128 v[224:227], v153 offset:7168
	global_load_lds_dwordx4 v[148:149], off
	v_lshl_add_u64 v[148:149], v[146:147], 0, s[42:43]
	s_add_i32 m0, s17, 0xe000
	s_nop 0
	global_load_lds_dwordx4 v[148:149], off
	s_waitcnt vmcnt(8)
	s_waitcnt lgkmcnt(0)
	s_barrier
	s_setprio 1
	v_mfma_f32_16x16x32_bf16 v[128:131], v[154:157], v[186:189], v[128:131]
	v_mfma_f32_16x16x32_bf16 v[124:127], v[162:165], v[186:189], v[124:127]
	v_mfma_f32_16x16x32_bf16 v[112:115], v[154:157], v[204:207], v[112:115]
	v_mfma_f32_16x16x32_bf16 v[108:111], v[162:165], v[204:207], v[108:111]
	v_mfma_f32_16x16x32_bf16 v[96:99], v[154:157], v[212:215], v[96:99]
	v_mfma_f32_16x16x32_bf16 v[92:95], v[162:165], v[212:215], v[92:95]
	v_mfma_f32_16x16x32_bf16 v[80:83], v[154:157], v[220:223], v[80:83]
	v_mfma_f32_16x16x32_bf16 v[76:79], v[162:165], v[220:223], v[76:79]
	v_mfma_f32_16x16x32_bf16 v[128:131], v[158:161], v[190:193], v[128:131]
	v_mfma_f32_16x16x32_bf16 v[124:127], v[166:169], v[190:193], v[124:127]
	v_mfma_f32_16x16x32_bf16 v[112:115], v[158:161], v[208:211], v[112:115]
	v_mfma_f32_16x16x32_bf16 v[108:111], v[166:169], v[208:211], v[108:111]
	v_mfma_f32_16x16x32_bf16 v[96:99], v[158:161], v[216:219], v[96:99]
	v_mfma_f32_16x16x32_bf16 v[92:95], v[166:169], v[216:219], v[92:95]
	v_mfma_f32_16x16x32_bf16 v[80:83], v[158:161], v[224:227], v[80:83]
	v_mfma_f32_16x16x32_bf16 v[76:79], v[166:169], v[224:227], v[76:79]
	v_mfma_f32_16x16x32_bf16 v[120:123], v[170:173], v[186:189], v[120:123]
	v_mfma_f32_16x16x32_bf16 v[116:119], v[178:181], v[186:189], v[116:119]
	v_mfma_f32_16x16x32_bf16 v[104:107], v[170:173], v[204:207], v[104:107]
	v_mfma_f32_16x16x32_bf16 v[100:103], v[178:181], v[204:207], v[100:103]
	v_mfma_f32_16x16x32_bf16 v[88:91], v[170:173], v[212:215], v[88:91]
	v_mfma_f32_16x16x32_bf16 v[84:87], v[178:181], v[212:215], v[84:87]
	v_mfma_f32_16x16x32_bf16 v[72:75], v[170:173], v[220:223], v[72:75]
	v_mfma_f32_16x16x32_bf16 v[68:71], v[178:181], v[220:223], v[68:71]
	v_mfma_f32_16x16x32_bf16 v[120:123], v[174:177], v[190:193], v[120:123]
	v_mfma_f32_16x16x32_bf16 v[116:119], v[182:185], v[190:193], v[116:119]
	v_mfma_f32_16x16x32_bf16 v[104:107], v[174:177], v[208:211], v[104:107]
	v_mfma_f32_16x16x32_bf16 v[100:103], v[182:185], v[208:211], v[100:103]
	v_mfma_f32_16x16x32_bf16 v[88:91], v[174:177], v[216:219], v[88:91]
	v_mfma_f32_16x16x32_bf16 v[84:87], v[182:185], v[216:219], v[84:87]
	v_mfma_f32_16x16x32_bf16 v[72:75], v[174:177], v[224:227], v[72:75]
	v_mfma_f32_16x16x32_bf16 v[68:71], v[182:185], v[224:227], v[68:71]
	s_setprio 0
	s_barrier
	s_add_i32 s81, s83, s16
	v_lshl_add_u64 v[148:149], s[60:61], 0, v[136:137]
	s_mov_b32 m0, s81
	ds_read_b128 v[186:189], v153 offset:16384
	ds_read_b128 v[190:193], v153 offset:17408
	ds_read_b128 v[204:207], v153 offset:18432
	ds_read_b128 v[208:211], v153 offset:19456
	ds_read_b128 v[212:215], v153 offset:20480
	ds_read_b128 v[216:219], v153 offset:21504
	ds_read_b128 v[220:223], v153 offset:22528
	ds_read_b128 v[224:227], v153 offset:23552
	global_load_lds_dwordx4 v[148:149], off
	s_add_i32 m0, s81, 0x2000
	s_add_u32 s82, s60, 0x40000
	v_lshl_add_u64 v[194:195], s[60:61], 0, v[132:133]
	s_addc_u32 s83, s61, 0
	s_add_i32 s81, s84, s16
	global_load_lds_dwordx4 v[194:195], off
	v_lshl_add_u64 v[196:197], s[82:83], 0, v[136:137]
	s_mov_b32 m0, s81
	s_nop 0
	global_load_lds_dwordx4 v[196:197], off
	v_lshl_add_u64 v[196:197], s[82:83], 0, v[132:133]
	s_add_i32 m0, s81, 0x2000
	s_nop 0
	global_load_lds_dwordx4 v[196:197], off
	v_lshl_add_u64 v[196:197], s[4:5], 0, v[138:139]
	s_mov_b32 m0, s17
	s_nop 0
	global_load_lds_dwordx4 v[196:197], off
	v_lshl_add_u64 v[196:197], s[4:5], 0, v[134:135]
	s_mov_b32 m0, s46
	s_nop 0
	global_load_lds_dwordx4 v[196:197], off
	s_waitcnt vmcnt(8)
	s_waitcnt lgkmcnt(0)
	s_barrier
	s_setprio 1
	v_mfma_f32_16x16x32_bf16 v[64:67], v[154:157], v[186:189], v[64:67]
	v_mfma_f32_16x16x32_bf16 v[60:63], v[162:165], v[186:189], v[60:63]
	v_mfma_f32_16x16x32_bf16 v[48:51], v[154:157], v[204:207], v[48:51]
	v_mfma_f32_16x16x32_bf16 v[44:47], v[162:165], v[204:207], v[44:47]
	v_mfma_f32_16x16x32_bf16 v[32:35], v[154:157], v[212:215], v[32:35]
	v_mfma_f32_16x16x32_bf16 v[28:31], v[162:165], v[212:215], v[28:31]
	v_mfma_f32_16x16x32_bf16 v[16:19], v[154:157], v[220:223], v[16:19]
	v_mfma_f32_16x16x32_bf16 v[12:15], v[162:165], v[220:223], v[12:15]
	v_mfma_f32_16x16x32_bf16 v[64:67], v[158:161], v[190:193], v[64:67]
	v_mfma_f32_16x16x32_bf16 v[60:63], v[166:169], v[190:193], v[60:63]
	v_mfma_f32_16x16x32_bf16 v[48:51], v[158:161], v[208:211], v[48:51]
	v_mfma_f32_16x16x32_bf16 v[44:47], v[166:169], v[208:211], v[44:47]
	v_mfma_f32_16x16x32_bf16 v[32:35], v[158:161], v[216:219], v[32:35]
	v_mfma_f32_16x16x32_bf16 v[28:31], v[166:169], v[216:219], v[28:31]
	v_mfma_f32_16x16x32_bf16 v[16:19], v[158:161], v[224:227], v[16:19]
	v_mfma_f32_16x16x32_bf16 v[12:15], v[166:169], v[224:227], v[12:15]
	v_mfma_f32_16x16x32_bf16 v[56:59], v[170:173], v[186:189], v[56:59]
	v_mfma_f32_16x16x32_bf16 v[52:55], v[178:181], v[186:189], v[52:55]
	v_mfma_f32_16x16x32_bf16 v[40:43], v[170:173], v[204:207], v[40:43]
	v_mfma_f32_16x16x32_bf16 v[36:39], v[178:181], v[204:207], v[36:39]
	v_mfma_f32_16x16x32_bf16 v[24:27], v[170:173], v[212:215], v[24:27]
	v_mfma_f32_16x16x32_bf16 v[20:23], v[178:181], v[212:215], v[20:23]
	v_mfma_f32_16x16x32_bf16 v[8:11], v[170:173], v[220:223], v[8:11]
	v_mfma_f32_16x16x32_bf16 v[4:7], v[178:181], v[220:223], v[4:7]
	v_mfma_f32_16x16x32_bf16 v[56:59], v[174:177], v[190:193], v[56:59]
	v_mfma_f32_16x16x32_bf16 v[52:55], v[182:185], v[190:193], v[52:55]
	v_mfma_f32_16x16x32_bf16 v[40:43], v[174:177], v[208:211], v[40:43]
	v_mfma_f32_16x16x32_bf16 v[36:39], v[182:185], v[208:211], v[36:39]
	v_mfma_f32_16x16x32_bf16 v[24:27], v[174:177], v[216:219], v[24:27]
	v_mfma_f32_16x16x32_bf16 v[20:23], v[182:185], v[216:219], v[20:23]
	v_mfma_f32_16x16x32_bf16 v[8:11], v[174:177], v[224:227], v[8:11]
	v_mfma_f32_16x16x32_bf16 v[4:7], v[182:185], v[224:227], v[4:7]
	s_setprio 0
	s_barrier
	s_add_i32 s81, 0, 0x18000
	v_add_u32_e32 v2, s81, v151
	s_add_i32 s82, 0, 0x1c000
	ds_read_b128 v[154:157], v2
	ds_read_b128 v[158:161], v2 offset:1024
	ds_read_b128 v[162:165], v2 offset:2048
	ds_read_b128 v[166:169], v2 offset:3072
	v_add_u32_e32 v2, s82, v151
	ds_read_b128 v[170:173], v2
	ds_read_b128 v[174:177], v2 offset:1024
	ds_read_b128 v[178:181], v2 offset:2048
	ds_read_b128 v[182:185], v2 offset:3072
	s_add_u32 s4, s4, 0x40000
	s_addc_u32 s5, s5, 0
	s_mov_b32 m0, s47
	v_lshl_add_u64 v[196:197], s[4:5], 0, v[138:139]
	ds_read_b128 v[186:189], v153 offset:32768
	ds_read_b128 v[190:193], v153 offset:33792
	ds_read_b128 v[204:207], v153 offset:34816
	ds_read_b128 v[208:211], v153 offset:35840
	ds_read_b128 v[212:215], v153 offset:36864
	ds_read_b128 v[216:219], v153 offset:37888
	ds_read_b128 v[220:223], v153 offset:38912
	ds_read_b128 v[224:227], v153 offset:39936
	global_load_lds_dwordx4 v[196:197], off
	v_lshl_add_u64 v[196:197], s[4:5], 0, v[134:135]
	s_mov_b32 m0, s58
	s_nop 0
	global_load_lds_dwordx4 v[196:197], off
	s_waitcnt vmcnt(8)
	s_waitcnt lgkmcnt(0)
	s_barrier
	s_setprio 1
	v_mfma_f32_16x16x32_bf16 v[128:131], v[154:157], v[186:189], v[128:131]
	v_mfma_f32_16x16x32_bf16 v[124:127], v[162:165], v[186:189], v[124:127]
	v_mfma_f32_16x16x32_bf16 v[112:115], v[154:157], v[204:207], v[112:115]
	v_mfma_f32_16x16x32_bf16 v[108:111], v[162:165], v[204:207], v[108:111]
	v_mfma_f32_16x16x32_bf16 v[96:99], v[154:157], v[212:215], v[96:99]
	v_mfma_f32_16x16x32_bf16 v[92:95], v[162:165], v[212:215], v[92:95]
	v_mfma_f32_16x16x32_bf16 v[80:83], v[154:157], v[220:223], v[80:83]
	v_mfma_f32_16x16x32_bf16 v[76:79], v[162:165], v[220:223], v[76:79]
	v_mfma_f32_16x16x32_bf16 v[128:131], v[158:161], v[190:193], v[128:131]
	v_mfma_f32_16x16x32_bf16 v[124:127], v[166:169], v[190:193], v[124:127]
	v_mfma_f32_16x16x32_bf16 v[112:115], v[158:161], v[208:211], v[112:115]
	v_mfma_f32_16x16x32_bf16 v[108:111], v[166:169], v[208:211], v[108:111]
	v_mfma_f32_16x16x32_bf16 v[96:99], v[158:161], v[216:219], v[96:99]
	v_mfma_f32_16x16x32_bf16 v[92:95], v[166:169], v[216:219], v[92:95]
	v_mfma_f32_16x16x32_bf16 v[80:83], v[158:161], v[224:227], v[80:83]
	v_mfma_f32_16x16x32_bf16 v[76:79], v[166:169], v[224:227], v[76:79]
	v_mfma_f32_16x16x32_bf16 v[120:123], v[170:173], v[186:189], v[120:123]
	v_mfma_f32_16x16x32_bf16 v[116:119], v[178:181], v[186:189], v[116:119]
	v_mfma_f32_16x16x32_bf16 v[104:107], v[170:173], v[204:207], v[104:107]
	v_mfma_f32_16x16x32_bf16 v[100:103], v[178:181], v[204:207], v[100:103]
	v_mfma_f32_16x16x32_bf16 v[88:91], v[170:173], v[212:215], v[88:91]
	v_mfma_f32_16x16x32_bf16 v[84:87], v[178:181], v[212:215], v[84:87]
	v_mfma_f32_16x16x32_bf16 v[72:75], v[170:173], v[220:223], v[72:75]
	v_mfma_f32_16x16x32_bf16 v[68:71], v[178:181], v[220:223], v[68:71]
	v_mfma_f32_16x16x32_bf16 v[120:123], v[174:177], v[190:193], v[120:123]
	v_mfma_f32_16x16x32_bf16 v[116:119], v[182:185], v[190:193], v[116:119]
	v_mfma_f32_16x16x32_bf16 v[104:107], v[174:177], v[208:211], v[104:107]
	v_mfma_f32_16x16x32_bf16 v[100:103], v[182:185], v[208:211], v[100:103]
	v_mfma_f32_16x16x32_bf16 v[88:91], v[174:177], v[216:219], v[88:91]
	v_mfma_f32_16x16x32_bf16 v[84:87], v[182:185], v[216:219], v[84:87]
	v_mfma_f32_16x16x32_bf16 v[72:75], v[174:177], v[224:227], v[72:75]
	v_mfma_f32_16x16x32_bf16 v[68:71], v[182:185], v[224:227], v[68:71]
	s_setprio 0
	s_barrier
	s_add_i32 s4, s81, s16
	v_lshl_add_u64 v[148:149], v[148:149], 0, s[34:35]
	s_mov_b32 m0, s4
	ds_read_b128 v[186:189], v153 offset:49152
	ds_read_b128 v[190:193], v153 offset:50176
	ds_read_b128 v[204:207], v153 offset:51200
	ds_read_b128 v[208:211], v153 offset:52224
	ds_read_b128 v[212:215], v153 offset:53248
	ds_read_b128 v[216:219], v153 offset:54272
	ds_read_b128 v[220:223], v153 offset:55296
	ds_read_b128 v[224:227], v153 offset:56320
	global_load_lds_dwordx4 v[148:149], off
	s_add_i32 m0, s4, 0x2000
	s_add_u32 s4, s60, 0x40080
	v_lshl_add_u64 v[148:149], v[194:195], 0, s[34:35]
	s_addc_u32 s5, s61, 0
	s_add_i32 s60, s82, s16
	global_load_lds_dwordx4 v[148:149], off
	v_lshl_add_u64 v[148:149], s[4:5], 0, v[136:137]
	s_mov_b32 m0, s60
	s_nop 0
	global_load_lds_dwordx4 v[148:149], off
	v_lshl_add_u64 v[148:149], s[4:5], 0, v[132:133]
	s_add_i32 m0, s60, 0x2000
	s_nop 0
	global_load_lds_dwordx4 v[148:149], off
	v_lshl_add_u64 v[148:149], s[12:13], 0, v[138:139]
	s_mov_b32 m0, s74
	s_nop 0
	global_load_lds_dwordx4 v[148:149], off
	v_lshl_add_u64 v[148:149], s[12:13], 0, v[134:135]
	s_mov_b32 m0, s75
	s_nop 0
	global_load_lds_dwordx4 v[148:149], off
	s_waitcnt vmcnt(8)
	s_waitcnt lgkmcnt(0)
	s_barrier
	s_setprio 1
	v_mfma_f32_16x16x32_bf16 v[64:67], v[154:157], v[186:189], v[64:67]
	v_mfma_f32_16x16x32_bf16 v[60:63], v[162:165], v[186:189], v[60:63]
	v_mfma_f32_16x16x32_bf16 v[48:51], v[154:157], v[204:207], v[48:51]
	v_mfma_f32_16x16x32_bf16 v[44:47], v[162:165], v[204:207], v[44:47]
	v_mfma_f32_16x16x32_bf16 v[32:35], v[154:157], v[212:215], v[32:35]
	v_mfma_f32_16x16x32_bf16 v[28:31], v[162:165], v[212:215], v[28:31]
	v_mfma_f32_16x16x32_bf16 v[16:19], v[154:157], v[220:223], v[16:19]
	v_mfma_f32_16x16x32_bf16 v[12:15], v[162:165], v[220:223], v[12:15]
	v_mfma_f32_16x16x32_bf16 v[64:67], v[158:161], v[190:193], v[64:67]
	v_mfma_f32_16x16x32_bf16 v[60:63], v[166:169], v[190:193], v[60:63]
	v_mfma_f32_16x16x32_bf16 v[48:51], v[158:161], v[208:211], v[48:51]
	v_mfma_f32_16x16x32_bf16 v[44:47], v[166:169], v[208:211], v[44:47]
	v_mfma_f32_16x16x32_bf16 v[32:35], v[158:161], v[216:219], v[32:35]
	v_mfma_f32_16x16x32_bf16 v[28:31], v[166:169], v[216:219], v[28:31]
	v_mfma_f32_16x16x32_bf16 v[16:19], v[158:161], v[224:227], v[16:19]
	v_mfma_f32_16x16x32_bf16 v[12:15], v[166:169], v[224:227], v[12:15]
	v_mfma_f32_16x16x32_bf16 v[56:59], v[170:173], v[186:189], v[56:59]
	v_mfma_f32_16x16x32_bf16 v[52:55], v[178:181], v[186:189], v[52:55]
	v_mfma_f32_16x16x32_bf16 v[40:43], v[170:173], v[204:207], v[40:43]
	v_mfma_f32_16x16x32_bf16 v[36:39], v[178:181], v[204:207], v[36:39]
	v_mfma_f32_16x16x32_bf16 v[24:27], v[170:173], v[212:215], v[24:27]
	v_mfma_f32_16x16x32_bf16 v[20:23], v[178:181], v[212:215], v[20:23]
	v_mfma_f32_16x16x32_bf16 v[8:11], v[170:173], v[220:223], v[8:11]
	v_mfma_f32_16x16x32_bf16 v[4:7], v[178:181], v[220:223], v[4:7]
	v_mfma_f32_16x16x32_bf16 v[56:59], v[174:177], v[190:193], v[56:59]
	v_mfma_f32_16x16x32_bf16 v[52:55], v[182:185], v[190:193], v[52:55]
	v_mfma_f32_16x16x32_bf16 v[40:43], v[174:177], v[208:211], v[40:43]
	v_mfma_f32_16x16x32_bf16 v[36:39], v[182:185], v[208:211], v[36:39]
	v_mfma_f32_16x16x32_bf16 v[24:27], v[174:177], v[216:219], v[24:27]
	v_mfma_f32_16x16x32_bf16 v[20:23], v[182:185], v[216:219], v[20:23]
	v_mfma_f32_16x16x32_bf16 v[8:11], v[174:177], v[224:227], v[8:11]
	v_mfma_f32_16x16x32_bf16 v[4:7], v[182:185], v[224:227], v[4:7]
	s_setprio 0
	s_barrier
	s_add_i32 s80, s80, 2
	s_add_u32 s42, s42, 0x100
	s_addc_u32 s43, s43, 0
	s_cmp_gt_u32 s80, 13
	s_cbranch_scc0 .LBB0_211
	s_and_b64 vcc, exec, s[22:23]
	s_cbranch_vccz .LBB0_214
	s_barrier

.LBB0_288:
	s_ashr_i32 s41, s40, 31
	s_lshl_b64 s[4:5], s[40:41], 19
	s_add_u32 s42, s6, s4
	s_addc_u32 s43, s7, s5
	s_and_b64 s[4:5], s[22:23], exec
	s_cselect_b32 s41, s43, s37
	s_cselect_b32 s61, s42, s36
	s_ashr_i32 s39, s38, 31
	s_lshl_b64 s[4:5], s[38:39], 19
	s_add_u32 s44, s8, s4
	s_addc_u32 s45, s9, s5
	s_and_b64 s[4:5], s[22:23], exec
	s_cselect_b32 s39, s45, s49
	s_cselect_b32 s62, s44, s48
	s_add_u32 s63, s61, 0x80
	s_addc_u32 s64, s41, 0
	s_add_u32 s4, s36, 0x40080
	s_addc_u32 s5, s37, 0
	s_add_u32 s65, s48, 0x100
	v_lshl_add_u64 v[142:143], s[4:5], 0, v[138:139]
	v_lshl_add_u64 v[144:145], s[4:5], 0, v[140:141]
	s_addc_u32 s68, s49, 0
	s_mov_b32 s69, -2
	s_mov_b64 s[48:49], 0
	s_add_u32 s4, s36, s48
	s_addc_u32 s5, s37, s49
	s_add_u32 s70, s4, 0x100
	s_addc_u32 s71, s5, 0
	s_add_u32 s50, s65, s48
	s_addc_u32 s51, s68, s49
	s_add_u32 s4, s4, 0x180
	s_addc_u32 s5, s5, 0
	s_add_i32 s72, 0, 0x10000
	s_add_i32 s73, 0, 0x14000
	v_add_u32_e32 v160, s72, v146
	s_waitcnt vmcnt(0)
	v_add_u32_e32 v176, s73, v146
	ds_read_b128 v[148:151], v160
	ds_read_b128 v[152:155], v160 offset:1024
	ds_read_b128 v[156:159], v160 offset:2048
	ds_read_b128 v[160:163], v160 offset:3072
	ds_read_b128 v[164:167], v176
	ds_read_b128 v[168:171], v176 offset:1024
	ds_read_b128 v[172:175], v176 offset:2048
	ds_read_b128 v[176:179], v176 offset:3072
	s_cmpk_eq_i32 s48, 0x700
	s_cselect_b32 s13, s64, s5
	s_cselect_b32 s12, s63, s4
	s_cselect_b32 s51, s39, s51
	s_cselect_b32 s50, s62, s50
	s_cselect_b32 s5, s41, s71
	s_cselect_b32 s4, s61, s70
	v_lshl_add_u64 v[196:197], v[142:143], 0, s[48:49]
	s_add_i32 m0, s17, 0xc000
	ds_read_b128 v[180:183], v147
	ds_read_b128 v[184:187], v147 offset:1024
	ds_read_b128 v[188:191], v147 offset:2048
	ds_read_b128 v[192:195], v147 offset:3072
	ds_read_b128 v[204:207], v147 offset:4096
	ds_read_b128 v[208:211], v147 offset:5120
	ds_read_b128 v[212:215], v147 offset:6144
	ds_read_b128 v[216:219], v147 offset:7168
	global_load_lds_dwordx4 v[196:197], off
	v_lshl_add_u64 v[196:197], v[144:145], 0, s[48:49]
	s_add_i32 m0, s17, 0xe000
	s_nop 0
	global_load_lds_dwordx4 v[196:197], off
	s_waitcnt vmcnt(8)
	s_waitcnt lgkmcnt(0)
	s_barrier
	s_setprio 1
	v_mfma_f32_16x16x32_bf16 v[128:131], v[148:151], v[180:183], 0
	v_mfma_f32_16x16x32_bf16 v[124:127], v[156:159], v[180:183], 0
	v_mfma_f32_16x16x32_bf16 v[120:123], v[148:151], v[188:191], 0
	v_mfma_f32_16x16x32_bf16 v[116:119], v[156:159], v[188:191], 0
	v_mfma_f32_16x16x32_bf16 v[104:107], v[148:151], v[204:207], 0
	v_mfma_f32_16x16x32_bf16 v[100:103], v[156:159], v[204:207], 0
	v_mfma_f32_16x16x32_bf16 v[88:91], v[148:151], v[212:215], 0
	v_mfma_f32_16x16x32_bf16 v[84:87], v[156:159], v[212:215], 0
	v_mfma_f32_16x16x32_bf16 v[128:131], v[152:155], v[184:187], v[128:131]
	v_mfma_f32_16x16x32_bf16 v[124:127], v[160:163], v[184:187], v[124:127]
	v_mfma_f32_16x16x32_bf16 v[120:123], v[152:155], v[192:195], v[120:123]
	v_mfma_f32_16x16x32_bf16 v[116:119], v[160:163], v[192:195], v[116:119]
	v_mfma_f32_16x16x32_bf16 v[104:107], v[152:155], v[208:211], v[104:107]
	v_mfma_f32_16x16x32_bf16 v[100:103], v[160:163], v[208:211], v[100:103]
	v_mfma_f32_16x16x32_bf16 v[88:91], v[152:155], v[216:219], v[88:91]
	v_mfma_f32_16x16x32_bf16 v[84:87], v[160:163], v[216:219], v[84:87]
	v_mfma_f32_16x16x32_bf16 v[112:115], v[164:167], v[180:183], 0
	v_mfma_f32_16x16x32_bf16 v[108:111], v[172:175], v[180:183], 0
	v_mfma_f32_16x16x32_bf16 v[96:99], v[164:167], v[188:191], 0
	v_mfma_f32_16x16x32_bf16 v[92:95], v[172:175], v[188:191], 0
	v_mfma_f32_16x16x32_bf16 v[80:83], v[164:167], v[204:207], 0
	v_mfma_f32_16x16x32_bf16 v[76:79], v[172:175], v[204:207], 0
	v_mfma_f32_16x16x32_bf16 v[72:75], v[164:167], v[212:215], 0
	v_mfma_f32_16x16x32_bf16 v[68:71], v[172:175], v[212:215], 0
	v_mfma_f32_16x16x32_bf16 v[112:115], v[168:171], v[184:187], v[112:115]
	v_mfma_f32_16x16x32_bf16 v[108:111], v[176:179], v[184:187], v[108:111]
	v_mfma_f32_16x16x32_bf16 v[96:99], v[168:171], v[192:195], v[96:99]
	v_mfma_f32_16x16x32_bf16 v[92:95], v[176:179], v[192:195], v[92:95]
	v_mfma_f32_16x16x32_bf16 v[80:83], v[168:171], v[208:211], v[80:83]
	v_mfma_f32_16x16x32_bf16 v[76:79], v[176:179], v[208:211], v[76:79]
	v_mfma_f32_16x16x32_bf16 v[72:75], v[168:171], v[216:219], v[72:75]
	v_mfma_f32_16x16x32_bf16 v[68:71], v[176:179], v[216:219], v[68:71]
	s_setprio 0
	s_barrier
	s_add_i32 s70, s72, s16
	v_lshl_add_u64 v[196:197], s[50:51], 0, v[2:3]
	s_mov_b32 m0, s70
	ds_read_b128 v[180:183], v147 offset:16384
	ds_read_b128 v[184:187], v147 offset:17408
	ds_read_b128 v[188:191], v147 offset:18432
	ds_read_b128 v[192:195], v147 offset:19456
	ds_read_b128 v[204:207], v147 offset:20480
	ds_read_b128 v[208:211], v147 offset:21504
	ds_read_b128 v[212:215], v147 offset:22528
	ds_read_b128 v[216:219], v147 offset:23552
	global_load_lds_dwordx4 v[196:197], off
	s_add_i32 m0, s70, 0x2000
	s_add_u32 s70, s50, 0x40000
	v_lshl_add_u64 v[198:199], s[50:51], 0, v[136:137]
	s_addc_u32 s71, s51, 0
	s_add_i32 s72, s73, s16
	global_load_lds_dwordx4 v[198:199], off
	v_lshl_add_u64 v[220:221], s[70:71], 0, v[2:3]
	s_mov_b32 m0, s72
	s_nop 0
	global_load_lds_dwordx4 v[220:221], off
	v_lshl_add_u64 v[220:221], s[70:71], 0, v[136:137]
	s_add_i32 m0, s72, 0x2000
	s_nop 0
	global_load_lds_dwordx4 v[220:221], off
	v_lshl_add_u64 v[220:221], s[4:5], 0, v[132:133]
	s_mov_b32 m0, s17
	s_nop 0
	global_load_lds_dwordx4 v[220:221], off
	v_lshl_add_u64 v[220:221], s[4:5], 0, v[134:135]
	s_mov_b32 m0, s21
	s_nop 0
	global_load_lds_dwordx4 v[220:221], off
	s_waitcnt vmcnt(8)
	s_waitcnt lgkmcnt(0)
	s_barrier
	s_setprio 1
	v_mfma_f32_16x16x32_bf16 v[64:67], v[148:151], v[180:183], 0
	v_mfma_f32_16x16x32_bf16 v[60:63], v[156:159], v[180:183], 0
	v_mfma_f32_16x16x32_bf16 v[56:59], v[148:151], v[188:191], 0
	v_mfma_f32_16x16x32_bf16 v[52:55], v[156:159], v[188:191], 0
	v_mfma_f32_16x16x32_bf16 v[40:43], v[148:151], v[204:207], 0
	v_mfma_f32_16x16x32_bf16 v[36:39], v[156:159], v[204:207], 0
	v_mfma_f32_16x16x32_bf16 v[24:27], v[148:151], v[212:215], 0
	v_mfma_f32_16x16x32_bf16 v[20:23], v[156:159], v[212:215], 0
	v_mfma_f32_16x16x32_bf16 v[64:67], v[152:155], v[184:187], v[64:67]
	v_mfma_f32_16x16x32_bf16 v[60:63], v[160:163], v[184:187], v[60:63]
	v_mfma_f32_16x16x32_bf16 v[56:59], v[152:155], v[192:195], v[56:59]
	v_mfma_f32_16x16x32_bf16 v[52:55], v[160:163], v[192:195], v[52:55]
	v_mfma_f32_16x16x32_bf16 v[40:43], v[152:155], v[208:211], v[40:43]
	v_mfma_f32_16x16x32_bf16 v[36:39], v[160:163], v[208:211], v[36:39]
	v_mfma_f32_16x16x32_bf16 v[24:27], v[152:155], v[216:219], v[24:27]
	v_mfma_f32_16x16x32_bf16 v[20:23], v[160:163], v[216:219], v[20:23]
	v_mfma_f32_16x16x32_bf16 v[48:51], v[164:167], v[180:183], 0
	v_mfma_f32_16x16x32_bf16 v[44:47], v[172:175], v[180:183], 0
	v_mfma_f32_16x16x32_bf16 v[32:35], v[164:167], v[188:191], 0
	v_mfma_f32_16x16x32_bf16 v[28:31], v[172:175], v[188:191], 0
	v_mfma_f32_16x16x32_bf16 v[16:19], v[164:167], v[204:207], 0
	v_mfma_f32_16x16x32_bf16 v[12:15], v[172:175], v[204:207], 0
	v_mfma_f32_16x16x32_bf16 v[8:11], v[164:167], v[212:215], 0
	v_mfma_f32_16x16x32_bf16 v[4:7], v[172:175], v[212:215], 0
	v_mfma_f32_16x16x32_bf16 v[48:51], v[168:171], v[184:187], v[48:51]
	v_mfma_f32_16x16x32_bf16 v[44:47], v[176:179], v[184:187], v[44:47]
	v_mfma_f32_16x16x32_bf16 v[32:35], v[168:171], v[192:195], v[32:35]
	v_mfma_f32_16x16x32_bf16 v[28:31], v[176:179], v[192:195], v[28:31]
	v_mfma_f32_16x16x32_bf16 v[16:19], v[168:171], v[208:211], v[16:19]
	v_mfma_f32_16x16x32_bf16 v[12:15], v[176:179], v[208:211], v[12:15]
	v_mfma_f32_16x16x32_bf16 v[8:11], v[168:171], v[216:219], v[8:11]
	v_mfma_f32_16x16x32_bf16 v[4:7], v[176:179], v[216:219], v[4:7]
	s_setprio 0
	s_barrier
	s_add_i32 s70, 0, 0x18000
	s_add_i32 s71, 0, 0x1c000
	v_add_u32_e32 v160, s70, v146
	v_add_u32_e32 v176, s71, v146
	ds_read_b128 v[148:151], v160
	ds_read_b128 v[152:155], v160 offset:1024
	ds_read_b128 v[156:159], v160 offset:2048
	ds_read_b128 v[160:163], v160 offset:3072
	ds_read_b128 v[164:167], v176
	ds_read_b128 v[168:171], v176 offset:1024
	ds_read_b128 v[172:175], v176 offset:2048
	ds_read_b128 v[176:179], v176 offset:3072
	s_add_u32 s4, s4, 0x40000
	s_addc_u32 s5, s5, 0
	s_mov_b32 m0, s46
	v_lshl_add_u64 v[220:221], s[4:5], 0, v[132:133]
	ds_read_b128 v[180:183], v147 offset:32768
	ds_read_b128 v[184:187], v147 offset:33792
	ds_read_b128 v[188:191], v147 offset:34816
	ds_read_b128 v[192:195], v147 offset:35840
	ds_read_b128 v[204:207], v147 offset:36864
	ds_read_b128 v[208:211], v147 offset:37888
	ds_read_b128 v[212:215], v147 offset:38912
	ds_read_b128 v[216:219], v147 offset:39936
	global_load_lds_dwordx4 v[220:221], off
	v_lshl_add_u64 v[220:221], s[4:5], 0, v[134:135]
	s_mov_b32 m0, s47
	s_nop 0
	global_load_lds_dwordx4 v[220:221], off
	s_waitcnt vmcnt(8)
	s_waitcnt lgkmcnt(0)
	s_barrier
	s_setprio 1
	v_mfma_f32_16x16x32_bf16 v[128:131], v[148:151], v[180:183], v[128:131]
	v_mfma_f32_16x16x32_bf16 v[124:127], v[156:159], v[180:183], v[124:127]
	v_mfma_f32_16x16x32_bf16 v[120:123], v[148:151], v[188:191], v[120:123]
	v_mfma_f32_16x16x32_bf16 v[116:119], v[156:159], v[188:191], v[116:119]
	v_mfma_f32_16x16x32_bf16 v[104:107], v[148:151], v[204:207], v[104:107]
	v_mfma_f32_16x16x32_bf16 v[100:103], v[156:159], v[204:207], v[100:103]
	v_mfma_f32_16x16x32_bf16 v[88:91], v[148:151], v[212:215], v[88:91]
	v_mfma_f32_16x16x32_bf16 v[84:87], v[156:159], v[212:215], v[84:87]
	v_mfma_f32_16x16x32_bf16 v[128:131], v[152:155], v[184:187], v[128:131]
	v_mfma_f32_16x16x32_bf16 v[124:127], v[160:163], v[184:187], v[124:127]
	v_mfma_f32_16x16x32_bf16 v[120:123], v[152:155], v[192:195], v[120:123]
	v_mfma_f32_16x16x32_bf16 v[116:119], v[160:163], v[192:195], v[116:119]
	v_mfma_f32_16x16x32_bf16 v[104:107], v[152:155], v[208:211], v[104:107]
	v_mfma_f32_16x16x32_bf16 v[100:103], v[160:163], v[208:211], v[100:103]
	v_mfma_f32_16x16x32_bf16 v[88:91], v[152:155], v[216:219], v[88:91]
	v_mfma_f32_16x16x32_bf16 v[84:87], v[160:163], v[216:219], v[84:87]
	v_mfma_f32_16x16x32_bf16 v[112:115], v[164:167], v[180:183], v[112:115]
	v_mfma_f32_16x16x32_bf16 v[108:111], v[172:175], v[180:183], v[108:111]
	v_mfma_f32_16x16x32_bf16 v[96:99], v[164:167], v[188:191], v[96:99]
	v_mfma_f32_16x16x32_bf16 v[92:95], v[172:175], v[188:191], v[92:95]
	v_mfma_f32_16x16x32_bf16 v[80:83], v[164:167], v[204:207], v[80:83]
	v_mfma_f32_16x16x32_bf16 v[76:79], v[172:175], v[204:207], v[76:79]
	v_mfma_f32_16x16x32_bf16 v[72:75], v[164:167], v[212:215], v[72:75]
	v_mfma_f32_16x16x32_bf16 v[68:71], v[172:175], v[212:215], v[68:71]
	v_mfma_f32_16x16x32_bf16 v[112:115], v[168:171], v[184:187], v[112:115]
	v_mfma_f32_16x16x32_bf16 v[108:111], v[176:179], v[184:187], v[108:111]
	v_mfma_f32_16x16x32_bf16 v[96:99], v[168:171], v[192:195], v[96:99]
	v_mfma_f32_16x16x32_bf16 v[92:95], v[176:179], v[192:195], v[92:95]
	v_mfma_f32_16x16x32_bf16 v[80:83], v[168:171], v[208:211], v[80:83]
	v_mfma_f32_16x16x32_bf16 v[76:79], v[176:179], v[208:211], v[76:79]
	v_mfma_f32_16x16x32_bf16 v[72:75], v[168:171], v[216:219], v[72:75]
	v_mfma_f32_16x16x32_bf16 v[68:71], v[176:179], v[216:219], v[68:71]
	s_setprio 0
	s_barrier
	s_add_i32 s4, s70, s16
	v_lshl_add_u64 v[196:197], v[196:197], 0, s[34:35]
	s_mov_b32 m0, s4
	ds_read_b128 v[180:183], v147 offset:49152
	ds_read_b128 v[184:187], v147 offset:50176
	ds_read_b128 v[188:191], v147 offset:51200
	ds_read_b128 v[192:195], v147 offset:52224
	ds_read_b128 v[204:207], v147 offset:53248
	ds_read_b128 v[208:211], v147 offset:54272
	ds_read_b128 v[212:215], v147 offset:55296
	ds_read_b128 v[216:219], v147 offset:56320
	global_load_lds_dwordx4 v[196:197], off
	s_add_i32 m0, s4, 0x2000
	s_add_u32 s4, s50, 0x40080
	v_lshl_add_u64 v[196:197], v[198:199], 0, s[34:35]
	s_addc_u32 s5, s51, 0
	s_add_i32 s50, s71, s16
	global_load_lds_dwordx4 v[196:197], off
	v_lshl_add_u64 v[196:197], s[4:5], 0, v[2:3]
	s_mov_b32 m0, s50
	s_nop 0
	global_load_lds_dwordx4 v[196:197], off
	v_lshl_add_u64 v[196:197], s[4:5], 0, v[136:137]
	s_add_i32 m0, s50, 0x2000
	s_nop 0
	global_load_lds_dwordx4 v[196:197], off
	v_lshl_add_u64 v[196:197], s[12:13], 0, v[132:133]
	s_mov_b32 m0, s56
	s_nop 0
	global_load_lds_dwordx4 v[196:197], off
	v_lshl_add_u64 v[196:197], s[12:13], 0, v[134:135]
	s_mov_b32 m0, s58
	s_nop 0
	global_load_lds_dwordx4 v[196:197], off
	s_waitcnt vmcnt(8)
	s_waitcnt lgkmcnt(0)
	s_barrier
	s_setprio 1
	v_mfma_f32_16x16x32_bf16 v[64:67], v[148:151], v[180:183], v[64:67]
	v_mfma_f32_16x16x32_bf16 v[60:63], v[156:159], v[180:183], v[60:63]
	v_mfma_f32_16x16x32_bf16 v[56:59], v[148:151], v[188:191], v[56:59]
	v_mfma_f32_16x16x32_bf16 v[52:55], v[156:159], v[188:191], v[52:55]
	v_mfma_f32_16x16x32_bf16 v[40:43], v[148:151], v[204:207], v[40:43]
	v_mfma_f32_16x16x32_bf16 v[36:39], v[156:159], v[204:207], v[36:39]
	v_mfma_f32_16x16x32_bf16 v[24:27], v[148:151], v[212:215], v[24:27]
	v_mfma_f32_16x16x32_bf16 v[20:23], v[156:159], v[212:215], v[20:23]
	v_mfma_f32_16x16x32_bf16 v[64:67], v[152:155], v[184:187], v[64:67]
	v_mfma_f32_16x16x32_bf16 v[60:63], v[160:163], v[184:187], v[60:63]
	v_mfma_f32_16x16x32_bf16 v[56:59], v[152:155], v[192:195], v[56:59]
	v_mfma_f32_16x16x32_bf16 v[52:55], v[160:163], v[192:195], v[52:55]
	v_mfma_f32_16x16x32_bf16 v[40:43], v[152:155], v[208:211], v[40:43]
	v_mfma_f32_16x16x32_bf16 v[36:39], v[160:163], v[208:211], v[36:39]
	v_mfma_f32_16x16x32_bf16 v[24:27], v[152:155], v[216:219], v[24:27]
	v_mfma_f32_16x16x32_bf16 v[20:23], v[160:163], v[216:219], v[20:23]
	v_mfma_f32_16x16x32_bf16 v[48:51], v[164:167], v[180:183], v[48:51]
	v_mfma_f32_16x16x32_bf16 v[44:47], v[172:175], v[180:183], v[44:47]
	v_mfma_f32_16x16x32_bf16 v[32:35], v[164:167], v[188:191], v[32:35]
	v_mfma_f32_16x16x32_bf16 v[28:31], v[172:175], v[188:191], v[28:31]
	v_mfma_f32_16x16x32_bf16 v[16:19], v[164:167], v[204:207], v[16:19]
	v_mfma_f32_16x16x32_bf16 v[12:15], v[172:175], v[204:207], v[12:15]
	v_mfma_f32_16x16x32_bf16 v[8:11], v[164:167], v[212:215], v[8:11]
	v_mfma_f32_16x16x32_bf16 v[4:7], v[172:175], v[212:215], v[4:7]
	v_mfma_f32_16x16x32_bf16 v[48:51], v[168:171], v[184:187], v[48:51]
	v_mfma_f32_16x16x32_bf16 v[44:47], v[176:179], v[184:187], v[44:47]
	v_mfma_f32_16x16x32_bf16 v[32:35], v[168:171], v[192:195], v[32:35]
	v_mfma_f32_16x16x32_bf16 v[28:31], v[176:179], v[192:195], v[28:31]
	v_mfma_f32_16x16x32_bf16 v[16:19], v[168:171], v[208:211], v[16:19]
	v_mfma_f32_16x16x32_bf16 v[12:15], v[176:179], v[208:211], v[12:15]
	v_mfma_f32_16x16x32_bf16 v[8:11], v[168:171], v[216:219], v[8:11]
	v_mfma_f32_16x16x32_bf16 v[4:7], v[176:179], v[216:219], v[4:7]
	s_setprio 0
	s_barrier
	s_add_i32 s69, s69, 2
	s_add_u32 s48, s48, 0x100
	s_addc_u32 s49, s49, 0
	s_cmp_gt_u32 s69, 13
.LBB0_289:
	s_add_u32 s4, s36, s48
	s_addc_u32 s5, s37, s49
	s_add_u32 s70, s4, 0x100
	s_addc_u32 s71, s5, 0
	s_add_u32 s50, s65, s48
	s_addc_u32 s51, s68, s49
	s_add_u32 s4, s4, 0x180
	s_addc_u32 s5, s5, 0
	s_add_i32 s72, 0, 0x10000
	s_add_i32 s73, 0, 0x14000
	v_add_u32_e32 v160, s72, v146
	s_waitcnt vmcnt(0)
	v_add_u32_e32 v176, s73, v146
	ds_read_b128 v[148:151], v160
	ds_read_b128 v[152:155], v160 offset:1024
	ds_read_b128 v[156:159], v160 offset:2048
	ds_read_b128 v[160:163], v160 offset:3072
	ds_read_b128 v[164:167], v176
	ds_read_b128 v[168:171], v176 offset:1024
	ds_read_b128 v[172:175], v176 offset:2048
	ds_read_b128 v[176:179], v176 offset:3072
	s_cmpk_eq_i32 s48, 0x700
	s_cselect_b32 s13, s64, s5
	s_cselect_b32 s12, s63, s4
	s_cselect_b32 s51, s39, s51
	s_cselect_b32 s50, s62, s50
	s_cselect_b32 s5, s41, s71
	s_cselect_b32 s4, s61, s70
	v_lshl_add_u64 v[196:197], v[142:143], 0, s[48:49]
	s_add_i32 m0, s17, 0xc000
	ds_read_b128 v[180:183], v147
	ds_read_b128 v[184:187], v147 offset:1024
	ds_read_b128 v[188:191], v147 offset:2048
	ds_read_b128 v[192:195], v147 offset:3072
	ds_read_b128 v[204:207], v147 offset:4096
	ds_read_b128 v[208:211], v147 offset:5120
	ds_read_b128 v[212:215], v147 offset:6144
	ds_read_b128 v[216:219], v147 offset:7168
	global_load_lds_dwordx4 v[196:197], off
	v_lshl_add_u64 v[196:197], v[144:145], 0, s[48:49]
	s_add_i32 m0, s17, 0xe000
	s_nop 0
	global_load_lds_dwordx4 v[196:197], off
	s_waitcnt vmcnt(8)
	s_waitcnt lgkmcnt(0)
	s_barrier
	s_setprio 1
	v_mfma_f32_16x16x32_bf16 v[128:131], v[148:151], v[180:183], v[128:131]
	v_mfma_f32_16x16x32_bf16 v[124:127], v[156:159], v[180:183], v[124:127]
	v_mfma_f32_16x16x32_bf16 v[120:123], v[148:151], v[188:191], v[120:123]
	v_mfma_f32_16x16x32_bf16 v[116:119], v[156:159], v[188:191], v[116:119]
	v_mfma_f32_16x16x32_bf16 v[104:107], v[148:151], v[204:207], v[104:107]
	v_mfma_f32_16x16x32_bf16 v[100:103], v[156:159], v[204:207], v[100:103]
	v_mfma_f32_16x16x32_bf16 v[88:91], v[148:151], v[212:215], v[88:91]
	v_mfma_f32_16x16x32_bf16 v[84:87], v[156:159], v[212:215], v[84:87]
	v_mfma_f32_16x16x32_bf16 v[128:131], v[152:155], v[184:187], v[128:131]
	v_mfma_f32_16x16x32_bf16 v[124:127], v[160:163], v[184:187], v[124:127]
	v_mfma_f32_16x16x32_bf16 v[120:123], v[152:155], v[192:195], v[120:123]
	v_mfma_f32_16x16x32_bf16 v[116:119], v[160:163], v[192:195], v[116:119]
	v_mfma_f32_16x16x32_bf16 v[104:107], v[152:155], v[208:211], v[104:107]
	v_mfma_f32_16x16x32_bf16 v[100:103], v[160:163], v[208:211], v[100:103]
	v_mfma_f32_16x16x32_bf16 v[88:91], v[152:155], v[216:219], v[88:91]
	v_mfma_f32_16x16x32_bf16 v[84:87], v[160:163], v[216:219], v[84:87]
	v_mfma_f32_16x16x32_bf16 v[112:115], v[164:167], v[180:183], v[112:115]
	v_mfma_f32_16x16x32_bf16 v[108:111], v[172:175], v[180:183], v[108:111]
	v_mfma_f32_16x16x32_bf16 v[96:99], v[164:167], v[188:191], v[96:99]
	v_mfma_f32_16x16x32_bf16 v[92:95], v[172:175], v[188:191], v[92:95]
	v_mfma_f32_16x16x32_bf16 v[80:83], v[164:167], v[204:207], v[80:83]
	v_mfma_f32_16x16x32_bf16 v[76:79], v[172:175], v[204:207], v[76:79]
	v_mfma_f32_16x16x32_bf16 v[72:75], v[164:167], v[212:215], v[72:75]
	v_mfma_f32_16x16x32_bf16 v[68:71], v[172:175], v[212:215], v[68:71]
	v_mfma_f32_16x16x32_bf16 v[112:115], v[168:171], v[184:187], v[112:115]
	v_mfma_f32_16x16x32_bf16 v[108:111], v[176:179], v[184:187], v[108:111]
	v_mfma_f32_16x16x32_bf16 v[96:99], v[168:171], v[192:195], v[96:99]
	v_mfma_f32_16x16x32_bf16 v[92:95], v[176:179], v[192:195], v[92:95]
	v_mfma_f32_16x16x32_bf16 v[80:83], v[168:171], v[208:211], v[80:83]
	v_mfma_f32_16x16x32_bf16 v[76:79], v[176:179], v[208:211], v[76:79]
	v_mfma_f32_16x16x32_bf16 v[72:75], v[168:171], v[216:219], v[72:75]
	v_mfma_f32_16x16x32_bf16 v[68:71], v[176:179], v[216:219], v[68:71]
	s_setprio 0
	s_barrier
	s_add_i32 s70, s72, s16
	v_lshl_add_u64 v[196:197], s[50:51], 0, v[2:3]
	s_mov_b32 m0, s70
	ds_read_b128 v[180:183], v147 offset:16384
	ds_read_b128 v[184:187], v147 offset:17408
	ds_read_b128 v[188:191], v147 offset:18432
	ds_read_b128 v[192:195], v147 offset:19456
	ds_read_b128 v[204:207], v147 offset:20480
	ds_read_b128 v[208:211], v147 offset:21504
	ds_read_b128 v[212:215], v147 offset:22528
	ds_read_b128 v[216:219], v147 offset:23552
	global_load_lds_dwordx4 v[196:197], off
	s_add_i32 m0, s70, 0x2000
	s_add_u32 s70, s50, 0x40000
	v_lshl_add_u64 v[198:199], s[50:51], 0, v[136:137]
	s_addc_u32 s71, s51, 0
	s_add_i32 s72, s73, s16
	global_load_lds_dwordx4 v[198:199], off
	v_lshl_add_u64 v[220:221], s[70:71], 0, v[2:3]
	s_mov_b32 m0, s72
	s_nop 0
	global_load_lds_dwordx4 v[220:221], off
	v_lshl_add_u64 v[220:221], s[70:71], 0, v[136:137]
	s_add_i32 m0, s72, 0x2000
	s_nop 0
	global_load_lds_dwordx4 v[220:221], off
	v_lshl_add_u64 v[220:221], s[4:5], 0, v[132:133]
	s_mov_b32 m0, s17
	s_nop 0
	global_load_lds_dwordx4 v[220:221], off
	v_lshl_add_u64 v[220:221], s[4:5], 0, v[134:135]
	s_mov_b32 m0, s21
	s_nop 0
	global_load_lds_dwordx4 v[220:221], off
	s_waitcnt vmcnt(8)
	s_waitcnt lgkmcnt(0)
	s_barrier
	s_setprio 1
	v_mfma_f32_16x16x32_bf16 v[64:67], v[148:151], v[180:183], v[64:67]
	v_mfma_f32_16x16x32_bf16 v[60:63], v[156:159], v[180:183], v[60:63]
	v_mfma_f32_16x16x32_bf16 v[56:59], v[148:151], v[188:191], v[56:59]
	v_mfma_f32_16x16x32_bf16 v[52:55], v[156:159], v[188:191], v[52:55]
	v_mfma_f32_16x16x32_bf16 v[40:43], v[148:151], v[204:207], v[40:43]
	v_mfma_f32_16x16x32_bf16 v[36:39], v[156:159], v[204:207], v[36:39]
	v_mfma_f32_16x16x32_bf16 v[24:27], v[148:151], v[212:215], v[24:27]
	v_mfma_f32_16x16x32_bf16 v[20:23], v[156:159], v[212:215], v[20:23]
	v_mfma_f32_16x16x32_bf16 v[64:67], v[152:155], v[184:187], v[64:67]
	v_mfma_f32_16x16x32_bf16 v[60:63], v[160:163], v[184:187], v[60:63]
	v_mfma_f32_16x16x32_bf16 v[56:59], v[152:155], v[192:195], v[56:59]
	v_mfma_f32_16x16x32_bf16 v[52:55], v[160:163], v[192:195], v[52:55]
	v_mfma_f32_16x16x32_bf16 v[40:43], v[152:155], v[208:211], v[40:43]
	v_mfma_f32_16x16x32_bf16 v[36:39], v[160:163], v[208:211], v[36:39]
	v_mfma_f32_16x16x32_bf16 v[24:27], v[152:155], v[216:219], v[24:27]
	v_mfma_f32_16x16x32_bf16 v[20:23], v[160:163], v[216:219], v[20:23]
	v_mfma_f32_16x16x32_bf16 v[48:51], v[164:167], v[180:183], v[48:51]
	v_mfma_f32_16x16x32_bf16 v[44:47], v[172:175], v[180:183], v[44:47]
	v_mfma_f32_16x16x32_bf16 v[32:35], v[164:167], v[188:191], v[32:35]
	v_mfma_f32_16x16x32_bf16 v[28:31], v[172:175], v[188:191], v[28:31]
	v_mfma_f32_16x16x32_bf16 v[16:19], v[164:167], v[204:207], v[16:19]
	v_mfma_f32_16x16x32_bf16 v[12:15], v[172:175], v[204:207], v[12:15]
	v_mfma_f32_16x16x32_bf16 v[8:11], v[164:167], v[212:215], v[8:11]
	v_mfma_f32_16x16x32_bf16 v[4:7], v[172:175], v[212:215], v[4:7]
	v_mfma_f32_16x16x32_bf16 v[48:51], v[168:171], v[184:187], v[48:51]
	v_mfma_f32_16x16x32_bf16 v[44:47], v[176:179], v[184:187], v[44:47]
	v_mfma_f32_16x16x32_bf16 v[32:35], v[168:171], v[192:195], v[32:35]
	v_mfma_f32_16x16x32_bf16 v[28:31], v[176:179], v[192:195], v[28:31]
	v_mfma_f32_16x16x32_bf16 v[16:19], v[168:171], v[208:211], v[16:19]
	v_mfma_f32_16x16x32_bf16 v[12:15], v[176:179], v[208:211], v[12:15]
	v_mfma_f32_16x16x32_bf16 v[8:11], v[168:171], v[216:219], v[8:11]
	v_mfma_f32_16x16x32_bf16 v[4:7], v[176:179], v[216:219], v[4:7]
	s_setprio 0
	s_barrier
	s_add_i32 s70, 0, 0x18000
	s_add_i32 s71, 0, 0x1c000
	v_add_u32_e32 v160, s70, v146
	v_add_u32_e32 v176, s71, v146
	ds_read_b128 v[148:151], v160
	ds_read_b128 v[152:155], v160 offset:1024
	ds_read_b128 v[156:159], v160 offset:2048
	ds_read_b128 v[160:163], v160 offset:3072
	ds_read_b128 v[164:167], v176
	ds_read_b128 v[168:171], v176 offset:1024
	ds_read_b128 v[172:175], v176 offset:2048
	ds_read_b128 v[176:179], v176 offset:3072
	s_add_u32 s4, s4, 0x40000
	s_addc_u32 s5, s5, 0
	s_mov_b32 m0, s46
	v_lshl_add_u64 v[220:221], s[4:5], 0, v[132:133]
	ds_read_b128 v[180:183], v147 offset:32768
	ds_read_b128 v[184:187], v147 offset:33792
	ds_read_b128 v[188:191], v147 offset:34816
	ds_read_b128 v[192:195], v147 offset:35840
	ds_read_b128 v[204:207], v147 offset:36864
	ds_read_b128 v[208:211], v147 offset:37888
	ds_read_b128 v[212:215], v147 offset:38912
	ds_read_b128 v[216:219], v147 offset:39936
	global_load_lds_dwordx4 v[220:221], off
	v_lshl_add_u64 v[220:221], s[4:5], 0, v[134:135]
	s_mov_b32 m0, s47
	s_nop 0
	global_load_lds_dwordx4 v[220:221], off
	s_waitcnt vmcnt(8)
	s_waitcnt lgkmcnt(0)
	s_barrier
	s_setprio 1
	v_mfma_f32_16x16x32_bf16 v[128:131], v[148:151], v[180:183], v[128:131]
	v_mfma_f32_16x16x32_bf16 v[124:127], v[156:159], v[180:183], v[124:127]
	v_mfma_f32_16x16x32_bf16 v[120:123], v[148:151], v[188:191], v[120:123]
	v_mfma_f32_16x16x32_bf16 v[116:119], v[156:159], v[188:191], v[116:119]
	v_mfma_f32_16x16x32_bf16 v[104:107], v[148:151], v[204:207], v[104:107]
	v_mfma_f32_16x16x32_bf16 v[100:103], v[156:159], v[204:207], v[100:103]
	v_mfma_f32_16x16x32_bf16 v[88:91], v[148:151], v[212:215], v[88:91]
	v_mfma_f32_16x16x32_bf16 v[84:87], v[156:159], v[212:215], v[84:87]
	v_mfma_f32_16x16x32_bf16 v[128:131], v[152:155], v[184:187], v[128:131]
	v_mfma_f32_16x16x32_bf16 v[124:127], v[160:163], v[184:187], v[124:127]
	v_mfma_f32_16x16x32_bf16 v[120:123], v[152:155], v[192:195], v[120:123]
	v_mfma_f32_16x16x32_bf16 v[116:119], v[160:163], v[192:195], v[116:119]
	v_mfma_f32_16x16x32_bf16 v[104:107], v[152:155], v[208:211], v[104:107]
	v_mfma_f32_16x16x32_bf16 v[100:103], v[160:163], v[208:211], v[100:103]
	v_mfma_f32_16x16x32_bf16 v[88:91], v[152:155], v[216:219], v[88:91]
	v_mfma_f32_16x16x32_bf16 v[84:87], v[160:163], v[216:219], v[84:87]
	v_mfma_f32_16x16x32_bf16 v[112:115], v[164:167], v[180:183], v[112:115]
	v_mfma_f32_16x16x32_bf16 v[108:111], v[172:175], v[180:183], v[108:111]
	v_mfma_f32_16x16x32_bf16 v[96:99], v[164:167], v[188:191], v[96:99]
	v_mfma_f32_16x16x32_bf16 v[92:95], v[172:175], v[188:191], v[92:95]
	v_mfma_f32_16x16x32_bf16 v[80:83], v[164:167], v[204:207], v[80:83]
	v_mfma_f32_16x16x32_bf16 v[76:79], v[172:175], v[204:207], v[76:79]
	v_mfma_f32_16x16x32_bf16 v[72:75], v[164:167], v[212:215], v[72:75]
	v_mfma_f32_16x16x32_bf16 v[68:71], v[172:175], v[212:215], v[68:71]
	v_mfma_f32_16x16x32_bf16 v[112:115], v[168:171], v[184:187], v[112:115]
	v_mfma_f32_16x16x32_bf16 v[108:111], v[176:179], v[184:187], v[108:111]
	v_mfma_f32_16x16x32_bf16 v[96:99], v[168:171], v[192:195], v[96:99]
	v_mfma_f32_16x16x32_bf16 v[92:95], v[176:179], v[192:195], v[92:95]
	v_mfma_f32_16x16x32_bf16 v[80:83], v[168:171], v[208:211], v[80:83]
	v_mfma_f32_16x16x32_bf16 v[76:79], v[176:179], v[208:211], v[76:79]
	v_mfma_f32_16x16x32_bf16 v[72:75], v[168:171], v[216:219], v[72:75]
	v_mfma_f32_16x16x32_bf16 v[68:71], v[176:179], v[216:219], v[68:71]
	s_setprio 0
	s_barrier
	s_add_i32 s4, s70, s16
	v_lshl_add_u64 v[196:197], v[196:197], 0, s[34:35]
	s_mov_b32 m0, s4
	ds_read_b128 v[180:183], v147 offset:49152
	ds_read_b128 v[184:187], v147 offset:50176
	ds_read_b128 v[188:191], v147 offset:51200
	ds_read_b128 v[192:195], v147 offset:52224
	ds_read_b128 v[204:207], v147 offset:53248
	ds_read_b128 v[208:211], v147 offset:54272
	ds_read_b128 v[212:215], v147 offset:55296
	ds_read_b128 v[216:219], v147 offset:56320
	global_load_lds_dwordx4 v[196:197], off
	s_add_i32 m0, s4, 0x2000
	s_add_u32 s4, s50, 0x40080
	v_lshl_add_u64 v[196:197], v[198:199], 0, s[34:35]
	s_addc_u32 s5, s51, 0
	s_add_i32 s50, s71, s16
	global_load_lds_dwordx4 v[196:197], off
	v_lshl_add_u64 v[196:197], s[4:5], 0, v[2:3]
	s_mov_b32 m0, s50
	s_nop 0
	global_load_lds_dwordx4 v[196:197], off
	v_lshl_add_u64 v[196:197], s[4:5], 0, v[136:137]
	s_add_i32 m0, s50, 0x2000
	s_nop 0
	global_load_lds_dwordx4 v[196:197], off
	v_lshl_add_u64 v[196:197], s[12:13], 0, v[132:133]
	s_mov_b32 m0, s56
	s_nop 0
	global_load_lds_dwordx4 v[196:197], off
	v_lshl_add_u64 v[196:197], s[12:13], 0, v[134:135]
	s_mov_b32 m0, s58
	s_nop 0
	global_load_lds_dwordx4 v[196:197], off
	s_waitcnt vmcnt(8)
	s_waitcnt lgkmcnt(0)
	s_barrier
	s_setprio 1
	v_mfma_f32_16x16x32_bf16 v[64:67], v[148:151], v[180:183], v[64:67]
	v_mfma_f32_16x16x32_bf16 v[60:63], v[156:159], v[180:183], v[60:63]
	v_mfma_f32_16x16x32_bf16 v[56:59], v[148:151], v[188:191], v[56:59]
	v_mfma_f32_16x16x32_bf16 v[52:55], v[156:159], v[188:191], v[52:55]
	v_mfma_f32_16x16x32_bf16 v[40:43], v[148:151], v[204:207], v[40:43]
	v_mfma_f32_16x16x32_bf16 v[36:39], v[156:159], v[204:207], v[36:39]
	v_mfma_f32_16x16x32_bf16 v[24:27], v[148:151], v[212:215], v[24:27]
	v_mfma_f32_16x16x32_bf16 v[20:23], v[156:159], v[212:215], v[20:23]
	v_mfma_f32_16x16x32_bf16 v[64:67], v[152:155], v[184:187], v[64:67]
	v_mfma_f32_16x16x32_bf16 v[60:63], v[160:163], v[184:187], v[60:63]
	v_mfma_f32_16x16x32_bf16 v[56:59], v[152:155], v[192:195], v[56:59]
	v_mfma_f32_16x16x32_bf16 v[52:55], v[160:163], v[192:195], v[52:55]
	v_mfma_f32_16x16x32_bf16 v[40:43], v[152:155], v[208:211], v[40:43]
	v_mfma_f32_16x16x32_bf16 v[36:39], v[160:163], v[208:211], v[36:39]
	v_mfma_f32_16x16x32_bf16 v[24:27], v[152:155], v[216:219], v[24:27]
	v_mfma_f32_16x16x32_bf16 v[20:23], v[160:163], v[216:219], v[20:23]
	v_mfma_f32_16x16x32_bf16 v[48:51], v[164:167], v[180:183], v[48:51]
	v_mfma_f32_16x16x32_bf16 v[44:47], v[172:175], v[180:183], v[44:47]
	v_mfma_f32_16x16x32_bf16 v[32:35], v[164:167], v[188:191], v[32:35]
	v_mfma_f32_16x16x32_bf16 v[28:31], v[172:175], v[188:191], v[28:31]
	v_mfma_f32_16x16x32_bf16 v[16:19], v[164:167], v[204:207], v[16:19]
	v_mfma_f32_16x16x32_bf16 v[12:15], v[172:175], v[204:207], v[12:15]
	v_mfma_f32_16x16x32_bf16 v[8:11], v[164:167], v[212:215], v[8:11]
	v_mfma_f32_16x16x32_bf16 v[4:7], v[172:175], v[212:215], v[4:7]
	v_mfma_f32_16x16x32_bf16 v[48:51], v[168:171], v[184:187], v[48:51]
	v_mfma_f32_16x16x32_bf16 v[44:47], v[176:179], v[184:187], v[44:47]
	v_mfma_f32_16x16x32_bf16 v[32:35], v[168:171], v[192:195], v[32:35]
	v_mfma_f32_16x16x32_bf16 v[28:31], v[176:179], v[192:195], v[28:31]
	v_mfma_f32_16x16x32_bf16 v[16:19], v[168:171], v[208:211], v[16:19]
	v_mfma_f32_16x16x32_bf16 v[12:15], v[176:179], v[208:211], v[12:15]
	v_mfma_f32_16x16x32_bf16 v[8:11], v[168:171], v[216:219], v[8:11]
	v_mfma_f32_16x16x32_bf16 v[4:7], v[176:179], v[216:219], v[4:7]
	s_setprio 0
	s_barrier
	s_add_i32 s69, s69, 2
	s_add_u32 s48, s48, 0x100
	s_addc_u32 s49, s49, 0
	s_cmp_gt_u32 s69, 13
	s_cbranch_scc0 .LBB0_289
	s_and_b64 vcc, exec, s[18:19]
	s_mov_b32 s62, 0x18000
	s_mov_b32 s63, 0x1a000
	s_cbranch_vccz .LBB0_292
	s_barrier

.LBB0_310:
	s_ashr_i32 s41, s40, 31
	s_lshl_b64 s[4:5], s[40:41], 19
	s_add_u32 s42, s6, s4
	s_addc_u32 s43, s7, s5
	s_and_b64 s[4:5], s[22:23], exec
	s_cselect_b32 s41, s43, s39
	s_cselect_b32 s60, s42, s38
	s_ashr_i32 s37, s36, 31
	s_lshl_b64 s[4:5], s[36:37], 19
	s_add_u32 s44, s8, s4
	s_addc_u32 s45, s9, s5
	s_and_b64 s[4:5], s[22:23], exec
	s_cselect_b32 s37, s45, s49
	s_cselect_b32 s61, s44, s48
	s_add_u32 s62, s60, 0x80
	s_addc_u32 s63, s41, 0
	s_add_u32 s4, s38, 0x40080
	s_addc_u32 s5, s39, 0
	s_add_u32 s64, s48, 0x100
	v_lshl_add_u64 v[144:145], s[4:5], 0, v[140:141]
	v_lshl_add_u64 v[146:147], s[4:5], 0, v[142:143]
	s_addc_u32 s65, s49, 0
	s_mov_b32 s68, -2
	s_mov_b64 s[48:49], 0
	s_add_u32 s4, s38, s48
	s_addc_u32 s5, s39, s49
	s_add_u32 s69, s4, 0x100
	s_addc_u32 s70, s5, 0
	s_add_u32 s50, s64, s48
	s_addc_u32 s51, s65, s49
	s_add_u32 s4, s4, 0x180
	s_addc_u32 s5, s5, 0
	s_add_i32 s71, 0, 0x10000
	s_add_i32 s72, 0, 0x14000
	v_add_u32_e32 v2, s71, v149
	ds_read_b128 v[152:155], v2
	s_waitcnt vmcnt(0)
	ds_read_b128 v[156:159], v2 offset:1024
	ds_read_b128 v[160:163], v2 offset:2048
	ds_read_b128 v[164:167], v2 offset:3072
	v_add_u32_e32 v2, s72, v149
	ds_read_b128 v[168:171], v2
	ds_read_b128 v[172:175], v2 offset:1024
	ds_read_b128 v[176:179], v2 offset:2048
	ds_read_b128 v[180:183], v2 offset:3072
	s_cmpk_eq_i32 s48, 0x700
	s_cselect_b32 s13, s63, s5
	s_cselect_b32 s12, s62, s4
	s_cselect_b32 s51, s37, s51
	s_cselect_b32 s50, s61, s50
	s_cselect_b32 s5, s41, s70
	s_cselect_b32 s4, s60, s69
	v_lshl_add_u64 v[196:197], v[144:145], 0, s[48:49]
	s_add_i32 m0, s17, 0xc000
	ds_read_b128 v[184:187], v151
	ds_read_b128 v[188:191], v151 offset:1024
	ds_read_b128 v[192:195], v151 offset:2048
	ds_read_b128 v[204:207], v151 offset:3072
	ds_read_b128 v[208:211], v151 offset:4096
	ds_read_b128 v[212:215], v151 offset:5120
	ds_read_b128 v[216:219], v151 offset:6144
	ds_read_b128 v[220:223], v151 offset:7168
	global_load_lds_dwordx4 v[196:197], off
	v_lshl_add_u64 v[196:197], v[146:147], 0, s[48:49]
	s_add_i32 m0, s17, 0xe000
	s_nop 0
	global_load_lds_dwordx4 v[196:197], off
	s_waitcnt vmcnt(8)
	s_waitcnt lgkmcnt(0)
	s_barrier
	s_setprio 1
	v_mfma_f32_16x16x32_bf16 v[128:131], v[152:155], v[184:187], 0
	v_mfma_f32_16x16x32_bf16 v[124:127], v[160:163], v[184:187], 0
	v_mfma_f32_16x16x32_bf16 v[120:123], v[152:155], v[192:195], 0
	v_mfma_f32_16x16x32_bf16 v[116:119], v[160:163], v[192:195], 0
	v_mfma_f32_16x16x32_bf16 v[104:107], v[152:155], v[208:211], 0
	v_mfma_f32_16x16x32_bf16 v[100:103], v[160:163], v[208:211], 0
	v_mfma_f32_16x16x32_bf16 v[88:91], v[152:155], v[216:219], 0
	v_mfma_f32_16x16x32_bf16 v[84:87], v[160:163], v[216:219], 0
	v_mfma_f32_16x16x32_bf16 v[128:131], v[156:159], v[188:191], v[128:131]
	v_mfma_f32_16x16x32_bf16 v[124:127], v[164:167], v[188:191], v[124:127]
	v_mfma_f32_16x16x32_bf16 v[120:123], v[156:159], v[204:207], v[120:123]
	v_mfma_f32_16x16x32_bf16 v[116:119], v[164:167], v[204:207], v[116:119]
	v_mfma_f32_16x16x32_bf16 v[104:107], v[156:159], v[212:215], v[104:107]
	v_mfma_f32_16x16x32_bf16 v[100:103], v[164:167], v[212:215], v[100:103]
	v_mfma_f32_16x16x32_bf16 v[88:91], v[156:159], v[220:223], v[88:91]
	v_mfma_f32_16x16x32_bf16 v[84:87], v[164:167], v[220:223], v[84:87]
	v_mfma_f32_16x16x32_bf16 v[112:115], v[168:171], v[184:187], 0
	v_mfma_f32_16x16x32_bf16 v[108:111], v[176:179], v[184:187], 0
	v_mfma_f32_16x16x32_bf16 v[96:99], v[168:171], v[192:195], 0
	v_mfma_f32_16x16x32_bf16 v[92:95], v[176:179], v[192:195], 0
	v_mfma_f32_16x16x32_bf16 v[80:83], v[168:171], v[208:211], 0
	v_mfma_f32_16x16x32_bf16 v[76:79], v[176:179], v[208:211], 0
	v_mfma_f32_16x16x32_bf16 v[72:75], v[168:171], v[216:219], 0
	v_mfma_f32_16x16x32_bf16 v[68:71], v[176:179], v[216:219], 0
	v_mfma_f32_16x16x32_bf16 v[112:115], v[172:175], v[188:191], v[112:115]
	v_mfma_f32_16x16x32_bf16 v[108:111], v[180:183], v[188:191], v[108:111]
	v_mfma_f32_16x16x32_bf16 v[96:99], v[172:175], v[204:207], v[96:99]
	v_mfma_f32_16x16x32_bf16 v[92:95], v[180:183], v[204:207], v[92:95]
	v_mfma_f32_16x16x32_bf16 v[80:83], v[172:175], v[212:215], v[80:83]
	v_mfma_f32_16x16x32_bf16 v[76:79], v[180:183], v[212:215], v[76:79]
	v_mfma_f32_16x16x32_bf16 v[72:75], v[172:175], v[220:223], v[72:75]
	v_mfma_f32_16x16x32_bf16 v[68:71], v[180:183], v[220:223], v[68:71]
	s_setprio 0
	s_barrier
	s_add_i32 s69, s71, s16
	v_lshl_add_u64 v[196:197], s[50:51], 0, v[134:135]
	s_mov_b32 m0, s69
	ds_read_b128 v[184:187], v151 offset:16384
	ds_read_b128 v[188:191], v151 offset:17408
	ds_read_b128 v[192:195], v151 offset:18432
	ds_read_b128 v[204:207], v151 offset:19456
	ds_read_b128 v[208:211], v151 offset:20480
	ds_read_b128 v[212:215], v151 offset:21504
	ds_read_b128 v[216:219], v151 offset:22528
	ds_read_b128 v[220:223], v151 offset:23552
	global_load_lds_dwordx4 v[196:197], off
	s_add_i32 m0, s69, 0x2000
	s_add_u32 s70, s50, 0x40000
	v_lshl_add_u64 v[198:199], s[50:51], 0, v[138:139]
	s_addc_u32 s71, s51, 0
	s_add_i32 s69, s72, s16
	global_load_lds_dwordx4 v[198:199], off
	v_lshl_add_u64 v[224:225], s[70:71], 0, v[134:135]
	s_mov_b32 m0, s69
	s_nop 0
	global_load_lds_dwordx4 v[224:225], off
	v_lshl_add_u64 v[224:225], s[70:71], 0, v[138:139]
	s_add_i32 m0, s69, 0x2000
	s_nop 0
	global_load_lds_dwordx4 v[224:225], off
	v_lshl_add_u64 v[224:225], s[4:5], 0, v[132:133]
	s_mov_b32 m0, s17
	s_nop 0
	global_load_lds_dwordx4 v[224:225], off
	v_lshl_add_u64 v[224:225], s[4:5], 0, v[136:137]
	s_mov_b32 m0, s21
	s_nop 0
	global_load_lds_dwordx4 v[224:225], off
	s_waitcnt vmcnt(8)
	s_waitcnt lgkmcnt(0)
	s_barrier
	s_setprio 1
	v_mfma_f32_16x16x32_bf16 v[64:67], v[152:155], v[184:187], 0
	v_mfma_f32_16x16x32_bf16 v[60:63], v[160:163], v[184:187], 0
	v_mfma_f32_16x16x32_bf16 v[56:59], v[152:155], v[192:195], 0
	v_mfma_f32_16x16x32_bf16 v[52:55], v[160:163], v[192:195], 0
	v_mfma_f32_16x16x32_bf16 v[40:43], v[152:155], v[208:211], 0
	v_mfma_f32_16x16x32_bf16 v[36:39], v[160:163], v[208:211], 0
	v_mfma_f32_16x16x32_bf16 v[24:27], v[152:155], v[216:219], 0
	v_mfma_f32_16x16x32_bf16 v[20:23], v[160:163], v[216:219], 0
	v_mfma_f32_16x16x32_bf16 v[64:67], v[156:159], v[188:191], v[64:67]
	v_mfma_f32_16x16x32_bf16 v[60:63], v[164:167], v[188:191], v[60:63]
	v_mfma_f32_16x16x32_bf16 v[56:59], v[156:159], v[204:207], v[56:59]
	v_mfma_f32_16x16x32_bf16 v[52:55], v[164:167], v[204:207], v[52:55]
	v_mfma_f32_16x16x32_bf16 v[40:43], v[156:159], v[212:215], v[40:43]
	v_mfma_f32_16x16x32_bf16 v[36:39], v[164:167], v[212:215], v[36:39]
	v_mfma_f32_16x16x32_bf16 v[24:27], v[156:159], v[220:223], v[24:27]
	v_mfma_f32_16x16x32_bf16 v[20:23], v[164:167], v[220:223], v[20:23]
	v_mfma_f32_16x16x32_bf16 v[48:51], v[168:171], v[184:187], 0
	v_mfma_f32_16x16x32_bf16 v[44:47], v[176:179], v[184:187], 0
	v_mfma_f32_16x16x32_bf16 v[32:35], v[168:171], v[192:195], 0
	v_mfma_f32_16x16x32_bf16 v[28:31], v[176:179], v[192:195], 0
	v_mfma_f32_16x16x32_bf16 v[16:19], v[168:171], v[208:211], 0
	v_mfma_f32_16x16x32_bf16 v[12:15], v[176:179], v[208:211], 0
	v_mfma_f32_16x16x32_bf16 v[8:11], v[168:171], v[216:219], 0
	v_mfma_f32_16x16x32_bf16 v[4:7], v[176:179], v[216:219], 0
	v_mfma_f32_16x16x32_bf16 v[48:51], v[172:175], v[188:191], v[48:51]
	v_mfma_f32_16x16x32_bf16 v[44:47], v[180:183], v[188:191], v[44:47]
	v_mfma_f32_16x16x32_bf16 v[32:35], v[172:175], v[204:207], v[32:35]
	v_mfma_f32_16x16x32_bf16 v[28:31], v[180:183], v[204:207], v[28:31]
	v_mfma_f32_16x16x32_bf16 v[16:19], v[172:175], v[212:215], v[16:19]
	v_mfma_f32_16x16x32_bf16 v[12:15], v[180:183], v[212:215], v[12:15]
	v_mfma_f32_16x16x32_bf16 v[8:11], v[172:175], v[220:223], v[8:11]
	v_mfma_f32_16x16x32_bf16 v[4:7], v[180:183], v[220:223], v[4:7]
	s_setprio 0
	s_barrier
	s_add_i32 s69, 0, 0x18000
	v_add_u32_e32 v2, s69, v149
	s_add_i32 s70, 0, 0x1c000
	ds_read_b128 v[152:155], v2
	ds_read_b128 v[156:159], v2 offset:1024
	ds_read_b128 v[160:163], v2 offset:2048
	ds_read_b128 v[164:167], v2 offset:3072
	v_add_u32_e32 v2, s70, v149
	ds_read_b128 v[168:171], v2
	ds_read_b128 v[172:175], v2 offset:1024
	ds_read_b128 v[176:179], v2 offset:2048
	ds_read_b128 v[180:183], v2 offset:3072
	s_add_u32 s4, s4, 0x40000
	s_addc_u32 s5, s5, 0
	s_mov_b32 m0, s46
	v_lshl_add_u64 v[224:225], s[4:5], 0, v[132:133]
	ds_read_b128 v[184:187], v151 offset:32768
	ds_read_b128 v[188:191], v151 offset:33792
	ds_read_b128 v[192:195], v151 offset:34816
	ds_read_b128 v[204:207], v151 offset:35840
	ds_read_b128 v[208:211], v151 offset:36864
	ds_read_b128 v[212:215], v151 offset:37888
	ds_read_b128 v[216:219], v151 offset:38912
	ds_read_b128 v[220:223], v151 offset:39936
	global_load_lds_dwordx4 v[224:225], off
	v_lshl_add_u64 v[224:225], s[4:5], 0, v[136:137]
	s_mov_b32 m0, s47
	s_nop 0
	global_load_lds_dwordx4 v[224:225], off
	s_waitcnt vmcnt(8)
	s_waitcnt lgkmcnt(0)
	s_barrier
	s_setprio 1
	v_mfma_f32_16x16x32_bf16 v[128:131], v[152:155], v[184:187], v[128:131]
	v_mfma_f32_16x16x32_bf16 v[124:127], v[160:163], v[184:187], v[124:127]
	v_mfma_f32_16x16x32_bf16 v[120:123], v[152:155], v[192:195], v[120:123]
	v_mfma_f32_16x16x32_bf16 v[116:119], v[160:163], v[192:195], v[116:119]
	v_mfma_f32_16x16x32_bf16 v[104:107], v[152:155], v[208:211], v[104:107]
	v_mfma_f32_16x16x32_bf16 v[100:103], v[160:163], v[208:211], v[100:103]
	v_mfma_f32_16x16x32_bf16 v[88:91], v[152:155], v[216:219], v[88:91]
	v_mfma_f32_16x16x32_bf16 v[84:87], v[160:163], v[216:219], v[84:87]
	v_mfma_f32_16x16x32_bf16 v[128:131], v[156:159], v[188:191], v[128:131]
	v_mfma_f32_16x16x32_bf16 v[124:127], v[164:167], v[188:191], v[124:127]
	v_mfma_f32_16x16x32_bf16 v[120:123], v[156:159], v[204:207], v[120:123]
	v_mfma_f32_16x16x32_bf16 v[116:119], v[164:167], v[204:207], v[116:119]
	v_mfma_f32_16x16x32_bf16 v[104:107], v[156:159], v[212:215], v[104:107]
	v_mfma_f32_16x16x32_bf16 v[100:103], v[164:167], v[212:215], v[100:103]
	v_mfma_f32_16x16x32_bf16 v[88:91], v[156:159], v[220:223], v[88:91]
	v_mfma_f32_16x16x32_bf16 v[84:87], v[164:167], v[220:223], v[84:87]
	v_mfma_f32_16x16x32_bf16 v[112:115], v[168:171], v[184:187], v[112:115]
	v_mfma_f32_16x16x32_bf16 v[108:111], v[176:179], v[184:187], v[108:111]
	v_mfma_f32_16x16x32_bf16 v[96:99], v[168:171], v[192:195], v[96:99]
	v_mfma_f32_16x16x32_bf16 v[92:95], v[176:179], v[192:195], v[92:95]
	v_mfma_f32_16x16x32_bf16 v[80:83], v[168:171], v[208:211], v[80:83]
	v_mfma_f32_16x16x32_bf16 v[76:79], v[176:179], v[208:211], v[76:79]
	v_mfma_f32_16x16x32_bf16 v[72:75], v[168:171], v[216:219], v[72:75]
	v_mfma_f32_16x16x32_bf16 v[68:71], v[176:179], v[216:219], v[68:71]
	v_mfma_f32_16x16x32_bf16 v[112:115], v[172:175], v[188:191], v[112:115]
	v_mfma_f32_16x16x32_bf16 v[108:111], v[180:183], v[188:191], v[108:111]
	v_mfma_f32_16x16x32_bf16 v[96:99], v[172:175], v[204:207], v[96:99]
	v_mfma_f32_16x16x32_bf16 v[92:95], v[180:183], v[204:207], v[92:95]
	v_mfma_f32_16x16x32_bf16 v[80:83], v[172:175], v[212:215], v[80:83]
	v_mfma_f32_16x16x32_bf16 v[76:79], v[180:183], v[212:215], v[76:79]
	v_mfma_f32_16x16x32_bf16 v[72:75], v[172:175], v[220:223], v[72:75]
	v_mfma_f32_16x16x32_bf16 v[68:71], v[180:183], v[220:223], v[68:71]
	s_setprio 0
	s_barrier
	s_add_i32 s4, s69, s16
	v_lshl_add_u64 v[196:197], v[196:197], 0, s[34:35]
	s_mov_b32 m0, s4
	ds_read_b128 v[184:187], v151 offset:49152
	ds_read_b128 v[188:191], v151 offset:50176
	ds_read_b128 v[192:195], v151 offset:51200
	ds_read_b128 v[204:207], v151 offset:52224
	ds_read_b128 v[208:211], v151 offset:53248
	ds_read_b128 v[212:215], v151 offset:54272
	ds_read_b128 v[216:219], v151 offset:55296
	ds_read_b128 v[220:223], v151 offset:56320
	global_load_lds_dwordx4 v[196:197], off
	s_add_i32 m0, s4, 0x2000
	s_add_u32 s4, s50, 0x40080
	v_lshl_add_u64 v[196:197], v[198:199], 0, s[34:35]
	s_addc_u32 s5, s51, 0
	s_add_i32 s50, s70, s16
	global_load_lds_dwordx4 v[196:197], off
	v_lshl_add_u64 v[196:197], s[4:5], 0, v[134:135]
	s_mov_b32 m0, s50
	s_nop 0
	global_load_lds_dwordx4 v[196:197], off
	v_lshl_add_u64 v[196:197], s[4:5], 0, v[138:139]
	s_add_i32 m0, s50, 0x2000
	s_nop 0
	global_load_lds_dwordx4 v[196:197], off
	v_lshl_add_u64 v[196:197], s[12:13], 0, v[132:133]
	s_mov_b32 m0, s53
	s_nop 0
	global_load_lds_dwordx4 v[196:197], off
	v_lshl_add_u64 v[196:197], s[12:13], 0, v[136:137]
	s_mov_b32 m0, s56
	s_nop 0
	global_load_lds_dwordx4 v[196:197], off
	s_waitcnt vmcnt(8)
	s_waitcnt lgkmcnt(0)
	s_barrier
	s_setprio 1
	v_mfma_f32_16x16x32_bf16 v[64:67], v[152:155], v[184:187], v[64:67]
	v_mfma_f32_16x16x32_bf16 v[60:63], v[160:163], v[184:187], v[60:63]
	v_mfma_f32_16x16x32_bf16 v[56:59], v[152:155], v[192:195], v[56:59]
	v_mfma_f32_16x16x32_bf16 v[52:55], v[160:163], v[192:195], v[52:55]
	v_mfma_f32_16x16x32_bf16 v[40:43], v[152:155], v[208:211], v[40:43]
	v_mfma_f32_16x16x32_bf16 v[36:39], v[160:163], v[208:211], v[36:39]
	v_mfma_f32_16x16x32_bf16 v[24:27], v[152:155], v[216:219], v[24:27]
	v_mfma_f32_16x16x32_bf16 v[20:23], v[160:163], v[216:219], v[20:23]
	v_mfma_f32_16x16x32_bf16 v[64:67], v[156:159], v[188:191], v[64:67]
	v_mfma_f32_16x16x32_bf16 v[60:63], v[164:167], v[188:191], v[60:63]
	v_mfma_f32_16x16x32_bf16 v[56:59], v[156:159], v[204:207], v[56:59]
	v_mfma_f32_16x16x32_bf16 v[52:55], v[164:167], v[204:207], v[52:55]
	v_mfma_f32_16x16x32_bf16 v[40:43], v[156:159], v[212:215], v[40:43]
	v_mfma_f32_16x16x32_bf16 v[36:39], v[164:167], v[212:215], v[36:39]
	v_mfma_f32_16x16x32_bf16 v[24:27], v[156:159], v[220:223], v[24:27]
	v_mfma_f32_16x16x32_bf16 v[20:23], v[164:167], v[220:223], v[20:23]
	v_mfma_f32_16x16x32_bf16 v[48:51], v[168:171], v[184:187], v[48:51]
	v_mfma_f32_16x16x32_bf16 v[44:47], v[176:179], v[184:187], v[44:47]
	v_mfma_f32_16x16x32_bf16 v[32:35], v[168:171], v[192:195], v[32:35]
	v_mfma_f32_16x16x32_bf16 v[28:31], v[176:179], v[192:195], v[28:31]
	v_mfma_f32_16x16x32_bf16 v[16:19], v[168:171], v[208:211], v[16:19]
	v_mfma_f32_16x16x32_bf16 v[12:15], v[176:179], v[208:211], v[12:15]
	v_mfma_f32_16x16x32_bf16 v[8:11], v[168:171], v[216:219], v[8:11]
	v_mfma_f32_16x16x32_bf16 v[4:7], v[176:179], v[216:219], v[4:7]
	v_mfma_f32_16x16x32_bf16 v[48:51], v[172:175], v[188:191], v[48:51]
	v_mfma_f32_16x16x32_bf16 v[44:47], v[180:183], v[188:191], v[44:47]
	v_mfma_f32_16x16x32_bf16 v[32:35], v[172:175], v[204:207], v[32:35]
	v_mfma_f32_16x16x32_bf16 v[28:31], v[180:183], v[204:207], v[28:31]
	v_mfma_f32_16x16x32_bf16 v[16:19], v[172:175], v[212:215], v[16:19]
	v_mfma_f32_16x16x32_bf16 v[12:15], v[180:183], v[212:215], v[12:15]
	v_mfma_f32_16x16x32_bf16 v[8:11], v[172:175], v[220:223], v[8:11]
	v_mfma_f32_16x16x32_bf16 v[4:7], v[180:183], v[220:223], v[4:7]
	s_setprio 0
	s_barrier
	s_add_i32 s68, s68, 2
	s_add_u32 s48, s48, 0x100
	s_addc_u32 s49, s49, 0
	s_cmp_gt_u32 s68, 13
.LBB0_311:
	s_add_u32 s4, s38, s48
	s_addc_u32 s5, s39, s49
	s_add_u32 s69, s4, 0x100
	s_addc_u32 s70, s5, 0
	s_add_u32 s50, s64, s48
	s_addc_u32 s51, s65, s49
	s_add_u32 s4, s4, 0x180
	s_addc_u32 s5, s5, 0
	s_add_i32 s71, 0, 0x10000
	s_add_i32 s72, 0, 0x14000
	v_add_u32_e32 v2, s71, v149
	ds_read_b128 v[152:155], v2
	s_waitcnt vmcnt(0)
	ds_read_b128 v[156:159], v2 offset:1024
	ds_read_b128 v[160:163], v2 offset:2048
	ds_read_b128 v[164:167], v2 offset:3072
	v_add_u32_e32 v2, s72, v149
	ds_read_b128 v[168:171], v2
	ds_read_b128 v[172:175], v2 offset:1024
	ds_read_b128 v[176:179], v2 offset:2048
	ds_read_b128 v[180:183], v2 offset:3072
	s_cmpk_eq_i32 s48, 0x700
	s_cselect_b32 s13, s63, s5
	s_cselect_b32 s12, s62, s4
	s_cselect_b32 s51, s37, s51
	s_cselect_b32 s50, s61, s50
	s_cselect_b32 s5, s41, s70
	s_cselect_b32 s4, s60, s69
	v_lshl_add_u64 v[196:197], v[144:145], 0, s[48:49]
	s_add_i32 m0, s17, 0xc000
	ds_read_b128 v[184:187], v151
	ds_read_b128 v[188:191], v151 offset:1024
	ds_read_b128 v[192:195], v151 offset:2048
	ds_read_b128 v[204:207], v151 offset:3072
	ds_read_b128 v[208:211], v151 offset:4096
	ds_read_b128 v[212:215], v151 offset:5120
	ds_read_b128 v[216:219], v151 offset:6144
	ds_read_b128 v[220:223], v151 offset:7168
	global_load_lds_dwordx4 v[196:197], off
	v_lshl_add_u64 v[196:197], v[146:147], 0, s[48:49]
	s_add_i32 m0, s17, 0xe000
	s_nop 0
	global_load_lds_dwordx4 v[196:197], off
	s_waitcnt vmcnt(8)
	s_waitcnt lgkmcnt(0)
	s_barrier
	s_setprio 1
	v_mfma_f32_16x16x32_bf16 v[128:131], v[152:155], v[184:187], v[128:131]
	v_mfma_f32_16x16x32_bf16 v[124:127], v[160:163], v[184:187], v[124:127]
	v_mfma_f32_16x16x32_bf16 v[120:123], v[152:155], v[192:195], v[120:123]
	v_mfma_f32_16x16x32_bf16 v[116:119], v[160:163], v[192:195], v[116:119]
	v_mfma_f32_16x16x32_bf16 v[104:107], v[152:155], v[208:211], v[104:107]
	v_mfma_f32_16x16x32_bf16 v[100:103], v[160:163], v[208:211], v[100:103]
	v_mfma_f32_16x16x32_bf16 v[88:91], v[152:155], v[216:219], v[88:91]
	v_mfma_f32_16x16x32_bf16 v[84:87], v[160:163], v[216:219], v[84:87]
	v_mfma_f32_16x16x32_bf16 v[128:131], v[156:159], v[188:191], v[128:131]
	v_mfma_f32_16x16x32_bf16 v[124:127], v[164:167], v[188:191], v[124:127]
	v_mfma_f32_16x16x32_bf16 v[120:123], v[156:159], v[204:207], v[120:123]
	v_mfma_f32_16x16x32_bf16 v[116:119], v[164:167], v[204:207], v[116:119]
	v_mfma_f32_16x16x32_bf16 v[104:107], v[156:159], v[212:215], v[104:107]
	v_mfma_f32_16x16x32_bf16 v[100:103], v[164:167], v[212:215], v[100:103]
	v_mfma_f32_16x16x32_bf16 v[88:91], v[156:159], v[220:223], v[88:91]
	v_mfma_f32_16x16x32_bf16 v[84:87], v[164:167], v[220:223], v[84:87]
	v_mfma_f32_16x16x32_bf16 v[112:115], v[168:171], v[184:187], v[112:115]
	v_mfma_f32_16x16x32_bf16 v[108:111], v[176:179], v[184:187], v[108:111]
	v_mfma_f32_16x16x32_bf16 v[96:99], v[168:171], v[192:195], v[96:99]
	v_mfma_f32_16x16x32_bf16 v[92:95], v[176:179], v[192:195], v[92:95]
	v_mfma_f32_16x16x32_bf16 v[80:83], v[168:171], v[208:211], v[80:83]
	v_mfma_f32_16x16x32_bf16 v[76:79], v[176:179], v[208:211], v[76:79]
	v_mfma_f32_16x16x32_bf16 v[72:75], v[168:171], v[216:219], v[72:75]
	v_mfma_f32_16x16x32_bf16 v[68:71], v[176:179], v[216:219], v[68:71]
	v_mfma_f32_16x16x32_bf16 v[112:115], v[172:175], v[188:191], v[112:115]
	v_mfma_f32_16x16x32_bf16 v[108:111], v[180:183], v[188:191], v[108:111]
	v_mfma_f32_16x16x32_bf16 v[96:99], v[172:175], v[204:207], v[96:99]
	v_mfma_f32_16x16x32_bf16 v[92:95], v[180:183], v[204:207], v[92:95]
	v_mfma_f32_16x16x32_bf16 v[80:83], v[172:175], v[212:215], v[80:83]
	v_mfma_f32_16x16x32_bf16 v[76:79], v[180:183], v[212:215], v[76:79]
	v_mfma_f32_16x16x32_bf16 v[72:75], v[172:175], v[220:223], v[72:75]
	v_mfma_f32_16x16x32_bf16 v[68:71], v[180:183], v[220:223], v[68:71]
	s_setprio 0
	s_barrier
	s_add_i32 s69, s71, s16
	v_lshl_add_u64 v[196:197], s[50:51], 0, v[134:135]
	s_mov_b32 m0, s69
	ds_read_b128 v[184:187], v151 offset:16384
	ds_read_b128 v[188:191], v151 offset:17408
	ds_read_b128 v[192:195], v151 offset:18432
	ds_read_b128 v[204:207], v151 offset:19456
	ds_read_b128 v[208:211], v151 offset:20480
	ds_read_b128 v[212:215], v151 offset:21504
	ds_read_b128 v[216:219], v151 offset:22528
	ds_read_b128 v[220:223], v151 offset:23552
	global_load_lds_dwordx4 v[196:197], off
	s_add_i32 m0, s69, 0x2000
	s_add_u32 s70, s50, 0x40000
	v_lshl_add_u64 v[198:199], s[50:51], 0, v[138:139]
	s_addc_u32 s71, s51, 0
	s_add_i32 s69, s72, s16
	global_load_lds_dwordx4 v[198:199], off
	v_lshl_add_u64 v[224:225], s[70:71], 0, v[134:135]
	s_mov_b32 m0, s69
	s_nop 0
	global_load_lds_dwordx4 v[224:225], off
	v_lshl_add_u64 v[224:225], s[70:71], 0, v[138:139]
	s_add_i32 m0, s69, 0x2000
	s_nop 0
	global_load_lds_dwordx4 v[224:225], off
	v_lshl_add_u64 v[224:225], s[4:5], 0, v[132:133]
	s_mov_b32 m0, s17
	s_nop 0
	global_load_lds_dwordx4 v[224:225], off
	v_lshl_add_u64 v[224:225], s[4:5], 0, v[136:137]
	s_mov_b32 m0, s21
	s_nop 0
	global_load_lds_dwordx4 v[224:225], off
	s_waitcnt vmcnt(8)
	s_waitcnt lgkmcnt(0)
	s_barrier
	s_setprio 1
	v_mfma_f32_16x16x32_bf16 v[64:67], v[152:155], v[184:187], v[64:67]
	v_mfma_f32_16x16x32_bf16 v[60:63], v[160:163], v[184:187], v[60:63]
	v_mfma_f32_16x16x32_bf16 v[56:59], v[152:155], v[192:195], v[56:59]
	v_mfma_f32_16x16x32_bf16 v[52:55], v[160:163], v[192:195], v[52:55]
	v_mfma_f32_16x16x32_bf16 v[40:43], v[152:155], v[208:211], v[40:43]
	v_mfma_f32_16x16x32_bf16 v[36:39], v[160:163], v[208:211], v[36:39]
	v_mfma_f32_16x16x32_bf16 v[24:27], v[152:155], v[216:219], v[24:27]
	v_mfma_f32_16x16x32_bf16 v[20:23], v[160:163], v[216:219], v[20:23]
	v_mfma_f32_16x16x32_bf16 v[64:67], v[156:159], v[188:191], v[64:67]
	v_mfma_f32_16x16x32_bf16 v[60:63], v[164:167], v[188:191], v[60:63]
	v_mfma_f32_16x16x32_bf16 v[56:59], v[156:159], v[204:207], v[56:59]
	v_mfma_f32_16x16x32_bf16 v[52:55], v[164:167], v[204:207], v[52:55]
	v_mfma_f32_16x16x32_bf16 v[40:43], v[156:159], v[212:215], v[40:43]
	v_mfma_f32_16x16x32_bf16 v[36:39], v[164:167], v[212:215], v[36:39]
	v_mfma_f32_16x16x32_bf16 v[24:27], v[156:159], v[220:223], v[24:27]
	v_mfma_f32_16x16x32_bf16 v[20:23], v[164:167], v[220:223], v[20:23]
	v_mfma_f32_16x16x32_bf16 v[48:51], v[168:171], v[184:187], v[48:51]
	v_mfma_f32_16x16x32_bf16 v[44:47], v[176:179], v[184:187], v[44:47]
	v_mfma_f32_16x16x32_bf16 v[32:35], v[168:171], v[192:195], v[32:35]
	v_mfma_f32_16x16x32_bf16 v[28:31], v[176:179], v[192:195], v[28:31]
	v_mfma_f32_16x16x32_bf16 v[16:19], v[168:171], v[208:211], v[16:19]
	v_mfma_f32_16x16x32_bf16 v[12:15], v[176:179], v[208:211], v[12:15]
	v_mfma_f32_16x16x32_bf16 v[8:11], v[168:171], v[216:219], v[8:11]
	v_mfma_f32_16x16x32_bf16 v[4:7], v[176:179], v[216:219], v[4:7]
	v_mfma_f32_16x16x32_bf16 v[48:51], v[172:175], v[188:191], v[48:51]
	v_mfma_f32_16x16x32_bf16 v[44:47], v[180:183], v[188:191], v[44:47]
	v_mfma_f32_16x16x32_bf16 v[32:35], v[172:175], v[204:207], v[32:35]
	v_mfma_f32_16x16x32_bf16 v[28:31], v[180:183], v[204:207], v[28:31]
	v_mfma_f32_16x16x32_bf16 v[16:19], v[172:175], v[212:215], v[16:19]
	v_mfma_f32_16x16x32_bf16 v[12:15], v[180:183], v[212:215], v[12:15]
	v_mfma_f32_16x16x32_bf16 v[8:11], v[172:175], v[220:223], v[8:11]
	v_mfma_f32_16x16x32_bf16 v[4:7], v[180:183], v[220:223], v[4:7]
	s_setprio 0
	s_barrier
	s_add_i32 s69, 0, 0x18000
	v_add_u32_e32 v2, s69, v149
	s_add_i32 s70, 0, 0x1c000
	ds_read_b128 v[152:155], v2
	ds_read_b128 v[156:159], v2 offset:1024
	ds_read_b128 v[160:163], v2 offset:2048
	ds_read_b128 v[164:167], v2 offset:3072
	v_add_u32_e32 v2, s70, v149
	ds_read_b128 v[168:171], v2
	ds_read_b128 v[172:175], v2 offset:1024
	ds_read_b128 v[176:179], v2 offset:2048
	ds_read_b128 v[180:183], v2 offset:3072
	s_add_u32 s4, s4, 0x40000
	s_addc_u32 s5, s5, 0
	s_mov_b32 m0, s46
	v_lshl_add_u64 v[224:225], s[4:5], 0, v[132:133]
	ds_read_b128 v[184:187], v151 offset:32768
	ds_read_b128 v[188:191], v151 offset:33792
	ds_read_b128 v[192:195], v151 offset:34816
	ds_read_b128 v[204:207], v151 offset:35840
	ds_read_b128 v[208:211], v151 offset:36864
	ds_read_b128 v[212:215], v151 offset:37888
	ds_read_b128 v[216:219], v151 offset:38912
	ds_read_b128 v[220:223], v151 offset:39936
	global_load_lds_dwordx4 v[224:225], off
	v_lshl_add_u64 v[224:225], s[4:5], 0, v[136:137]
	s_mov_b32 m0, s47
	s_nop 0
	global_load_lds_dwordx4 v[224:225], off
	s_waitcnt vmcnt(8)
	s_waitcnt lgkmcnt(0)
	s_barrier
	s_setprio 1
	v_mfma_f32_16x16x32_bf16 v[128:131], v[152:155], v[184:187], v[128:131]
	v_mfma_f32_16x16x32_bf16 v[124:127], v[160:163], v[184:187], v[124:127]
	v_mfma_f32_16x16x32_bf16 v[120:123], v[152:155], v[192:195], v[120:123]
	v_mfma_f32_16x16x32_bf16 v[116:119], v[160:163], v[192:195], v[116:119]
	v_mfma_f32_16x16x32_bf16 v[104:107], v[152:155], v[208:211], v[104:107]
	v_mfma_f32_16x16x32_bf16 v[100:103], v[160:163], v[208:211], v[100:103]
	v_mfma_f32_16x16x32_bf16 v[88:91], v[152:155], v[216:219], v[88:91]
	v_mfma_f32_16x16x32_bf16 v[84:87], v[160:163], v[216:219], v[84:87]
	v_mfma_f32_16x16x32_bf16 v[128:131], v[156:159], v[188:191], v[128:131]
	v_mfma_f32_16x16x32_bf16 v[124:127], v[164:167], v[188:191], v[124:127]
	v_mfma_f32_16x16x32_bf16 v[120:123], v[156:159], v[204:207], v[120:123]
	v_mfma_f32_16x16x32_bf16 v[116:119], v[164:167], v[204:207], v[116:119]
	v_mfma_f32_16x16x32_bf16 v[104:107], v[156:159], v[212:215], v[104:107]
	v_mfma_f32_16x16x32_bf16 v[100:103], v[164:167], v[212:215], v[100:103]
	v_mfma_f32_16x16x32_bf16 v[88:91], v[156:159], v[220:223], v[88:91]
	v_mfma_f32_16x16x32_bf16 v[84:87], v[164:167], v[220:223], v[84:87]
	v_mfma_f32_16x16x32_bf16 v[112:115], v[168:171], v[184:187], v[112:115]
	v_mfma_f32_16x16x32_bf16 v[108:111], v[176:179], v[184:187], v[108:111]
	v_mfma_f32_16x16x32_bf16 v[96:99], v[168:171], v[192:195], v[96:99]
	v_mfma_f32_16x16x32_bf16 v[92:95], v[176:179], v[192:195], v[92:95]
	v_mfma_f32_16x16x32_bf16 v[80:83], v[168:171], v[208:211], v[80:83]
	v_mfma_f32_16x16x32_bf16 v[76:79], v[176:179], v[208:211], v[76:79]
	v_mfma_f32_16x16x32_bf16 v[72:75], v[168:171], v[216:219], v[72:75]
	v_mfma_f32_16x16x32_bf16 v[68:71], v[176:179], v[216:219], v[68:71]
	v_mfma_f32_16x16x32_bf16 v[112:115], v[172:175], v[188:191], v[112:115]
	v_mfma_f32_16x16x32_bf16 v[108:111], v[180:183], v[188:191], v[108:111]
	v_mfma_f32_16x16x32_bf16 v[96:99], v[172:175], v[204:207], v[96:99]
	v_mfma_f32_16x16x32_bf16 v[92:95], v[180:183], v[204:207], v[92:95]
	v_mfma_f32_16x16x32_bf16 v[80:83], v[172:175], v[212:215], v[80:83]
	v_mfma_f32_16x16x32_bf16 v[76:79], v[180:183], v[212:215], v[76:79]
	v_mfma_f32_16x16x32_bf16 v[72:75], v[172:175], v[220:223], v[72:75]
	v_mfma_f32_16x16x32_bf16 v[68:71], v[180:183], v[220:223], v[68:71]
	s_setprio 0
	s_barrier
	s_add_i32 s4, s69, s16
	v_lshl_add_u64 v[196:197], v[196:197], 0, s[34:35]
	s_mov_b32 m0, s4
	ds_read_b128 v[184:187], v151 offset:49152
	ds_read_b128 v[188:191], v151 offset:50176
	ds_read_b128 v[192:195], v151 offset:51200
	ds_read_b128 v[204:207], v151 offset:52224
	ds_read_b128 v[208:211], v151 offset:53248
	ds_read_b128 v[212:215], v151 offset:54272
	ds_read_b128 v[216:219], v151 offset:55296
	ds_read_b128 v[220:223], v151 offset:56320
	global_load_lds_dwordx4 v[196:197], off
	s_add_i32 m0, s4, 0x2000
	s_add_u32 s4, s50, 0x40080
	v_lshl_add_u64 v[196:197], v[198:199], 0, s[34:35]
	s_addc_u32 s5, s51, 0
	s_add_i32 s50, s70, s16
	global_load_lds_dwordx4 v[196:197], off
	v_lshl_add_u64 v[196:197], s[4:5], 0, v[134:135]
	s_mov_b32 m0, s50
	s_nop 0
	global_load_lds_dwordx4 v[196:197], off
	v_lshl_add_u64 v[196:197], s[4:5], 0, v[138:139]
	s_add_i32 m0, s50, 0x2000
	s_nop 0
	global_load_lds_dwordx4 v[196:197], off
	v_lshl_add_u64 v[196:197], s[12:13], 0, v[132:133]
	s_mov_b32 m0, s53
	s_nop 0
	global_load_lds_dwordx4 v[196:197], off
	v_lshl_add_u64 v[196:197], s[12:13], 0, v[136:137]
	s_mov_b32 m0, s56
	s_nop 0
	global_load_lds_dwordx4 v[196:197], off
	s_waitcnt vmcnt(8)
	s_waitcnt lgkmcnt(0)
	s_barrier
	s_setprio 1
	v_mfma_f32_16x16x32_bf16 v[64:67], v[152:155], v[184:187], v[64:67]
	v_mfma_f32_16x16x32_bf16 v[60:63], v[160:163], v[184:187], v[60:63]
	v_mfma_f32_16x16x32_bf16 v[56:59], v[152:155], v[192:195], v[56:59]
	v_mfma_f32_16x16x32_bf16 v[52:55], v[160:163], v[192:195], v[52:55]
	v_mfma_f32_16x16x32_bf16 v[40:43], v[152:155], v[208:211], v[40:43]
	v_mfma_f32_16x16x32_bf16 v[36:39], v[160:163], v[208:211], v[36:39]
	v_mfma_f32_16x16x32_bf16 v[24:27], v[152:155], v[216:219], v[24:27]
	v_mfma_f32_16x16x32_bf16 v[20:23], v[160:163], v[216:219], v[20:23]
	v_mfma_f32_16x16x32_bf16 v[64:67], v[156:159], v[188:191], v[64:67]
	v_mfma_f32_16x16x32_bf16 v[60:63], v[164:167], v[188:191], v[60:63]
	v_mfma_f32_16x16x32_bf16 v[56:59], v[156:159], v[204:207], v[56:59]
	v_mfma_f32_16x16x32_bf16 v[52:55], v[164:167], v[204:207], v[52:55]
	v_mfma_f32_16x16x32_bf16 v[40:43], v[156:159], v[212:215], v[40:43]
	v_mfma_f32_16x16x32_bf16 v[36:39], v[164:167], v[212:215], v[36:39]
	v_mfma_f32_16x16x32_bf16 v[24:27], v[156:159], v[220:223], v[24:27]
	v_mfma_f32_16x16x32_bf16 v[20:23], v[164:167], v[220:223], v[20:23]
	v_mfma_f32_16x16x32_bf16 v[48:51], v[168:171], v[184:187], v[48:51]
	v_mfma_f32_16x16x32_bf16 v[44:47], v[176:179], v[184:187], v[44:47]
	v_mfma_f32_16x16x32_bf16 v[32:35], v[168:171], v[192:195], v[32:35]
	v_mfma_f32_16x16x32_bf16 v[28:31], v[176:179], v[192:195], v[28:31]
	v_mfma_f32_16x16x32_bf16 v[16:19], v[168:171], v[208:211], v[16:19]
	v_mfma_f32_16x16x32_bf16 v[12:15], v[176:179], v[208:211], v[12:15]
	v_mfma_f32_16x16x32_bf16 v[8:11], v[168:171], v[216:219], v[8:11]
	v_mfma_f32_16x16x32_bf16 v[4:7], v[176:179], v[216:219], v[4:7]
	v_mfma_f32_16x16x32_bf16 v[48:51], v[172:175], v[188:191], v[48:51]
	v_mfma_f32_16x16x32_bf16 v[44:47], v[180:183], v[188:191], v[44:47]
	v_mfma_f32_16x16x32_bf16 v[32:35], v[172:175], v[204:207], v[32:35]
	v_mfma_f32_16x16x32_bf16 v[28:31], v[180:183], v[204:207], v[28:31]
	v_mfma_f32_16x16x32_bf16 v[16:19], v[172:175], v[212:215], v[16:19]
	v_mfma_f32_16x16x32_bf16 v[12:15], v[180:183], v[212:215], v[12:15]
	v_mfma_f32_16x16x32_bf16 v[8:11], v[172:175], v[220:223], v[8:11]
	v_mfma_f32_16x16x32_bf16 v[4:7], v[180:183], v[220:223], v[4:7]
	s_setprio 0
	s_barrier
	s_add_i32 s68, s68, 2
	s_add_u32 s48, s48, 0x100
	s_addc_u32 s49, s49, 0
	s_cmp_gt_u32 s68, 13
	s_cbranch_scc0 .LBB0_311
	s_and_b64 vcc, exec, s[18:19]
	s_mov_b32 s62, 0x18000
	s_mov_b32 s63, 0x1a000
	s_cbranch_vccz .LBB0_314
	s_barrier

.LBB0_382:
	s_ashr_i32 s51, s50, 31
	s_lshl_b64 s[4:5], s[50:51], 19
	s_add_u32 s64, s8, s4
	s_addc_u32 s65, s9, s5
	s_and_b64 s[4:5], s[38:39], exec
	s_cselect_b32 s51, s65, s41
	s_cselect_b32 s71, s64, s40
	s_ashr_i32 s11, s10, 31
	s_lshl_b64 s[4:5], s[10:11], 18
	s_add_u32 s36, s16, s4
	s_addc_u32 s37, s17, s5
	s_and_b64 s[4:5], s[38:39], exec
	s_cselect_b32 s11, s37, s43
	s_cselect_b32 s74, s36, s42
	s_add_u32 s75, s71, 0x80
	s_addc_u32 s76, s51, 0
	s_add_u32 s4, s40, 0x40080
	s_addc_u32 s5, s41, 0
	s_add_u32 s77, s42, 0x100
	v_lshl_add_u64 v[100:101], s[4:5], 0, v[176:177]
	v_lshl_add_u64 v[102:103], s[4:5], 0, v[178:179]
	s_addc_u32 s78, s43, 0
	s_mov_b32 s79, -2
	s_mov_b64 s[42:43], 0
	s_add_u32 s4, s40, s42
	s_addc_u32 s5, s41, s43
	s_add_u32 s80, s4, 0x100
	s_addc_u32 s81, s5, 0
	s_add_u32 s48, s77, s42
	s_addc_u32 s49, s78, s43
	s_add_u32 s4, s4, 0x180
	s_addc_u32 s5, s5, 0
	s_add_i32 s82, 0, 0x10000
	s_add_i32 s83, 0, 0x14000
	v_add_u32_e32 v2, s82, v203
	ds_read_b128 v[104:107], v2
	ds_read_b128 v[124:127], v2 offset:1024
	ds_read_b128 v[128:131], v2 offset:2048
	ds_read_b128 v[148:151], v2 offset:3072
	v_add_u32_e32 v2, s83, v203
	ds_read_b128 v[152:155], v2
	ds_read_b128 v[156:159], v2 offset:1024
	ds_read_b128 v[160:163], v2 offset:2048
	ds_read_b128 v[164:167], v2 offset:3072
	s_cmpk_eq_i32 s42, 0x300
	s_cselect_b32 s45, s76, s5
	s_cselect_b32 s44, s75, s4
	s_cselect_b32 s49, s11, s49
	s_cselect_b32 s48, s74, s48
	s_cselect_b32 s5, s51, s81
	s_cselect_b32 s4, s71, s80
	v_lshl_add_u64 v[196:197], v[100:101], 0, s[42:43]
	s_add_i32 m0, s47, 0xc000
	ds_read_b128 v[180:183], v210
	ds_read_b128 v[184:187], v210 offset:1024
	ds_read_b128 v[188:191], v210 offset:2048
	ds_read_b128 v[192:195], v210 offset:3072
	ds_read_b128 v[204:207], v210 offset:4096
	ds_read_b128 v[212:215], v210 offset:5120
	ds_read_b128 v[216:219], v210 offset:6144
	ds_read_b128 v[220:223], v210 offset:7168
	global_load_lds_dwordx4 v[196:197], off
	v_lshl_add_u64 v[196:197], v[102:103], 0, s[42:43]
	s_add_i32 m0, s47, 0xe000
	s_nop 0
	global_load_lds_dwordx4 v[196:197], off
	s_waitcnt vmcnt(8)
	s_waitcnt lgkmcnt(0)
	s_barrier
	s_setprio 1
	v_mfma_f32_16x16x32_bf16 v[144:147], v[104:107], v[180:183], 0
	v_mfma_f32_16x16x32_bf16 v[140:143], v[128:131], v[180:183], 0
	v_mfma_f32_16x16x32_bf16 v[120:123], v[104:107], v[188:191], 0
	v_mfma_f32_16x16x32_bf16 v[116:119], v[128:131], v[188:191], 0
	v_mfma_f32_16x16x32_bf16 v[96:99], v[104:107], v[204:207], 0
	v_mfma_f32_16x16x32_bf16 v[92:95], v[128:131], v[204:207], 0
	v_mfma_f32_16x16x32_bf16 v[80:83], v[104:107], v[216:219], 0
	v_mfma_f32_16x16x32_bf16 v[76:79], v[128:131], v[216:219], 0
	v_mfma_f32_16x16x32_bf16 v[144:147], v[124:127], v[184:187], v[144:147]
	v_mfma_f32_16x16x32_bf16 v[140:143], v[148:151], v[184:187], v[140:143]
	v_mfma_f32_16x16x32_bf16 v[120:123], v[124:127], v[192:195], v[120:123]
	v_mfma_f32_16x16x32_bf16 v[116:119], v[148:151], v[192:195], v[116:119]
	v_mfma_f32_16x16x32_bf16 v[96:99], v[124:127], v[212:215], v[96:99]
	v_mfma_f32_16x16x32_bf16 v[92:95], v[148:151], v[212:215], v[92:95]
	v_mfma_f32_16x16x32_bf16 v[80:83], v[124:127], v[220:223], v[80:83]
	v_mfma_f32_16x16x32_bf16 v[76:79], v[148:151], v[220:223], v[76:79]
	v_mfma_f32_16x16x32_bf16 v[136:139], v[152:155], v[180:183], 0
	v_mfma_f32_16x16x32_bf16 v[132:135], v[160:163], v[180:183], 0
	v_mfma_f32_16x16x32_bf16 v[112:115], v[152:155], v[188:191], 0
	v_mfma_f32_16x16x32_bf16 v[108:111], v[160:163], v[188:191], 0
	v_mfma_f32_16x16x32_bf16 v[88:91], v[152:155], v[204:207], 0
	v_mfma_f32_16x16x32_bf16 v[84:87], v[160:163], v[204:207], 0
	v_mfma_f32_16x16x32_bf16 v[72:75], v[152:155], v[216:219], 0
	v_mfma_f32_16x16x32_bf16 v[68:71], v[160:163], v[216:219], 0
	v_mfma_f32_16x16x32_bf16 v[136:139], v[156:159], v[184:187], v[136:139]
	v_mfma_f32_16x16x32_bf16 v[132:135], v[164:167], v[184:187], v[132:135]
	v_mfma_f32_16x16x32_bf16 v[112:115], v[156:159], v[192:195], v[112:115]
	v_mfma_f32_16x16x32_bf16 v[108:111], v[164:167], v[192:195], v[108:111]
	v_mfma_f32_16x16x32_bf16 v[88:91], v[156:159], v[212:215], v[88:91]
	v_mfma_f32_16x16x32_bf16 v[84:87], v[164:167], v[212:215], v[84:87]
	v_mfma_f32_16x16x32_bf16 v[72:75], v[156:159], v[220:223], v[72:75]
	v_mfma_f32_16x16x32_bf16 v[68:71], v[164:167], v[220:223], v[68:71]
	s_setprio 0
	s_barrier
	s_add_i32 s80, s82, s46
	v_lshl_add_u64 v[196:197], s[48:49], 0, v[172:173]
	s_mov_b32 m0, s80
	ds_read_b128 v[180:183], v210 offset:16384
	ds_read_b128 v[184:187], v210 offset:17408
	ds_read_b128 v[188:191], v210 offset:18432
	ds_read_b128 v[192:195], v210 offset:19456
	ds_read_b128 v[204:207], v210 offset:20480
	ds_read_b128 v[212:215], v210 offset:21504
	ds_read_b128 v[216:219], v210 offset:22528
	ds_read_b128 v[220:223], v210 offset:23552
	global_load_lds_dwordx4 v[196:197], off
	s_add_i32 m0, s80, 0x2000
	s_add_u32 s80, s48, 0x20000
	v_lshl_add_u64 v[198:199], s[48:49], 0, v[168:169]
	s_addc_u32 s81, s49, 0
	s_add_i32 s82, s83, s46
	global_load_lds_dwordx4 v[198:199], off
	v_lshl_add_u64 v[208:209], s[80:81], 0, v[172:173]
	s_mov_b32 m0, s82
	s_nop 0
	global_load_lds_dwordx4 v[208:209], off
	v_lshl_add_u64 v[208:209], s[80:81], 0, v[168:169]
	s_add_i32 m0, s82, 0x2000
	s_nop 0
	global_load_lds_dwordx4 v[208:209], off
	v_lshl_add_u64 v[208:209], s[4:5], 0, v[174:175]
	s_mov_b32 m0, s47
	s_nop 0
	global_load_lds_dwordx4 v[208:209], off
	v_lshl_add_u64 v[208:209], s[4:5], 0, v[170:171]
	s_mov_b32 m0, s56
	s_nop 0
	global_load_lds_dwordx4 v[208:209], off
	s_waitcnt vmcnt(8)
	s_waitcnt lgkmcnt(0)
	s_barrier
	s_setprio 1
	v_mfma_f32_16x16x32_bf16 v[64:67], v[104:107], v[180:183], 0
	v_mfma_f32_16x16x32_bf16 v[60:63], v[128:131], v[180:183], 0
	v_mfma_f32_16x16x32_bf16 v[48:51], v[104:107], v[188:191], 0
	v_mfma_f32_16x16x32_bf16 v[44:47], v[128:131], v[188:191], 0
	v_mfma_f32_16x16x32_bf16 v[32:35], v[104:107], v[204:207], 0
	v_mfma_f32_16x16x32_bf16 v[28:31], v[128:131], v[204:207], 0
	v_mfma_f32_16x16x32_bf16 v[16:19], v[104:107], v[216:219], 0
	v_mfma_f32_16x16x32_bf16 v[12:15], v[128:131], v[216:219], 0
	v_mfma_f32_16x16x32_bf16 v[64:67], v[124:127], v[184:187], v[64:67]
	v_mfma_f32_16x16x32_bf16 v[60:63], v[148:151], v[184:187], v[60:63]
	v_mfma_f32_16x16x32_bf16 v[48:51], v[124:127], v[192:195], v[48:51]
	v_mfma_f32_16x16x32_bf16 v[44:47], v[148:151], v[192:195], v[44:47]
	v_mfma_f32_16x16x32_bf16 v[32:35], v[124:127], v[212:215], v[32:35]
	v_mfma_f32_16x16x32_bf16 v[28:31], v[148:151], v[212:215], v[28:31]
	v_mfma_f32_16x16x32_bf16 v[16:19], v[124:127], v[220:223], v[16:19]
	v_mfma_f32_16x16x32_bf16 v[12:15], v[148:151], v[220:223], v[12:15]
	v_mfma_f32_16x16x32_bf16 v[56:59], v[152:155], v[180:183], 0
	v_mfma_f32_16x16x32_bf16 v[52:55], v[160:163], v[180:183], 0
	v_mfma_f32_16x16x32_bf16 v[40:43], v[152:155], v[188:191], 0
	v_mfma_f32_16x16x32_bf16 v[36:39], v[160:163], v[188:191], 0
	v_mfma_f32_16x16x32_bf16 v[24:27], v[152:155], v[204:207], 0
	v_mfma_f32_16x16x32_bf16 v[20:23], v[160:163], v[204:207], 0
	v_mfma_f32_16x16x32_bf16 v[8:11], v[152:155], v[216:219], 0
	v_mfma_f32_16x16x32_bf16 v[4:7], v[160:163], v[216:219], 0
	v_mfma_f32_16x16x32_bf16 v[56:59], v[156:159], v[184:187], v[56:59]
	v_mfma_f32_16x16x32_bf16 v[52:55], v[164:167], v[184:187], v[52:55]
	v_mfma_f32_16x16x32_bf16 v[40:43], v[156:159], v[192:195], v[40:43]
	v_mfma_f32_16x16x32_bf16 v[36:39], v[164:167], v[192:195], v[36:39]
	v_mfma_f32_16x16x32_bf16 v[24:27], v[156:159], v[212:215], v[24:27]
	v_mfma_f32_16x16x32_bf16 v[20:23], v[164:167], v[212:215], v[20:23]
	v_mfma_f32_16x16x32_bf16 v[8:11], v[156:159], v[220:223], v[8:11]
	v_mfma_f32_16x16x32_bf16 v[4:7], v[164:167], v[220:223], v[4:7]
	s_setprio 0
	s_barrier
	s_add_i32 s80, 0, 0x18000
	v_add_u32_e32 v2, s80, v203
	s_add_i32 s81, 0, 0x1c000
	ds_read_b128 v[104:107], v2
	ds_read_b128 v[124:127], v2 offset:1024
	ds_read_b128 v[128:131], v2 offset:2048
	ds_read_b128 v[148:151], v2 offset:3072
	v_add_u32_e32 v2, s81, v203
	ds_read_b128 v[152:155], v2
	ds_read_b128 v[156:159], v2 offset:1024
	ds_read_b128 v[160:163], v2 offset:2048
	ds_read_b128 v[164:167], v2 offset:3072
	s_add_u32 s4, s4, 0x40000
	s_addc_u32 s5, s5, 0
	s_mov_b32 m0, s58
	v_lshl_add_u64 v[208:209], s[4:5], 0, v[174:175]
	ds_read_b128 v[180:183], v210 offset:32768
	ds_read_b128 v[184:187], v210 offset:33792
	ds_read_b128 v[188:191], v210 offset:34816
	ds_read_b128 v[192:195], v210 offset:35840
	ds_read_b128 v[204:207], v210 offset:36864
	ds_read_b128 v[212:215], v210 offset:37888
	ds_read_b128 v[216:219], v210 offset:38912
	ds_read_b128 v[220:223], v210 offset:39936
	global_load_lds_dwordx4 v[208:209], off
	v_lshl_add_u64 v[208:209], s[4:5], 0, v[170:171]
	s_mov_b32 m0, s59
	s_nop 0
	global_load_lds_dwordx4 v[208:209], off
	s_waitcnt vmcnt(8)
	s_waitcnt lgkmcnt(0)
	s_barrier
	s_setprio 1
	v_mfma_f32_16x16x32_bf16 v[144:147], v[104:107], v[180:183], v[144:147]
	v_mfma_f32_16x16x32_bf16 v[140:143], v[128:131], v[180:183], v[140:143]
	v_mfma_f32_16x16x32_bf16 v[120:123], v[104:107], v[188:191], v[120:123]
	v_mfma_f32_16x16x32_bf16 v[116:119], v[128:131], v[188:191], v[116:119]
	v_mfma_f32_16x16x32_bf16 v[96:99], v[104:107], v[204:207], v[96:99]
	v_mfma_f32_16x16x32_bf16 v[92:95], v[128:131], v[204:207], v[92:95]
	v_mfma_f32_16x16x32_bf16 v[80:83], v[104:107], v[216:219], v[80:83]
	v_mfma_f32_16x16x32_bf16 v[76:79], v[128:131], v[216:219], v[76:79]
	v_mfma_f32_16x16x32_bf16 v[144:147], v[124:127], v[184:187], v[144:147]
	v_mfma_f32_16x16x32_bf16 v[140:143], v[148:151], v[184:187], v[140:143]
	v_mfma_f32_16x16x32_bf16 v[120:123], v[124:127], v[192:195], v[120:123]
	v_mfma_f32_16x16x32_bf16 v[116:119], v[148:151], v[192:195], v[116:119]
	v_mfma_f32_16x16x32_bf16 v[96:99], v[124:127], v[212:215], v[96:99]
	v_mfma_f32_16x16x32_bf16 v[92:95], v[148:151], v[212:215], v[92:95]
	v_mfma_f32_16x16x32_bf16 v[80:83], v[124:127], v[220:223], v[80:83]
	v_mfma_f32_16x16x32_bf16 v[76:79], v[148:151], v[220:223], v[76:79]
	v_mfma_f32_16x16x32_bf16 v[136:139], v[152:155], v[180:183], v[136:139]
	v_mfma_f32_16x16x32_bf16 v[132:135], v[160:163], v[180:183], v[132:135]
	v_mfma_f32_16x16x32_bf16 v[112:115], v[152:155], v[188:191], v[112:115]
	v_mfma_f32_16x16x32_bf16 v[108:111], v[160:163], v[188:191], v[108:111]
	v_mfma_f32_16x16x32_bf16 v[88:91], v[152:155], v[204:207], v[88:91]
	v_mfma_f32_16x16x32_bf16 v[84:87], v[160:163], v[204:207], v[84:87]
	v_mfma_f32_16x16x32_bf16 v[72:75], v[152:155], v[216:219], v[72:75]
	v_mfma_f32_16x16x32_bf16 v[68:71], v[160:163], v[216:219], v[68:71]
	v_mfma_f32_16x16x32_bf16 v[136:139], v[156:159], v[184:187], v[136:139]
	v_mfma_f32_16x16x32_bf16 v[132:135], v[164:167], v[184:187], v[132:135]
	v_mfma_f32_16x16x32_bf16 v[112:115], v[156:159], v[192:195], v[112:115]
	v_mfma_f32_16x16x32_bf16 v[108:111], v[164:167], v[192:195], v[108:111]
	v_mfma_f32_16x16x32_bf16 v[88:91], v[156:159], v[212:215], v[88:91]
	v_mfma_f32_16x16x32_bf16 v[84:87], v[164:167], v[212:215], v[84:87]
	v_mfma_f32_16x16x32_bf16 v[72:75], v[156:159], v[220:223], v[72:75]
	v_mfma_f32_16x16x32_bf16 v[68:71], v[164:167], v[220:223], v[68:71]
	s_setprio 0
	s_barrier
	s_add_i32 s4, s80, s46
	v_lshl_add_u64 v[196:197], v[196:197], 0, s[34:35]
	s_mov_b32 m0, s4
	ds_read_b128 v[180:183], v210 offset:49152
	ds_read_b128 v[184:187], v210 offset:50176
	ds_read_b128 v[188:191], v210 offset:51200
	ds_read_b128 v[192:195], v210 offset:52224
	ds_read_b128 v[204:207], v210 offset:53248
	ds_read_b128 v[212:215], v210 offset:54272
	ds_read_b128 v[216:219], v210 offset:55296
	ds_read_b128 v[220:223], v210 offset:56320
	global_load_lds_dwordx4 v[196:197], off
	s_add_i32 m0, s4, 0x2000
	s_add_u32 s4, s48, 0x20080
	v_lshl_add_u64 v[196:197], v[198:199], 0, s[34:35]
	s_addc_u32 s5, s49, 0
	s_add_i32 s48, s81, s46
	global_load_lds_dwordx4 v[196:197], off
	v_lshl_add_u64 v[196:197], s[4:5], 0, v[172:173]
	s_mov_b32 m0, s48
	s_nop 0
	global_load_lds_dwordx4 v[196:197], off
	v_lshl_add_u64 v[196:197], s[4:5], 0, v[168:169]
	s_add_i32 m0, s48, 0x2000
	s_nop 0
	global_load_lds_dwordx4 v[196:197], off
	v_lshl_add_u64 v[196:197], s[44:45], 0, v[174:175]
	s_mov_b32 m0, s68
	s_nop 0
	global_load_lds_dwordx4 v[196:197], off
	v_lshl_add_u64 v[196:197], s[44:45], 0, v[170:171]
	s_mov_b32 m0, s69
	s_nop 0
	global_load_lds_dwordx4 v[196:197], off
	s_waitcnt vmcnt(8)
	s_waitcnt lgkmcnt(0)
	s_barrier
	s_setprio 1
	v_mfma_f32_16x16x32_bf16 v[64:67], v[104:107], v[180:183], v[64:67]
	v_mfma_f32_16x16x32_bf16 v[60:63], v[128:131], v[180:183], v[60:63]
	v_mfma_f32_16x16x32_bf16 v[48:51], v[104:107], v[188:191], v[48:51]
	v_mfma_f32_16x16x32_bf16 v[44:47], v[128:131], v[188:191], v[44:47]
	v_mfma_f32_16x16x32_bf16 v[32:35], v[104:107], v[204:207], v[32:35]
	v_mfma_f32_16x16x32_bf16 v[28:31], v[128:131], v[204:207], v[28:31]
	v_mfma_f32_16x16x32_bf16 v[16:19], v[104:107], v[216:219], v[16:19]
	v_mfma_f32_16x16x32_bf16 v[12:15], v[128:131], v[216:219], v[12:15]
	v_mfma_f32_16x16x32_bf16 v[64:67], v[124:127], v[184:187], v[64:67]
	v_mfma_f32_16x16x32_bf16 v[60:63], v[148:151], v[184:187], v[60:63]
	v_mfma_f32_16x16x32_bf16 v[48:51], v[124:127], v[192:195], v[48:51]
	v_mfma_f32_16x16x32_bf16 v[44:47], v[148:151], v[192:195], v[44:47]
	v_mfma_f32_16x16x32_bf16 v[32:35], v[124:127], v[212:215], v[32:35]
	v_mfma_f32_16x16x32_bf16 v[28:31], v[148:151], v[212:215], v[28:31]
	v_mfma_f32_16x16x32_bf16 v[16:19], v[124:127], v[220:223], v[16:19]
	v_mfma_f32_16x16x32_bf16 v[12:15], v[148:151], v[220:223], v[12:15]
	v_mfma_f32_16x16x32_bf16 v[56:59], v[152:155], v[180:183], v[56:59]
	v_mfma_f32_16x16x32_bf16 v[52:55], v[160:163], v[180:183], v[52:55]
	v_mfma_f32_16x16x32_bf16 v[40:43], v[152:155], v[188:191], v[40:43]
	v_mfma_f32_16x16x32_bf16 v[36:39], v[160:163], v[188:191], v[36:39]
	v_mfma_f32_16x16x32_bf16 v[24:27], v[152:155], v[204:207], v[24:27]
	v_mfma_f32_16x16x32_bf16 v[20:23], v[160:163], v[204:207], v[20:23]
	v_mfma_f32_16x16x32_bf16 v[8:11], v[152:155], v[216:219], v[8:11]
	v_mfma_f32_16x16x32_bf16 v[4:7], v[160:163], v[216:219], v[4:7]
	v_mfma_f32_16x16x32_bf16 v[56:59], v[156:159], v[184:187], v[56:59]
	v_mfma_f32_16x16x32_bf16 v[52:55], v[164:167], v[184:187], v[52:55]
	v_mfma_f32_16x16x32_bf16 v[40:43], v[156:159], v[192:195], v[40:43]
	v_mfma_f32_16x16x32_bf16 v[36:39], v[164:167], v[192:195], v[36:39]
	v_mfma_f32_16x16x32_bf16 v[24:27], v[156:159], v[212:215], v[24:27]
	v_mfma_f32_16x16x32_bf16 v[20:23], v[164:167], v[212:215], v[20:23]
	v_mfma_f32_16x16x32_bf16 v[8:11], v[156:159], v[220:223], v[8:11]
	v_mfma_f32_16x16x32_bf16 v[4:7], v[164:167], v[220:223], v[4:7]
	s_setprio 0
	s_barrier
	s_add_i32 s79, s79, 2
	s_add_u32 s42, s42, 0x100
	s_addc_u32 s43, s43, 0
	s_cmp_gt_u32 s79, 5
.LBB0_383:
	s_add_u32 s4, s40, s42
	s_addc_u32 s5, s41, s43
	s_add_u32 s80, s4, 0x100
	s_addc_u32 s81, s5, 0
	s_add_u32 s48, s77, s42
	s_addc_u32 s49, s78, s43
	s_add_u32 s4, s4, 0x180
	s_addc_u32 s5, s5, 0
	s_add_i32 s82, 0, 0x10000
	s_add_i32 s83, 0, 0x14000
	v_add_u32_e32 v2, s82, v203
	ds_read_b128 v[104:107], v2
	ds_read_b128 v[124:127], v2 offset:1024
	ds_read_b128 v[128:131], v2 offset:2048
	ds_read_b128 v[148:151], v2 offset:3072
	v_add_u32_e32 v2, s83, v203
	ds_read_b128 v[152:155], v2
	ds_read_b128 v[156:159], v2 offset:1024
	ds_read_b128 v[160:163], v2 offset:2048
	ds_read_b128 v[164:167], v2 offset:3072
	s_cmpk_eq_i32 s42, 0x300
	s_cselect_b32 s45, s76, s5
	s_cselect_b32 s44, s75, s4
	s_cselect_b32 s49, s11, s49
	s_cselect_b32 s48, s74, s48
	s_cselect_b32 s5, s51, s81
	s_cselect_b32 s4, s71, s80
	v_lshl_add_u64 v[196:197], v[100:101], 0, s[42:43]
	s_add_i32 m0, s47, 0xc000
	ds_read_b128 v[180:183], v210
	ds_read_b128 v[184:187], v210 offset:1024
	ds_read_b128 v[188:191], v210 offset:2048
	ds_read_b128 v[192:195], v210 offset:3072
	ds_read_b128 v[204:207], v210 offset:4096
	ds_read_b128 v[212:215], v210 offset:5120
	ds_read_b128 v[216:219], v210 offset:6144
	ds_read_b128 v[220:223], v210 offset:7168
	global_load_lds_dwordx4 v[196:197], off
	v_lshl_add_u64 v[196:197], v[102:103], 0, s[42:43]
	s_add_i32 m0, s47, 0xe000
	s_nop 0
	global_load_lds_dwordx4 v[196:197], off
	s_waitcnt vmcnt(8)
	s_waitcnt lgkmcnt(0)
	s_barrier
	s_setprio 1
	v_mfma_f32_16x16x32_bf16 v[144:147], v[104:107], v[180:183], v[144:147]
	v_mfma_f32_16x16x32_bf16 v[140:143], v[128:131], v[180:183], v[140:143]
	v_mfma_f32_16x16x32_bf16 v[120:123], v[104:107], v[188:191], v[120:123]
	v_mfma_f32_16x16x32_bf16 v[116:119], v[128:131], v[188:191], v[116:119]
	v_mfma_f32_16x16x32_bf16 v[96:99], v[104:107], v[204:207], v[96:99]
	v_mfma_f32_16x16x32_bf16 v[92:95], v[128:131], v[204:207], v[92:95]
	v_mfma_f32_16x16x32_bf16 v[80:83], v[104:107], v[216:219], v[80:83]
	v_mfma_f32_16x16x32_bf16 v[76:79], v[128:131], v[216:219], v[76:79]
	v_mfma_f32_16x16x32_bf16 v[144:147], v[124:127], v[184:187], v[144:147]
	v_mfma_f32_16x16x32_bf16 v[140:143], v[148:151], v[184:187], v[140:143]
	v_mfma_f32_16x16x32_bf16 v[120:123], v[124:127], v[192:195], v[120:123]
	v_mfma_f32_16x16x32_bf16 v[116:119], v[148:151], v[192:195], v[116:119]
	v_mfma_f32_16x16x32_bf16 v[96:99], v[124:127], v[212:215], v[96:99]
	v_mfma_f32_16x16x32_bf16 v[92:95], v[148:151], v[212:215], v[92:95]
	v_mfma_f32_16x16x32_bf16 v[80:83], v[124:127], v[220:223], v[80:83]
	v_mfma_f32_16x16x32_bf16 v[76:79], v[148:151], v[220:223], v[76:79]
	v_mfma_f32_16x16x32_bf16 v[136:139], v[152:155], v[180:183], v[136:139]
	v_mfma_f32_16x16x32_bf16 v[132:135], v[160:163], v[180:183], v[132:135]
	v_mfma_f32_16x16x32_bf16 v[112:115], v[152:155], v[188:191], v[112:115]
	v_mfma_f32_16x16x32_bf16 v[108:111], v[160:163], v[188:191], v[108:111]
	v_mfma_f32_16x16x32_bf16 v[88:91], v[152:155], v[204:207], v[88:91]
	v_mfma_f32_16x16x32_bf16 v[84:87], v[160:163], v[204:207], v[84:87]
	v_mfma_f32_16x16x32_bf16 v[72:75], v[152:155], v[216:219], v[72:75]
	v_mfma_f32_16x16x32_bf16 v[68:71], v[160:163], v[216:219], v[68:71]
	v_mfma_f32_16x16x32_bf16 v[136:139], v[156:159], v[184:187], v[136:139]
	v_mfma_f32_16x16x32_bf16 v[132:135], v[164:167], v[184:187], v[132:135]
	v_mfma_f32_16x16x32_bf16 v[112:115], v[156:159], v[192:195], v[112:115]
	v_mfma_f32_16x16x32_bf16 v[108:111], v[164:167], v[192:195], v[108:111]
	v_mfma_f32_16x16x32_bf16 v[88:91], v[156:159], v[212:215], v[88:91]
	v_mfma_f32_16x16x32_bf16 v[84:87], v[164:167], v[212:215], v[84:87]
	v_mfma_f32_16x16x32_bf16 v[72:75], v[156:159], v[220:223], v[72:75]
	v_mfma_f32_16x16x32_bf16 v[68:71], v[164:167], v[220:223], v[68:71]
	s_setprio 0
	s_barrier
	s_add_i32 s80, s82, s46
	v_lshl_add_u64 v[196:197], s[48:49], 0, v[172:173]
	s_mov_b32 m0, s80
	ds_read_b128 v[180:183], v210 offset:16384
	ds_read_b128 v[184:187], v210 offset:17408
	ds_read_b128 v[188:191], v210 offset:18432
	ds_read_b128 v[192:195], v210 offset:19456
	ds_read_b128 v[204:207], v210 offset:20480
	ds_read_b128 v[212:215], v210 offset:21504
	ds_read_b128 v[216:219], v210 offset:22528
	ds_read_b128 v[220:223], v210 offset:23552
	global_load_lds_dwordx4 v[196:197], off
	s_add_i32 m0, s80, 0x2000
	s_add_u32 s80, s48, 0x20000
	v_lshl_add_u64 v[198:199], s[48:49], 0, v[168:169]
	s_addc_u32 s81, s49, 0
	s_add_i32 s82, s83, s46
	global_load_lds_dwordx4 v[198:199], off
	v_lshl_add_u64 v[208:209], s[80:81], 0, v[172:173]
	s_mov_b32 m0, s82
	s_nop 0
	global_load_lds_dwordx4 v[208:209], off
	v_lshl_add_u64 v[208:209], s[80:81], 0, v[168:169]
	s_add_i32 m0, s82, 0x2000
	s_nop 0
	global_load_lds_dwordx4 v[208:209], off
	v_lshl_add_u64 v[208:209], s[4:5], 0, v[174:175]
	s_mov_b32 m0, s47
	s_nop 0
	global_load_lds_dwordx4 v[208:209], off
	v_lshl_add_u64 v[208:209], s[4:5], 0, v[170:171]
	s_mov_b32 m0, s56
	s_nop 0
	global_load_lds_dwordx4 v[208:209], off
	s_waitcnt vmcnt(8)
	s_waitcnt lgkmcnt(0)
	s_barrier
	s_setprio 1
	v_mfma_f32_16x16x32_bf16 v[64:67], v[104:107], v[180:183], v[64:67]
	v_mfma_f32_16x16x32_bf16 v[60:63], v[128:131], v[180:183], v[60:63]
	v_mfma_f32_16x16x32_bf16 v[48:51], v[104:107], v[188:191], v[48:51]
	v_mfma_f32_16x16x32_bf16 v[44:47], v[128:131], v[188:191], v[44:47]
	v_mfma_f32_16x16x32_bf16 v[32:35], v[104:107], v[204:207], v[32:35]
	v_mfma_f32_16x16x32_bf16 v[28:31], v[128:131], v[204:207], v[28:31]
	v_mfma_f32_16x16x32_bf16 v[16:19], v[104:107], v[216:219], v[16:19]
	v_mfma_f32_16x16x32_bf16 v[12:15], v[128:131], v[216:219], v[12:15]
	v_mfma_f32_16x16x32_bf16 v[64:67], v[124:127], v[184:187], v[64:67]
	v_mfma_f32_16x16x32_bf16 v[60:63], v[148:151], v[184:187], v[60:63]
	v_mfma_f32_16x16x32_bf16 v[48:51], v[124:127], v[192:195], v[48:51]
	v_mfma_f32_16x16x32_bf16 v[44:47], v[148:151], v[192:195], v[44:47]
	v_mfma_f32_16x16x32_bf16 v[32:35], v[124:127], v[212:215], v[32:35]
	v_mfma_f32_16x16x32_bf16 v[28:31], v[148:151], v[212:215], v[28:31]
	v_mfma_f32_16x16x32_bf16 v[16:19], v[124:127], v[220:223], v[16:19]
	v_mfma_f32_16x16x32_bf16 v[12:15], v[148:151], v[220:223], v[12:15]
	v_mfma_f32_16x16x32_bf16 v[56:59], v[152:155], v[180:183], v[56:59]
	v_mfma_f32_16x16x32_bf16 v[52:55], v[160:163], v[180:183], v[52:55]
	v_mfma_f32_16x16x32_bf16 v[40:43], v[152:155], v[188:191], v[40:43]
	v_mfma_f32_16x16x32_bf16 v[36:39], v[160:163], v[188:191], v[36:39]
	v_mfma_f32_16x16x32_bf16 v[24:27], v[152:155], v[204:207], v[24:27]
	v_mfma_f32_16x16x32_bf16 v[20:23], v[160:163], v[204:207], v[20:23]
	v_mfma_f32_16x16x32_bf16 v[8:11], v[152:155], v[216:219], v[8:11]
	v_mfma_f32_16x16x32_bf16 v[4:7], v[160:163], v[216:219], v[4:7]
	v_mfma_f32_16x16x32_bf16 v[56:59], v[156:159], v[184:187], v[56:59]
	v_mfma_f32_16x16x32_bf16 v[52:55], v[164:167], v[184:187], v[52:55]
	v_mfma_f32_16x16x32_bf16 v[40:43], v[156:159], v[192:195], v[40:43]
	v_mfma_f32_16x16x32_bf16 v[36:39], v[164:167], v[192:195], v[36:39]
	v_mfma_f32_16x16x32_bf16 v[24:27], v[156:159], v[212:215], v[24:27]
	v_mfma_f32_16x16x32_bf16 v[20:23], v[164:167], v[212:215], v[20:23]
	v_mfma_f32_16x16x32_bf16 v[8:11], v[156:159], v[220:223], v[8:11]
	v_mfma_f32_16x16x32_bf16 v[4:7], v[164:167], v[220:223], v[4:7]
	s_setprio 0
	s_barrier
	s_add_i32 s80, 0, 0x18000
	v_add_u32_e32 v2, s80, v203
	s_add_i32 s81, 0, 0x1c000
	ds_read_b128 v[104:107], v2
	ds_read_b128 v[124:127], v2 offset:1024
	ds_read_b128 v[128:131], v2 offset:2048
	ds_read_b128 v[148:151], v2 offset:3072
	v_add_u32_e32 v2, s81, v203
	ds_read_b128 v[152:155], v2
	ds_read_b128 v[156:159], v2 offset:1024
	ds_read_b128 v[160:163], v2 offset:2048
	ds_read_b128 v[164:167], v2 offset:3072
	s_add_u32 s4, s4, 0x40000
	s_addc_u32 s5, s5, 0
	s_mov_b32 m0, s58
	v_lshl_add_u64 v[208:209], s[4:5], 0, v[174:175]
	ds_read_b128 v[180:183], v210 offset:32768
	ds_read_b128 v[184:187], v210 offset:33792
	ds_read_b128 v[188:191], v210 offset:34816
	ds_read_b128 v[192:195], v210 offset:35840
	ds_read_b128 v[204:207], v210 offset:36864
	ds_read_b128 v[212:215], v210 offset:37888
	ds_read_b128 v[216:219], v210 offset:38912
	ds_read_b128 v[220:223], v210 offset:39936
	global_load_lds_dwordx4 v[208:209], off
	v_lshl_add_u64 v[208:209], s[4:5], 0, v[170:171]
	s_mov_b32 m0, s59
	s_nop 0
	global_load_lds_dwordx4 v[208:209], off
	s_waitcnt vmcnt(8)
	s_waitcnt lgkmcnt(0)
	s_barrier
	s_setprio 1
	v_mfma_f32_16x16x32_bf16 v[144:147], v[104:107], v[180:183], v[144:147]
	v_mfma_f32_16x16x32_bf16 v[140:143], v[128:131], v[180:183], v[140:143]
	v_mfma_f32_16x16x32_bf16 v[120:123], v[104:107], v[188:191], v[120:123]
	v_mfma_f32_16x16x32_bf16 v[116:119], v[128:131], v[188:191], v[116:119]
	v_mfma_f32_16x16x32_bf16 v[96:99], v[104:107], v[204:207], v[96:99]
	v_mfma_f32_16x16x32_bf16 v[92:95], v[128:131], v[204:207], v[92:95]
	v_mfma_f32_16x16x32_bf16 v[80:83], v[104:107], v[216:219], v[80:83]
	v_mfma_f32_16x16x32_bf16 v[76:79], v[128:131], v[216:219], v[76:79]
	v_mfma_f32_16x16x32_bf16 v[144:147], v[124:127], v[184:187], v[144:147]
	v_mfma_f32_16x16x32_bf16 v[140:143], v[148:151], v[184:187], v[140:143]
	v_mfma_f32_16x16x32_bf16 v[120:123], v[124:127], v[192:195], v[120:123]
	v_mfma_f32_16x16x32_bf16 v[116:119], v[148:151], v[192:195], v[116:119]
	v_mfma_f32_16x16x32_bf16 v[96:99], v[124:127], v[212:215], v[96:99]
	v_mfma_f32_16x16x32_bf16 v[92:95], v[148:151], v[212:215], v[92:95]
	v_mfma_f32_16x16x32_bf16 v[80:83], v[124:127], v[220:223], v[80:83]
	v_mfma_f32_16x16x32_bf16 v[76:79], v[148:151], v[220:223], v[76:79]
	v_mfma_f32_16x16x32_bf16 v[136:139], v[152:155], v[180:183], v[136:139]
	v_mfma_f32_16x16x32_bf16 v[132:135], v[160:163], v[180:183], v[132:135]
	v_mfma_f32_16x16x32_bf16 v[112:115], v[152:155], v[188:191], v[112:115]
	v_mfma_f32_16x16x32_bf16 v[108:111], v[160:163], v[188:191], v[108:111]
	v_mfma_f32_16x16x32_bf16 v[88:91], v[152:155], v[204:207], v[88:91]
	v_mfma_f32_16x16x32_bf16 v[84:87], v[160:163], v[204:207], v[84:87]
	v_mfma_f32_16x16x32_bf16 v[72:75], v[152:155], v[216:219], v[72:75]
	v_mfma_f32_16x16x32_bf16 v[68:71], v[160:163], v[216:219], v[68:71]
	v_mfma_f32_16x16x32_bf16 v[136:139], v[156:159], v[184:187], v[136:139]
	v_mfma_f32_16x16x32_bf16 v[132:135], v[164:167], v[184:187], v[132:135]
	v_mfma_f32_16x16x32_bf16 v[112:115], v[156:159], v[192:195], v[112:115]
	v_mfma_f32_16x16x32_bf16 v[108:111], v[164:167], v[192:195], v[108:111]
	v_mfma_f32_16x16x32_bf16 v[88:91], v[156:159], v[212:215], v[88:91]
	v_mfma_f32_16x16x32_bf16 v[84:87], v[164:167], v[212:215], v[84:87]
	v_mfma_f32_16x16x32_bf16 v[72:75], v[156:159], v[220:223], v[72:75]
	v_mfma_f32_16x16x32_bf16 v[68:71], v[164:167], v[220:223], v[68:71]
	s_setprio 0
	s_barrier
	s_add_i32 s4, s80, s46
	v_lshl_add_u64 v[196:197], v[196:197], 0, s[34:35]
	s_mov_b32 m0, s4
	ds_read_b128 v[180:183], v210 offset:49152
	ds_read_b128 v[184:187], v210 offset:50176
	ds_read_b128 v[188:191], v210 offset:51200
	ds_read_b128 v[192:195], v210 offset:52224
	ds_read_b128 v[204:207], v210 offset:53248
	ds_read_b128 v[212:215], v210 offset:54272
	ds_read_b128 v[216:219], v210 offset:55296
	ds_read_b128 v[220:223], v210 offset:56320
	global_load_lds_dwordx4 v[196:197], off
	s_add_i32 m0, s4, 0x2000
	s_add_u32 s4, s48, 0x20080
	v_lshl_add_u64 v[196:197], v[198:199], 0, s[34:35]
	s_addc_u32 s5, s49, 0
	s_add_i32 s48, s81, s46
	global_load_lds_dwordx4 v[196:197], off
	v_lshl_add_u64 v[196:197], s[4:5], 0, v[172:173]
	s_mov_b32 m0, s48
	s_nop 0
	global_load_lds_dwordx4 v[196:197], off
	v_lshl_add_u64 v[196:197], s[4:5], 0, v[168:169]
	s_add_i32 m0, s48, 0x2000
	s_nop 0
	global_load_lds_dwordx4 v[196:197], off
	v_lshl_add_u64 v[196:197], s[44:45], 0, v[174:175]
	s_mov_b32 m0, s68
	s_nop 0
	global_load_lds_dwordx4 v[196:197], off
	v_lshl_add_u64 v[196:197], s[44:45], 0, v[170:171]
	s_mov_b32 m0, s69
	s_nop 0
	global_load_lds_dwordx4 v[196:197], off
	s_waitcnt vmcnt(8)
	s_waitcnt lgkmcnt(0)
	s_barrier
	s_setprio 1
	v_mfma_f32_16x16x32_bf16 v[64:67], v[104:107], v[180:183], v[64:67]
	v_mfma_f32_16x16x32_bf16 v[60:63], v[128:131], v[180:183], v[60:63]
	v_mfma_f32_16x16x32_bf16 v[48:51], v[104:107], v[188:191], v[48:51]
	v_mfma_f32_16x16x32_bf16 v[44:47], v[128:131], v[188:191], v[44:47]
	v_mfma_f32_16x16x32_bf16 v[32:35], v[104:107], v[204:207], v[32:35]
	v_mfma_f32_16x16x32_bf16 v[28:31], v[128:131], v[204:207], v[28:31]
	v_mfma_f32_16x16x32_bf16 v[16:19], v[104:107], v[216:219], v[16:19]
	v_mfma_f32_16x16x32_bf16 v[12:15], v[128:131], v[216:219], v[12:15]
	v_mfma_f32_16x16x32_bf16 v[64:67], v[124:127], v[184:187], v[64:67]
	v_mfma_f32_16x16x32_bf16 v[60:63], v[148:151], v[184:187], v[60:63]
	v_mfma_f32_16x16x32_bf16 v[48:51], v[124:127], v[192:195], v[48:51]
	v_mfma_f32_16x16x32_bf16 v[44:47], v[148:151], v[192:195], v[44:47]
	v_mfma_f32_16x16x32_bf16 v[32:35], v[124:127], v[212:215], v[32:35]
	v_mfma_f32_16x16x32_bf16 v[28:31], v[148:151], v[212:215], v[28:31]
	v_mfma_f32_16x16x32_bf16 v[16:19], v[124:127], v[220:223], v[16:19]
	v_mfma_f32_16x16x32_bf16 v[12:15], v[148:151], v[220:223], v[12:15]
	v_mfma_f32_16x16x32_bf16 v[56:59], v[152:155], v[180:183], v[56:59]
	v_mfma_f32_16x16x32_bf16 v[52:55], v[160:163], v[180:183], v[52:55]
	v_mfma_f32_16x16x32_bf16 v[40:43], v[152:155], v[188:191], v[40:43]
	v_mfma_f32_16x16x32_bf16 v[36:39], v[160:163], v[188:191], v[36:39]
	v_mfma_f32_16x16x32_bf16 v[24:27], v[152:155], v[204:207], v[24:27]
	v_mfma_f32_16x16x32_bf16 v[20:23], v[160:163], v[204:207], v[20:23]
	v_mfma_f32_16x16x32_bf16 v[8:11], v[152:155], v[216:219], v[8:11]
	v_mfma_f32_16x16x32_bf16 v[4:7], v[160:163], v[216:219], v[4:7]
	v_mfma_f32_16x16x32_bf16 v[56:59], v[156:159], v[184:187], v[56:59]
	v_mfma_f32_16x16x32_bf16 v[52:55], v[164:167], v[184:187], v[52:55]
	v_mfma_f32_16x16x32_bf16 v[40:43], v[156:159], v[192:195], v[40:43]
	v_mfma_f32_16x16x32_bf16 v[36:39], v[164:167], v[192:195], v[36:39]
	v_mfma_f32_16x16x32_bf16 v[24:27], v[156:159], v[212:215], v[24:27]
	v_mfma_f32_16x16x32_bf16 v[20:23], v[164:167], v[212:215], v[20:23]
	v_mfma_f32_16x16x32_bf16 v[8:11], v[156:159], v[220:223], v[8:11]
	v_mfma_f32_16x16x32_bf16 v[4:7], v[164:167], v[220:223], v[4:7]
	s_setprio 0
	s_barrier
	s_add_i32 s79, s79, 2
	s_add_u32 s42, s42, 0x100
	s_addc_u32 s43, s43, 0
	s_cmp_gt_u32 s79, 5
	s_cbranch_scc0 .LBB0_383
	s_and_b64 vcc, exec, s[72:73]
	s_cbranch_vccz .LBB0_386
	s_barrier

.LBB0_1043:
	s_ashr_i32 s41, s40, 31
	s_lshl_b64 s[4:5], s[40:41], 19
	s_add_u32 s42, s6, s4
	s_addc_u32 s43, s7, s5
	s_and_b64 s[4:5], s[38:39], exec
	s_cselect_b32 s41, s43, s49
	s_cselect_b32 s65, s42, s48
	s_ashr_i32 s37, s36, 31
	s_lshl_b64 s[4:5], s[36:37], 19
	s_add_u32 s44, s8, s4
	s_addc_u32 s45, s9, s5
	s_and_b64 s[4:5], s[38:39], exec
	s_cselect_b32 s37, s45, s51
	s_cselect_b32 s68, s44, s50
	s_add_u32 s69, s65, 0x80
	s_addc_u32 s70, s41, 0
	s_add_u32 s4, s48, 0x40080
	s_addc_u32 s5, s49, 0
	s_add_u32 s71, s50, 0x100
	v_lshl_add_u64 v[140:141], s[4:5], 0, v[136:137]
	v_lshl_add_u64 v[142:143], s[4:5], 0, v[138:139]
	s_addc_u32 s72, s51, 0
	s_mov_b32 s73, -2
	s_mov_b64 s[50:51], 0
	s_waitcnt vmcnt(0)
	s_add_u32 s4, s48, s50
	s_addc_u32 s5, s49, s51
	s_add_u32 s74, s4, 0x100
	s_addc_u32 s75, s5, 0
	s_add_u32 s52, s71, s50
	s_addc_u32 s53, s72, s51
	s_add_u32 s4, s4, 0x180
	s_addc_u32 s5, s5, 0
	s_add_i32 s76, 0, 0x10000
	s_add_i32 s77, 0, 0x14000
	v_add_u32_e32 v2, s76, v203
	ds_read_b128 v[144:147], v2
	ds_read_b128 v[148:151], v2 offset:1024
	ds_read_b128 v[152:155], v2 offset:2048
	ds_read_b128 v[156:159], v2 offset:3072
	v_add_u32_e32 v2, s77, v203
	ds_read_b128 v[160:163], v2
	ds_read_b128 v[164:167], v2 offset:1024
	ds_read_b128 v[168:171], v2 offset:2048
	ds_read_b128 v[172:175], v2 offset:3072
	s_cmpk_eq_i32 s50, 0x700
	s_cselect_b32 s13, s70, s5
	s_cselect_b32 s12, s69, s4
	s_cselect_b32 s53, s37, s53
	s_cselect_b32 s52, s68, s52
	s_cselect_b32 s5, s41, s75
	s_cselect_b32 s4, s65, s74
	v_lshl_add_u64 v[212:213], v[140:141], 0, s[50:51]
	s_add_i32 m0, s17, 0xc000
	ds_read_b128 v[176:179], v224
	ds_read_b128 v[180:183], v224 offset:1024
	ds_read_b128 v[184:187], v224 offset:2048
	ds_read_b128 v[188:191], v224 offset:3072
	ds_read_b128 v[192:195], v224 offset:4096
	ds_read_b128 v[196:199], v224 offset:5120
	ds_read_b128 v[204:207], v224 offset:6144
	ds_read_b128 v[208:211], v224 offset:7168
	global_load_lds_dwordx4 v[212:213], off
	v_lshl_add_u64 v[212:213], v[142:143], 0, s[50:51]
	s_add_i32 m0, s17, 0xe000
	s_nop 0
	global_load_lds_dwordx4 v[212:213], off
	s_waitcnt vmcnt(8)
	s_waitcnt lgkmcnt(0)
	s_barrier
	s_setprio 1
	v_mfma_f32_16x16x32_bf16 v[128:131], v[144:147], v[176:179], 0
	v_mfma_f32_16x16x32_bf16 v[124:127], v[152:155], v[176:179], 0
	v_mfma_f32_16x16x32_bf16 v[112:115], v[144:147], v[184:187], 0
	v_mfma_f32_16x16x32_bf16 v[108:111], v[152:155], v[184:187], 0
	v_mfma_f32_16x16x32_bf16 v[96:99], v[144:147], v[192:195], 0
	v_mfma_f32_16x16x32_bf16 v[92:95], v[152:155], v[192:195], 0
	v_mfma_f32_16x16x32_bf16 v[80:83], v[144:147], v[204:207], 0
	v_mfma_f32_16x16x32_bf16 v[76:79], v[152:155], v[204:207], 0
	v_mfma_f32_16x16x32_bf16 v[128:131], v[148:151], v[180:183], v[128:131]
	v_mfma_f32_16x16x32_bf16 v[124:127], v[156:159], v[180:183], v[124:127]
	v_mfma_f32_16x16x32_bf16 v[112:115], v[148:151], v[188:191], v[112:115]
	v_mfma_f32_16x16x32_bf16 v[108:111], v[156:159], v[188:191], v[108:111]
	v_mfma_f32_16x16x32_bf16 v[96:99], v[148:151], v[196:199], v[96:99]
	v_mfma_f32_16x16x32_bf16 v[92:95], v[156:159], v[196:199], v[92:95]
	v_mfma_f32_16x16x32_bf16 v[80:83], v[148:151], v[208:211], v[80:83]
	v_mfma_f32_16x16x32_bf16 v[76:79], v[156:159], v[208:211], v[76:79]
	v_mfma_f32_16x16x32_bf16 v[120:123], v[160:163], v[176:179], 0
	v_mfma_f32_16x16x32_bf16 v[116:119], v[168:171], v[176:179], 0
	v_mfma_f32_16x16x32_bf16 v[104:107], v[160:163], v[184:187], 0
	v_mfma_f32_16x16x32_bf16 v[100:103], v[168:171], v[184:187], 0
	v_mfma_f32_16x16x32_bf16 v[88:91], v[160:163], v[192:195], 0
	v_mfma_f32_16x16x32_bf16 v[84:87], v[168:171], v[192:195], 0
	v_mfma_f32_16x16x32_bf16 v[72:75], v[160:163], v[204:207], 0
	v_mfma_f32_16x16x32_bf16 v[68:71], v[168:171], v[204:207], 0
	v_mfma_f32_16x16x32_bf16 v[120:123], v[164:167], v[180:183], v[120:123]
	v_mfma_f32_16x16x32_bf16 v[116:119], v[172:175], v[180:183], v[116:119]
	v_mfma_f32_16x16x32_bf16 v[104:107], v[164:167], v[188:191], v[104:107]
	v_mfma_f32_16x16x32_bf16 v[100:103], v[172:175], v[188:191], v[100:103]
	v_mfma_f32_16x16x32_bf16 v[88:91], v[164:167], v[196:199], v[88:91]
	v_mfma_f32_16x16x32_bf16 v[84:87], v[172:175], v[196:199], v[84:87]
	v_mfma_f32_16x16x32_bf16 v[72:75], v[164:167], v[208:211], v[72:75]
	v_mfma_f32_16x16x32_bf16 v[68:71], v[172:175], v[208:211], v[68:71]
	s_setprio 0
	s_barrier
	s_add_i32 s74, s76, s16
	v_lshl_add_u64 v[212:213], s[52:53], 0, v[134:135]
	s_mov_b32 m0, s74
	ds_read_b128 v[176:179], v224 offset:16384
	ds_read_b128 v[180:183], v224 offset:17408
	ds_read_b128 v[184:187], v224 offset:18432
	ds_read_b128 v[188:191], v224 offset:19456
	ds_read_b128 v[192:195], v224 offset:20480
	ds_read_b128 v[196:199], v224 offset:21504
	ds_read_b128 v[204:207], v224 offset:22528
	ds_read_b128 v[208:211], v224 offset:23552
	global_load_lds_dwordx4 v[212:213], off
	s_add_i32 m0, s74, 0x2000
	s_add_u32 s74, s52, 0x40000
	v_lshl_add_u64 v[214:215], s[52:53], 0, v[132:133]
	s_addc_u32 s75, s53, 0
	s_add_i32 s76, s77, s16
	global_load_lds_dwordx4 v[214:215], off
	v_lshl_add_u64 v[216:217], s[74:75], 0, v[134:135]
	s_mov_b32 m0, s76
	s_nop 0
	global_load_lds_dwordx4 v[216:217], off
	v_lshl_add_u64 v[216:217], s[74:75], 0, v[132:133]
	s_add_i32 m0, s76, 0x2000
	s_nop 0
	global_load_lds_dwordx4 v[216:217], off
	v_lshl_add_u64 v[216:217], s[4:5], 0, v[134:135]
	s_mov_b32 m0, s17
	s_nop 0
	global_load_lds_dwordx4 v[216:217], off
	v_lshl_add_u64 v[216:217], s[4:5], 0, v[132:133]
	s_mov_b32 m0, s46
	s_nop 0
	global_load_lds_dwordx4 v[216:217], off
	s_waitcnt vmcnt(8)
	s_waitcnt lgkmcnt(0)
	s_barrier
	s_setprio 1
	v_mfma_f32_16x16x32_bf16 v[64:67], v[144:147], v[176:179], 0
	v_mfma_f32_16x16x32_bf16 v[60:63], v[152:155], v[176:179], 0
	v_mfma_f32_16x16x32_bf16 v[48:51], v[144:147], v[184:187], 0
	v_mfma_f32_16x16x32_bf16 v[44:47], v[152:155], v[184:187], 0
	v_mfma_f32_16x16x32_bf16 v[32:35], v[144:147], v[192:195], 0
	v_mfma_f32_16x16x32_bf16 v[28:31], v[152:155], v[192:195], 0
	v_mfma_f32_16x16x32_bf16 v[16:19], v[144:147], v[204:207], 0
	v_mfma_f32_16x16x32_bf16 v[12:15], v[152:155], v[204:207], 0
	v_mfma_f32_16x16x32_bf16 v[64:67], v[148:151], v[180:183], v[64:67]
	v_mfma_f32_16x16x32_bf16 v[60:63], v[156:159], v[180:183], v[60:63]
	v_mfma_f32_16x16x32_bf16 v[48:51], v[148:151], v[188:191], v[48:51]
	v_mfma_f32_16x16x32_bf16 v[44:47], v[156:159], v[188:191], v[44:47]
	v_mfma_f32_16x16x32_bf16 v[32:35], v[148:151], v[196:199], v[32:35]
	v_mfma_f32_16x16x32_bf16 v[28:31], v[156:159], v[196:199], v[28:31]
	v_mfma_f32_16x16x32_bf16 v[16:19], v[148:151], v[208:211], v[16:19]
	v_mfma_f32_16x16x32_bf16 v[12:15], v[156:159], v[208:211], v[12:15]
	v_mfma_f32_16x16x32_bf16 v[56:59], v[160:163], v[176:179], 0
	v_mfma_f32_16x16x32_bf16 v[52:55], v[168:171], v[176:179], 0
	v_mfma_f32_16x16x32_bf16 v[40:43], v[160:163], v[184:187], 0
	v_mfma_f32_16x16x32_bf16 v[36:39], v[168:171], v[184:187], 0
	v_mfma_f32_16x16x32_bf16 v[24:27], v[160:163], v[192:195], 0
	v_mfma_f32_16x16x32_bf16 v[20:23], v[168:171], v[192:195], 0
	v_mfma_f32_16x16x32_bf16 v[8:11], v[160:163], v[204:207], 0
	v_mfma_f32_16x16x32_bf16 v[4:7], v[168:171], v[204:207], 0
	v_mfma_f32_16x16x32_bf16 v[56:59], v[164:167], v[180:183], v[56:59]
	v_mfma_f32_16x16x32_bf16 v[52:55], v[172:175], v[180:183], v[52:55]
	v_mfma_f32_16x16x32_bf16 v[40:43], v[164:167], v[188:191], v[40:43]
	v_mfma_f32_16x16x32_bf16 v[36:39], v[172:175], v[188:191], v[36:39]
	v_mfma_f32_16x16x32_bf16 v[24:27], v[164:167], v[196:199], v[24:27]
	v_mfma_f32_16x16x32_bf16 v[20:23], v[172:175], v[196:199], v[20:23]
	v_mfma_f32_16x16x32_bf16 v[8:11], v[164:167], v[208:211], v[8:11]
	v_mfma_f32_16x16x32_bf16 v[4:7], v[172:175], v[208:211], v[4:7]
	s_setprio 0
	s_barrier
	s_add_i32 s74, 0, 0x18000
	v_add_u32_e32 v2, s74, v203
	s_add_i32 s75, 0, 0x1c000
	ds_read_b128 v[144:147], v2
	ds_read_b128 v[148:151], v2 offset:1024
	ds_read_b128 v[152:155], v2 offset:2048
	ds_read_b128 v[156:159], v2 offset:3072
	v_add_u32_e32 v2, s75, v203
	ds_read_b128 v[160:163], v2
	ds_read_b128 v[164:167], v2 offset:1024
	ds_read_b128 v[168:171], v2 offset:2048
	ds_read_b128 v[172:175], v2 offset:3072
	s_add_u32 s4, s4, 0x40000
	s_addc_u32 s5, s5, 0
	s_mov_b32 m0, s47
	v_lshl_add_u64 v[216:217], s[4:5], 0, v[134:135]
	ds_read_b128 v[176:179], v224 offset:32768
	ds_read_b128 v[180:183], v224 offset:33792
	ds_read_b128 v[184:187], v224 offset:34816
	ds_read_b128 v[188:191], v224 offset:35840
	ds_read_b128 v[192:195], v224 offset:36864
	ds_read_b128 v[196:199], v224 offset:37888
	ds_read_b128 v[204:207], v224 offset:38912
	ds_read_b128 v[208:211], v224 offset:39936
	global_load_lds_dwordx4 v[216:217], off
	v_lshl_add_u64 v[216:217], s[4:5], 0, v[132:133]
	s_mov_b32 m0, s56
	s_nop 0
	global_load_lds_dwordx4 v[216:217], off
	s_waitcnt vmcnt(8)
	s_waitcnt lgkmcnt(0)
	s_barrier
	s_setprio 1
	v_mfma_f32_16x16x32_bf16 v[128:131], v[144:147], v[176:179], v[128:131]
	v_mfma_f32_16x16x32_bf16 v[124:127], v[152:155], v[176:179], v[124:127]
	v_mfma_f32_16x16x32_bf16 v[112:115], v[144:147], v[184:187], v[112:115]
	v_mfma_f32_16x16x32_bf16 v[108:111], v[152:155], v[184:187], v[108:111]
	v_mfma_f32_16x16x32_bf16 v[96:99], v[144:147], v[192:195], v[96:99]
	v_mfma_f32_16x16x32_bf16 v[92:95], v[152:155], v[192:195], v[92:95]
	v_mfma_f32_16x16x32_bf16 v[80:83], v[144:147], v[204:207], v[80:83]
	v_mfma_f32_16x16x32_bf16 v[76:79], v[152:155], v[204:207], v[76:79]
	v_mfma_f32_16x16x32_bf16 v[128:131], v[148:151], v[180:183], v[128:131]
	v_mfma_f32_16x16x32_bf16 v[124:127], v[156:159], v[180:183], v[124:127]
	v_mfma_f32_16x16x32_bf16 v[112:115], v[148:151], v[188:191], v[112:115]
	v_mfma_f32_16x16x32_bf16 v[108:111], v[156:159], v[188:191], v[108:111]
	v_mfma_f32_16x16x32_bf16 v[96:99], v[148:151], v[196:199], v[96:99]
	v_mfma_f32_16x16x32_bf16 v[92:95], v[156:159], v[196:199], v[92:95]
	v_mfma_f32_16x16x32_bf16 v[80:83], v[148:151], v[208:211], v[80:83]
	v_mfma_f32_16x16x32_bf16 v[76:79], v[156:159], v[208:211], v[76:79]
	v_mfma_f32_16x16x32_bf16 v[120:123], v[160:163], v[176:179], v[120:123]
	v_mfma_f32_16x16x32_bf16 v[116:119], v[168:171], v[176:179], v[116:119]
	v_mfma_f32_16x16x32_bf16 v[104:107], v[160:163], v[184:187], v[104:107]
	v_mfma_f32_16x16x32_bf16 v[100:103], v[168:171], v[184:187], v[100:103]
	v_mfma_f32_16x16x32_bf16 v[88:91], v[160:163], v[192:195], v[88:91]
	v_mfma_f32_16x16x32_bf16 v[84:87], v[168:171], v[192:195], v[84:87]
	v_mfma_f32_16x16x32_bf16 v[72:75], v[160:163], v[204:207], v[72:75]
	v_mfma_f32_16x16x32_bf16 v[68:71], v[168:171], v[204:207], v[68:71]
	v_mfma_f32_16x16x32_bf16 v[120:123], v[164:167], v[180:183], v[120:123]
	v_mfma_f32_16x16x32_bf16 v[116:119], v[172:175], v[180:183], v[116:119]
	v_mfma_f32_16x16x32_bf16 v[104:107], v[164:167], v[188:191], v[104:107]
	v_mfma_f32_16x16x32_bf16 v[100:103], v[172:175], v[188:191], v[100:103]
	v_mfma_f32_16x16x32_bf16 v[88:91], v[164:167], v[196:199], v[88:91]
	v_mfma_f32_16x16x32_bf16 v[84:87], v[172:175], v[196:199], v[84:87]
	v_mfma_f32_16x16x32_bf16 v[72:75], v[164:167], v[208:211], v[72:75]
	v_mfma_f32_16x16x32_bf16 v[68:71], v[172:175], v[208:211], v[68:71]
	s_setprio 0
	s_barrier
	s_add_i32 s4, s74, s16
	v_lshl_add_u64 v[212:213], v[212:213], 0, s[34:35]
	s_mov_b32 m0, s4
	ds_read_b128 v[176:179], v224 offset:49152
	ds_read_b128 v[180:183], v224 offset:50176
	ds_read_b128 v[184:187], v224 offset:51200
	ds_read_b128 v[188:191], v224 offset:52224
	ds_read_b128 v[192:195], v224 offset:53248
	ds_read_b128 v[196:199], v224 offset:54272
	ds_read_b128 v[204:207], v224 offset:55296
	ds_read_b128 v[208:211], v224 offset:56320
	global_load_lds_dwordx4 v[212:213], off
	s_add_i32 m0, s4, 0x2000
	s_add_u32 s4, s52, 0x40080
	v_lshl_add_u64 v[212:213], v[214:215], 0, s[34:35]
	s_addc_u32 s5, s53, 0
	s_add_i32 s52, s75, s16
	global_load_lds_dwordx4 v[212:213], off
	v_lshl_add_u64 v[212:213], s[4:5], 0, v[134:135]
	s_mov_b32 m0, s52
	s_nop 0
	global_load_lds_dwordx4 v[212:213], off
	v_lshl_add_u64 v[212:213], s[4:5], 0, v[132:133]
	s_add_i32 m0, s52, 0x2000
	s_nop 0
	global_load_lds_dwordx4 v[212:213], off
	v_lshl_add_u64 v[212:213], s[12:13], 0, v[134:135]
	s_mov_b32 m0, s59
	s_nop 0
	global_load_lds_dwordx4 v[212:213], off
	v_lshl_add_u64 v[212:213], s[12:13], 0, v[132:133]
	s_mov_b32 m0, s60
	s_nop 0
	global_load_lds_dwordx4 v[212:213], off
	s_waitcnt vmcnt(8)
	s_waitcnt lgkmcnt(0)
	s_barrier
	s_setprio 1
	v_mfma_f32_16x16x32_bf16 v[64:67], v[144:147], v[176:179], v[64:67]
	v_mfma_f32_16x16x32_bf16 v[60:63], v[152:155], v[176:179], v[60:63]
	v_mfma_f32_16x16x32_bf16 v[48:51], v[144:147], v[184:187], v[48:51]
	v_mfma_f32_16x16x32_bf16 v[44:47], v[152:155], v[184:187], v[44:47]
	v_mfma_f32_16x16x32_bf16 v[32:35], v[144:147], v[192:195], v[32:35]
	v_mfma_f32_16x16x32_bf16 v[28:31], v[152:155], v[192:195], v[28:31]
	v_mfma_f32_16x16x32_bf16 v[16:19], v[144:147], v[204:207], v[16:19]
	v_mfma_f32_16x16x32_bf16 v[12:15], v[152:155], v[204:207], v[12:15]
	v_mfma_f32_16x16x32_bf16 v[64:67], v[148:151], v[180:183], v[64:67]
	v_mfma_f32_16x16x32_bf16 v[60:63], v[156:159], v[180:183], v[60:63]
	v_mfma_f32_16x16x32_bf16 v[48:51], v[148:151], v[188:191], v[48:51]
	v_mfma_f32_16x16x32_bf16 v[44:47], v[156:159], v[188:191], v[44:47]
	v_mfma_f32_16x16x32_bf16 v[32:35], v[148:151], v[196:199], v[32:35]
	v_mfma_f32_16x16x32_bf16 v[28:31], v[156:159], v[196:199], v[28:31]
	v_mfma_f32_16x16x32_bf16 v[16:19], v[148:151], v[208:211], v[16:19]
	v_mfma_f32_16x16x32_bf16 v[12:15], v[156:159], v[208:211], v[12:15]
	v_mfma_f32_16x16x32_bf16 v[56:59], v[160:163], v[176:179], v[56:59]
	v_mfma_f32_16x16x32_bf16 v[52:55], v[168:171], v[176:179], v[52:55]
	v_mfma_f32_16x16x32_bf16 v[40:43], v[160:163], v[184:187], v[40:43]
	v_mfma_f32_16x16x32_bf16 v[36:39], v[168:171], v[184:187], v[36:39]
	v_mfma_f32_16x16x32_bf16 v[24:27], v[160:163], v[192:195], v[24:27]
	v_mfma_f32_16x16x32_bf16 v[20:23], v[168:171], v[192:195], v[20:23]
	v_mfma_f32_16x16x32_bf16 v[8:11], v[160:163], v[204:207], v[8:11]
	v_mfma_f32_16x16x32_bf16 v[4:7], v[168:171], v[204:207], v[4:7]
	v_mfma_f32_16x16x32_bf16 v[56:59], v[164:167], v[180:183], v[56:59]
	v_mfma_f32_16x16x32_bf16 v[52:55], v[172:175], v[180:183], v[52:55]
	v_mfma_f32_16x16x32_bf16 v[40:43], v[164:167], v[188:191], v[40:43]
	v_mfma_f32_16x16x32_bf16 v[36:39], v[172:175], v[188:191], v[36:39]
	v_mfma_f32_16x16x32_bf16 v[24:27], v[164:167], v[196:199], v[24:27]
	v_mfma_f32_16x16x32_bf16 v[20:23], v[172:175], v[196:199], v[20:23]
	v_mfma_f32_16x16x32_bf16 v[8:11], v[164:167], v[208:211], v[8:11]
	v_mfma_f32_16x16x32_bf16 v[4:7], v[172:175], v[208:211], v[4:7]
	s_setprio 0
	s_barrier
	s_add_i32 s73, s73, 2
	s_add_u32 s50, s50, 0x100
	s_addc_u32 s51, s51, 0
	s_cmp_gt_u32 s73, 13
.LBB0_1044:
	s_add_u32 s4, s48, s50
	s_addc_u32 s5, s49, s51
	s_add_u32 s74, s4, 0x100
	s_addc_u32 s75, s5, 0
	s_add_u32 s52, s71, s50
	s_addc_u32 s53, s72, s51
	s_add_u32 s4, s4, 0x180
	s_addc_u32 s5, s5, 0
	s_add_i32 s76, 0, 0x10000
	s_add_i32 s77, 0, 0x14000
	v_add_u32_e32 v2, s76, v203
	ds_read_b128 v[144:147], v2
	ds_read_b128 v[148:151], v2 offset:1024
	ds_read_b128 v[152:155], v2 offset:2048
	ds_read_b128 v[156:159], v2 offset:3072
	v_add_u32_e32 v2, s77, v203
	ds_read_b128 v[160:163], v2
	ds_read_b128 v[164:167], v2 offset:1024
	ds_read_b128 v[168:171], v2 offset:2048
	ds_read_b128 v[172:175], v2 offset:3072
	s_cmpk_eq_i32 s50, 0x700
	s_cselect_b32 s13, s70, s5
	s_cselect_b32 s12, s69, s4
	s_cselect_b32 s53, s37, s53
	s_cselect_b32 s52, s68, s52
	s_cselect_b32 s5, s41, s75
	s_cselect_b32 s4, s65, s74
	v_lshl_add_u64 v[212:213], v[140:141], 0, s[50:51]
	s_add_i32 m0, s17, 0xc000
	ds_read_b128 v[176:179], v224
	ds_read_b128 v[180:183], v224 offset:1024
	ds_read_b128 v[184:187], v224 offset:2048
	ds_read_b128 v[188:191], v224 offset:3072
	ds_read_b128 v[192:195], v224 offset:4096
	ds_read_b128 v[196:199], v224 offset:5120
	ds_read_b128 v[204:207], v224 offset:6144
	ds_read_b128 v[208:211], v224 offset:7168
	global_load_lds_dwordx4 v[212:213], off
	v_lshl_add_u64 v[212:213], v[142:143], 0, s[50:51]
	s_add_i32 m0, s17, 0xe000
	s_nop 0
	global_load_lds_dwordx4 v[212:213], off
	s_waitcnt vmcnt(8)
	s_waitcnt lgkmcnt(0)
	s_barrier
	s_setprio 1
	v_mfma_f32_16x16x32_bf16 v[128:131], v[144:147], v[176:179], v[128:131]
	v_mfma_f32_16x16x32_bf16 v[124:127], v[152:155], v[176:179], v[124:127]
	v_mfma_f32_16x16x32_bf16 v[112:115], v[144:147], v[184:187], v[112:115]
	v_mfma_f32_16x16x32_bf16 v[108:111], v[152:155], v[184:187], v[108:111]
	v_mfma_f32_16x16x32_bf16 v[96:99], v[144:147], v[192:195], v[96:99]
	v_mfma_f32_16x16x32_bf16 v[92:95], v[152:155], v[192:195], v[92:95]
	v_mfma_f32_16x16x32_bf16 v[80:83], v[144:147], v[204:207], v[80:83]
	v_mfma_f32_16x16x32_bf16 v[76:79], v[152:155], v[204:207], v[76:79]
	v_mfma_f32_16x16x32_bf16 v[128:131], v[148:151], v[180:183], v[128:131]
	v_mfma_f32_16x16x32_bf16 v[124:127], v[156:159], v[180:183], v[124:127]
	v_mfma_f32_16x16x32_bf16 v[112:115], v[148:151], v[188:191], v[112:115]
	v_mfma_f32_16x16x32_bf16 v[108:111], v[156:159], v[188:191], v[108:111]
	v_mfma_f32_16x16x32_bf16 v[96:99], v[148:151], v[196:199], v[96:99]
	v_mfma_f32_16x16x32_bf16 v[92:95], v[156:159], v[196:199], v[92:95]
	v_mfma_f32_16x16x32_bf16 v[80:83], v[148:151], v[208:211], v[80:83]
	v_mfma_f32_16x16x32_bf16 v[76:79], v[156:159], v[208:211], v[76:79]
	v_mfma_f32_16x16x32_bf16 v[120:123], v[160:163], v[176:179], v[120:123]
	v_mfma_f32_16x16x32_bf16 v[116:119], v[168:171], v[176:179], v[116:119]
	v_mfma_f32_16x16x32_bf16 v[104:107], v[160:163], v[184:187], v[104:107]
	v_mfma_f32_16x16x32_bf16 v[100:103], v[168:171], v[184:187], v[100:103]
	v_mfma_f32_16x16x32_bf16 v[88:91], v[160:163], v[192:195], v[88:91]
	v_mfma_f32_16x16x32_bf16 v[84:87], v[168:171], v[192:195], v[84:87]
	v_mfma_f32_16x16x32_bf16 v[72:75], v[160:163], v[204:207], v[72:75]
	v_mfma_f32_16x16x32_bf16 v[68:71], v[168:171], v[204:207], v[68:71]
	v_mfma_f32_16x16x32_bf16 v[120:123], v[164:167], v[180:183], v[120:123]
	v_mfma_f32_16x16x32_bf16 v[116:119], v[172:175], v[180:183], v[116:119]
	v_mfma_f32_16x16x32_bf16 v[104:107], v[164:167], v[188:191], v[104:107]
	v_mfma_f32_16x16x32_bf16 v[100:103], v[172:175], v[188:191], v[100:103]
	v_mfma_f32_16x16x32_bf16 v[88:91], v[164:167], v[196:199], v[88:91]
	v_mfma_f32_16x16x32_bf16 v[84:87], v[172:175], v[196:199], v[84:87]
	v_mfma_f32_16x16x32_bf16 v[72:75], v[164:167], v[208:211], v[72:75]
	v_mfma_f32_16x16x32_bf16 v[68:71], v[172:175], v[208:211], v[68:71]
	s_setprio 0
	s_barrier
	s_add_i32 s74, s76, s16
	v_lshl_add_u64 v[212:213], s[52:53], 0, v[134:135]
	s_mov_b32 m0, s74
	ds_read_b128 v[176:179], v224 offset:16384
	ds_read_b128 v[180:183], v224 offset:17408
	ds_read_b128 v[184:187], v224 offset:18432
	ds_read_b128 v[188:191], v224 offset:19456
	ds_read_b128 v[192:195], v224 offset:20480
	ds_read_b128 v[196:199], v224 offset:21504
	ds_read_b128 v[204:207], v224 offset:22528
	ds_read_b128 v[208:211], v224 offset:23552
	global_load_lds_dwordx4 v[212:213], off
	s_add_i32 m0, s74, 0x2000
	s_add_u32 s74, s52, 0x40000
	v_lshl_add_u64 v[214:215], s[52:53], 0, v[132:133]
	s_addc_u32 s75, s53, 0
	s_add_i32 s76, s77, s16
	global_load_lds_dwordx4 v[214:215], off
	v_lshl_add_u64 v[216:217], s[74:75], 0, v[134:135]
	s_mov_b32 m0, s76
	s_nop 0
	global_load_lds_dwordx4 v[216:217], off
	v_lshl_add_u64 v[216:217], s[74:75], 0, v[132:133]
	s_add_i32 m0, s76, 0x2000
	s_nop 0
	global_load_lds_dwordx4 v[216:217], off
	v_lshl_add_u64 v[216:217], s[4:5], 0, v[134:135]
	s_mov_b32 m0, s17
	s_nop 0
	global_load_lds_dwordx4 v[216:217], off
	v_lshl_add_u64 v[216:217], s[4:5], 0, v[132:133]
	s_mov_b32 m0, s46
	s_nop 0
	global_load_lds_dwordx4 v[216:217], off
	s_waitcnt vmcnt(8)
	s_waitcnt lgkmcnt(0)
	s_barrier
	s_setprio 1
	v_mfma_f32_16x16x32_bf16 v[64:67], v[144:147], v[176:179], v[64:67]
	v_mfma_f32_16x16x32_bf16 v[60:63], v[152:155], v[176:179], v[60:63]
	v_mfma_f32_16x16x32_bf16 v[48:51], v[144:147], v[184:187], v[48:51]
	v_mfma_f32_16x16x32_bf16 v[44:47], v[152:155], v[184:187], v[44:47]
	v_mfma_f32_16x16x32_bf16 v[32:35], v[144:147], v[192:195], v[32:35]
	v_mfma_f32_16x16x32_bf16 v[28:31], v[152:155], v[192:195], v[28:31]
	v_mfma_f32_16x16x32_bf16 v[16:19], v[144:147], v[204:207], v[16:19]
	v_mfma_f32_16x16x32_bf16 v[12:15], v[152:155], v[204:207], v[12:15]
	v_mfma_f32_16x16x32_bf16 v[64:67], v[148:151], v[180:183], v[64:67]
	v_mfma_f32_16x16x32_bf16 v[60:63], v[156:159], v[180:183], v[60:63]
	v_mfma_f32_16x16x32_bf16 v[48:51], v[148:151], v[188:191], v[48:51]
	v_mfma_f32_16x16x32_bf16 v[44:47], v[156:159], v[188:191], v[44:47]
	v_mfma_f32_16x16x32_bf16 v[32:35], v[148:151], v[196:199], v[32:35]
	v_mfma_f32_16x16x32_bf16 v[28:31], v[156:159], v[196:199], v[28:31]
	v_mfma_f32_16x16x32_bf16 v[16:19], v[148:151], v[208:211], v[16:19]
	v_mfma_f32_16x16x32_bf16 v[12:15], v[156:159], v[208:211], v[12:15]
	v_mfma_f32_16x16x32_bf16 v[56:59], v[160:163], v[176:179], v[56:59]
	v_mfma_f32_16x16x32_bf16 v[52:55], v[168:171], v[176:179], v[52:55]
	v_mfma_f32_16x16x32_bf16 v[40:43], v[160:163], v[184:187], v[40:43]
	v_mfma_f32_16x16x32_bf16 v[36:39], v[168:171], v[184:187], v[36:39]
	v_mfma_f32_16x16x32_bf16 v[24:27], v[160:163], v[192:195], v[24:27]
	v_mfma_f32_16x16x32_bf16 v[20:23], v[168:171], v[192:195], v[20:23]
	v_mfma_f32_16x16x32_bf16 v[8:11], v[160:163], v[204:207], v[8:11]
	v_mfma_f32_16x16x32_bf16 v[4:7], v[168:171], v[204:207], v[4:7]
	v_mfma_f32_16x16x32_bf16 v[56:59], v[164:167], v[180:183], v[56:59]
	v_mfma_f32_16x16x32_bf16 v[52:55], v[172:175], v[180:183], v[52:55]
	v_mfma_f32_16x16x32_bf16 v[40:43], v[164:167], v[188:191], v[40:43]
	v_mfma_f32_16x16x32_bf16 v[36:39], v[172:175], v[188:191], v[36:39]
	v_mfma_f32_16x16x32_bf16 v[24:27], v[164:167], v[196:199], v[24:27]
	v_mfma_f32_16x16x32_bf16 v[20:23], v[172:175], v[196:199], v[20:23]
	v_mfma_f32_16x16x32_bf16 v[8:11], v[164:167], v[208:211], v[8:11]
	v_mfma_f32_16x16x32_bf16 v[4:7], v[172:175], v[208:211], v[4:7]
	s_setprio 0
	s_barrier
	s_add_i32 s74, 0, 0x18000
	v_add_u32_e32 v2, s74, v203
	s_add_i32 s75, 0, 0x1c000
	ds_read_b128 v[144:147], v2
	ds_read_b128 v[148:151], v2 offset:1024
	ds_read_b128 v[152:155], v2 offset:2048
	ds_read_b128 v[156:159], v2 offset:3072
	v_add_u32_e32 v2, s75, v203
	ds_read_b128 v[160:163], v2
	ds_read_b128 v[164:167], v2 offset:1024
	ds_read_b128 v[168:171], v2 offset:2048
	ds_read_b128 v[172:175], v2 offset:3072
	s_add_u32 s4, s4, 0x40000
	s_addc_u32 s5, s5, 0
	s_mov_b32 m0, s47
	v_lshl_add_u64 v[216:217], s[4:5], 0, v[134:135]
	ds_read_b128 v[176:179], v224 offset:32768
	ds_read_b128 v[180:183], v224 offset:33792
	ds_read_b128 v[184:187], v224 offset:34816
	ds_read_b128 v[188:191], v224 offset:35840
	ds_read_b128 v[192:195], v224 offset:36864
	ds_read_b128 v[196:199], v224 offset:37888
	ds_read_b128 v[204:207], v224 offset:38912
	ds_read_b128 v[208:211], v224 offset:39936
	global_load_lds_dwordx4 v[216:217], off
	v_lshl_add_u64 v[216:217], s[4:5], 0, v[132:133]
	s_mov_b32 m0, s56
	s_nop 0
	global_load_lds_dwordx4 v[216:217], off
	s_waitcnt vmcnt(8)
	s_waitcnt lgkmcnt(0)
	s_barrier
	s_setprio 1
	v_mfma_f32_16x16x32_bf16 v[128:131], v[144:147], v[176:179], v[128:131]
	v_mfma_f32_16x16x32_bf16 v[124:127], v[152:155], v[176:179], v[124:127]
	v_mfma_f32_16x16x32_bf16 v[112:115], v[144:147], v[184:187], v[112:115]
	v_mfma_f32_16x16x32_bf16 v[108:111], v[152:155], v[184:187], v[108:111]
	v_mfma_f32_16x16x32_bf16 v[96:99], v[144:147], v[192:195], v[96:99]
	v_mfma_f32_16x16x32_bf16 v[92:95], v[152:155], v[192:195], v[92:95]
	v_mfma_f32_16x16x32_bf16 v[80:83], v[144:147], v[204:207], v[80:83]
	v_mfma_f32_16x16x32_bf16 v[76:79], v[152:155], v[204:207], v[76:79]
	v_mfma_f32_16x16x32_bf16 v[128:131], v[148:151], v[180:183], v[128:131]
	v_mfma_f32_16x16x32_bf16 v[124:127], v[156:159], v[180:183], v[124:127]
	v_mfma_f32_16x16x32_bf16 v[112:115], v[148:151], v[188:191], v[112:115]
	v_mfma_f32_16x16x32_bf16 v[108:111], v[156:159], v[188:191], v[108:111]
	v_mfma_f32_16x16x32_bf16 v[96:99], v[148:151], v[196:199], v[96:99]
	v_mfma_f32_16x16x32_bf16 v[92:95], v[156:159], v[196:199], v[92:95]
	v_mfma_f32_16x16x32_bf16 v[80:83], v[148:151], v[208:211], v[80:83]
	v_mfma_f32_16x16x32_bf16 v[76:79], v[156:159], v[208:211], v[76:79]
	v_mfma_f32_16x16x32_bf16 v[120:123], v[160:163], v[176:179], v[120:123]
	v_mfma_f32_16x16x32_bf16 v[116:119], v[168:171], v[176:179], v[116:119]
	v_mfma_f32_16x16x32_bf16 v[104:107], v[160:163], v[184:187], v[104:107]
	v_mfma_f32_16x16x32_bf16 v[100:103], v[168:171], v[184:187], v[100:103]
	v_mfma_f32_16x16x32_bf16 v[88:91], v[160:163], v[192:195], v[88:91]
	v_mfma_f32_16x16x32_bf16 v[84:87], v[168:171], v[192:195], v[84:87]
	v_mfma_f32_16x16x32_bf16 v[72:75], v[160:163], v[204:207], v[72:75]
	v_mfma_f32_16x16x32_bf16 v[68:71], v[168:171], v[204:207], v[68:71]
	v_mfma_f32_16x16x32_bf16 v[120:123], v[164:167], v[180:183], v[120:123]
	v_mfma_f32_16x16x32_bf16 v[116:119], v[172:175], v[180:183], v[116:119]
	v_mfma_f32_16x16x32_bf16 v[104:107], v[164:167], v[188:191], v[104:107]
	v_mfma_f32_16x16x32_bf16 v[100:103], v[172:175], v[188:191], v[100:103]
	v_mfma_f32_16x16x32_bf16 v[88:91], v[164:167], v[196:199], v[88:91]
	v_mfma_f32_16x16x32_bf16 v[84:87], v[172:175], v[196:199], v[84:87]
	v_mfma_f32_16x16x32_bf16 v[72:75], v[164:167], v[208:211], v[72:75]
	v_mfma_f32_16x16x32_bf16 v[68:71], v[172:175], v[208:211], v[68:71]
	s_setprio 0
	s_barrier
	s_add_i32 s4, s74, s16
	v_lshl_add_u64 v[212:213], v[212:213], 0, s[34:35]
	s_mov_b32 m0, s4
	ds_read_b128 v[176:179], v224 offset:49152
	ds_read_b128 v[180:183], v224 offset:50176
	ds_read_b128 v[184:187], v224 offset:51200
	ds_read_b128 v[188:191], v224 offset:52224
	ds_read_b128 v[192:195], v224 offset:53248
	ds_read_b128 v[196:199], v224 offset:54272
	ds_read_b128 v[204:207], v224 offset:55296
	ds_read_b128 v[208:211], v224 offset:56320
	global_load_lds_dwordx4 v[212:213], off
	s_add_i32 m0, s4, 0x2000
	s_add_u32 s4, s52, 0x40080
	v_lshl_add_u64 v[212:213], v[214:215], 0, s[34:35]
	s_addc_u32 s5, s53, 0
	s_add_i32 s52, s75, s16
	global_load_lds_dwordx4 v[212:213], off
	v_lshl_add_u64 v[212:213], s[4:5], 0, v[134:135]
	s_mov_b32 m0, s52
	s_nop 0
	global_load_lds_dwordx4 v[212:213], off
	v_lshl_add_u64 v[212:213], s[4:5], 0, v[132:133]
	s_add_i32 m0, s52, 0x2000
	s_nop 0
	global_load_lds_dwordx4 v[212:213], off
	v_lshl_add_u64 v[212:213], s[12:13], 0, v[134:135]
	s_mov_b32 m0, s59
	s_nop 0
	global_load_lds_dwordx4 v[212:213], off
	v_lshl_add_u64 v[212:213], s[12:13], 0, v[132:133]
	s_mov_b32 m0, s60
	s_nop 0
	global_load_lds_dwordx4 v[212:213], off
	s_waitcnt vmcnt(8)
	s_waitcnt lgkmcnt(0)
	s_barrier
	s_setprio 1
	v_mfma_f32_16x16x32_bf16 v[64:67], v[144:147], v[176:179], v[64:67]
	v_mfma_f32_16x16x32_bf16 v[60:63], v[152:155], v[176:179], v[60:63]
	v_mfma_f32_16x16x32_bf16 v[48:51], v[144:147], v[184:187], v[48:51]
	v_mfma_f32_16x16x32_bf16 v[44:47], v[152:155], v[184:187], v[44:47]
	v_mfma_f32_16x16x32_bf16 v[32:35], v[144:147], v[192:195], v[32:35]
	v_mfma_f32_16x16x32_bf16 v[28:31], v[152:155], v[192:195], v[28:31]
	v_mfma_f32_16x16x32_bf16 v[16:19], v[144:147], v[204:207], v[16:19]
	v_mfma_f32_16x16x32_bf16 v[12:15], v[152:155], v[204:207], v[12:15]
	v_mfma_f32_16x16x32_bf16 v[64:67], v[148:151], v[180:183], v[64:67]
	v_mfma_f32_16x16x32_bf16 v[60:63], v[156:159], v[180:183], v[60:63]
	v_mfma_f32_16x16x32_bf16 v[48:51], v[148:151], v[188:191], v[48:51]
	v_mfma_f32_16x16x32_bf16 v[44:47], v[156:159], v[188:191], v[44:47]
	v_mfma_f32_16x16x32_bf16 v[32:35], v[148:151], v[196:199], v[32:35]
	v_mfma_f32_16x16x32_bf16 v[28:31], v[156:159], v[196:199], v[28:31]
	v_mfma_f32_16x16x32_bf16 v[16:19], v[148:151], v[208:211], v[16:19]
	v_mfma_f32_16x16x32_bf16 v[12:15], v[156:159], v[208:211], v[12:15]
	v_mfma_f32_16x16x32_bf16 v[56:59], v[160:163], v[176:179], v[56:59]
	v_mfma_f32_16x16x32_bf16 v[52:55], v[168:171], v[176:179], v[52:55]
	v_mfma_f32_16x16x32_bf16 v[40:43], v[160:163], v[184:187], v[40:43]
	v_mfma_f32_16x16x32_bf16 v[36:39], v[168:171], v[184:187], v[36:39]
	v_mfma_f32_16x16x32_bf16 v[24:27], v[160:163], v[192:195], v[24:27]
	v_mfma_f32_16x16x32_bf16 v[20:23], v[168:171], v[192:195], v[20:23]
	v_mfma_f32_16x16x32_bf16 v[8:11], v[160:163], v[204:207], v[8:11]
	v_mfma_f32_16x16x32_bf16 v[4:7], v[168:171], v[204:207], v[4:7]
	v_mfma_f32_16x16x32_bf16 v[56:59], v[164:167], v[180:183], v[56:59]
	v_mfma_f32_16x16x32_bf16 v[52:55], v[172:175], v[180:183], v[52:55]
	v_mfma_f32_16x16x32_bf16 v[40:43], v[164:167], v[188:191], v[40:43]
	v_mfma_f32_16x16x32_bf16 v[36:39], v[172:175], v[188:191], v[36:39]
	v_mfma_f32_16x16x32_bf16 v[24:27], v[164:167], v[196:199], v[24:27]
	v_mfma_f32_16x16x32_bf16 v[20:23], v[172:175], v[196:199], v[20:23]
	v_mfma_f32_16x16x32_bf16 v[8:11], v[164:167], v[208:211], v[8:11]
	v_mfma_f32_16x16x32_bf16 v[4:7], v[172:175], v[208:211], v[4:7]
	s_setprio 0
	s_barrier
	s_add_i32 s73, s73, 2
	s_add_u32 s50, s50, 0x100
	s_addc_u32 s51, s51, 0
	s_cmp_gt_u32 s73, 13
	s_cbranch_scc0 .LBB0_1044
	s_and_b64 vcc, exec, s[22:23]
	s_cbranch_vccz .LBB0_1047
	s_barrier

.LBB0_1117:
	s_ashr_i32 s37, s36, 31
	s_lshl_b64 s[4:5], s[36:37], 19
	s_add_u32 s40, s6, s4
	s_addc_u32 s41, s7, s5
	s_and_b64 s[4:5], s[38:39], exec
	s_cselect_b32 s37, s41, s45
	s_cselect_b32 s64, s40, s44
	s_ashr_i32 s23, s22, 31
	s_lshl_b64 s[4:5], s[22:23], 19
	s_add_u32 s42, s8, s4
	s_addc_u32 s43, s9, s5
	s_and_b64 s[4:5], s[38:39], exec
	s_cselect_b32 s23, s43, s49
	s_cselect_b32 s65, s42, s48
	s_add_u32 s68, s64, 0x80
	s_addc_u32 s69, s37, 0
	s_add_u32 s70, s48, 0x100
	s_addc_u32 s71, s49, 0
	s_add_u32 s4, s44, 0x40080
	s_addc_u32 s5, s45, 0
	v_lshl_add_u64 v[108:109], s[4:5], 0, v[210:211]
	v_lshl_add_u64 v[110:111], s[4:5], 0, v[212:213]
	s_mov_b32 s72, -2
	s_mov_b64 s[48:49], 0
	s_waitcnt lgkmcnt(0)
	s_waitcnt vmcnt(0)
	s_add_u32 s4, s44, s48
	s_addc_u32 s5, s45, s49
	s_add_u32 s73, s4, 0x100
	s_addc_u32 s74, s5, 0
	s_add_u32 s50, s70, s48
	s_addc_u32 s51, s71, s49
	s_add_u32 s4, s4, 0x180
	s_addc_u32 s5, s5, 0
	s_add_i32 s75, 0, 0x10000
	s_add_i32 s76, 0, 0x14000
	v_add_u32_e32 v148, s75, v203
	v_add_u32_e32 v164, s76, v203
	ds_read_b128 v[116:119], v148
	ds_read_b128 v[128:131], v148 offset:1024
	ds_read_b128 v[136:139], v148 offset:2048
	ds_read_b128 v[148:151], v148 offset:3072
	ds_read_b128 v[152:155], v164
	ds_read_b128 v[156:159], v164 offset:1024
	ds_read_b128 v[160:163], v164 offset:2048
	ds_read_b128 v[164:167], v164 offset:3072
	s_cmpk_eq_i32 s48, 0x700
	s_cselect_b32 s13, s69, s5
	s_cselect_b32 s12, s68, s4
	s_cselect_b32 s51, s23, s51
	s_cselect_b32 s50, s65, s50
	s_cselect_b32 s5, s37, s74
	s_cselect_b32 s4, s64, s73
	v_lshl_add_u64 v[214:215], v[108:109], 0, s[48:49]
	s_add_i32 m0, s17, 0xc000
	ds_read_b128 v[168:171], v236
	ds_read_b128 v[172:175], v236 offset:1024
	ds_read_b128 v[176:179], v236 offset:2048
	ds_read_b128 v[180:183], v236 offset:3072
	ds_read_b128 v[184:187], v236 offset:4096
	ds_read_b128 v[188:191], v236 offset:5120
	ds_read_b128 v[192:195], v236 offset:6144
	ds_read_b128 v[196:199], v236 offset:7168
	global_load_lds_dwordx4 v[214:215], off
	v_lshl_add_u64 v[214:215], v[110:111], 0, s[48:49]
	s_add_i32 m0, s17, 0xe000
	s_nop 0
	global_load_lds_dwordx4 v[214:215], off
	s_waitcnt vmcnt(8)
	s_waitcnt lgkmcnt(0)
	s_barrier
	s_setprio 1
	v_mfma_f32_16x16x32_bf16 v[144:147], v[116:119], v[168:171], 0
	v_mfma_f32_16x16x32_bf16 v[140:143], v[136:139], v[168:171], 0
	v_mfma_f32_16x16x32_bf16 v[120:123], v[116:119], v[176:179], 0
	v_mfma_f32_16x16x32_bf16 v[112:115], v[136:139], v[176:179], 0
	v_mfma_f32_16x16x32_bf16 v[96:99], v[116:119], v[184:187], 0
	v_mfma_f32_16x16x32_bf16 v[92:95], v[136:139], v[184:187], 0
	v_mfma_f32_16x16x32_bf16 v[80:83], v[116:119], v[192:195], 0
	v_mfma_f32_16x16x32_bf16 v[76:79], v[136:139], v[192:195], 0
	v_mfma_f32_16x16x32_bf16 v[144:147], v[128:131], v[172:175], v[144:147]
	v_mfma_f32_16x16x32_bf16 v[140:143], v[148:151], v[172:175], v[140:143]
	v_mfma_f32_16x16x32_bf16 v[120:123], v[128:131], v[180:183], v[120:123]
	v_mfma_f32_16x16x32_bf16 v[112:115], v[148:151], v[180:183], v[112:115]
	v_mfma_f32_16x16x32_bf16 v[96:99], v[128:131], v[188:191], v[96:99]
	v_mfma_f32_16x16x32_bf16 v[92:95], v[148:151], v[188:191], v[92:95]
	v_mfma_f32_16x16x32_bf16 v[80:83], v[128:131], v[196:199], v[80:83]
	v_mfma_f32_16x16x32_bf16 v[76:79], v[148:151], v[196:199], v[76:79]
	v_mfma_f32_16x16x32_bf16 v[132:135], v[152:155], v[168:171], 0
	v_mfma_f32_16x16x32_bf16 v[124:127], v[160:163], v[168:171], 0
	v_mfma_f32_16x16x32_bf16 v[104:107], v[152:155], v[176:179], 0
	v_mfma_f32_16x16x32_bf16 v[100:103], v[160:163], v[176:179], 0
	v_mfma_f32_16x16x32_bf16 v[88:91], v[152:155], v[184:187], 0
	v_mfma_f32_16x16x32_bf16 v[84:87], v[160:163], v[184:187], 0
	v_mfma_f32_16x16x32_bf16 v[72:75], v[152:155], v[192:195], 0
	v_mfma_f32_16x16x32_bf16 v[68:71], v[160:163], v[192:195], 0
	v_mfma_f32_16x16x32_bf16 v[132:135], v[156:159], v[172:175], v[132:135]
	v_mfma_f32_16x16x32_bf16 v[124:127], v[164:167], v[172:175], v[124:127]
	v_mfma_f32_16x16x32_bf16 v[104:107], v[156:159], v[180:183], v[104:107]
	v_mfma_f32_16x16x32_bf16 v[100:103], v[164:167], v[180:183], v[100:103]
	v_mfma_f32_16x16x32_bf16 v[88:91], v[156:159], v[188:191], v[88:91]
	v_mfma_f32_16x16x32_bf16 v[84:87], v[164:167], v[188:191], v[84:87]
	v_mfma_f32_16x16x32_bf16 v[72:75], v[156:159], v[196:199], v[72:75]
	v_mfma_f32_16x16x32_bf16 v[68:71], v[164:167], v[196:199], v[68:71]
	s_setprio 0
	s_barrier
	s_add_i32 s73, s75, s16
	v_lshl_add_u64 v[214:215], s[50:51], 0, v[2:3]
	s_mov_b32 m0, s73
	ds_read_b128 v[168:171], v236 offset:16384
	ds_read_b128 v[172:175], v236 offset:17408
	ds_read_b128 v[176:179], v236 offset:18432
	ds_read_b128 v[180:183], v236 offset:19456
	ds_read_b128 v[184:187], v236 offset:20480
	ds_read_b128 v[188:191], v236 offset:21504
	ds_read_b128 v[192:195], v236 offset:22528
	ds_read_b128 v[196:199], v236 offset:23552
	global_load_lds_dwordx4 v[214:215], off
	s_add_i32 m0, s73, 0x2000
	s_add_u32 s74, s50, 0x40000
	v_lshl_add_u64 v[216:217], s[50:51], 0, v[204:205]
	s_addc_u32 s75, s51, 0
	s_add_i32 s73, s76, s16
	global_load_lds_dwordx4 v[216:217], off
	v_lshl_add_u64 v[218:219], s[74:75], 0, v[2:3]
	s_mov_b32 m0, s73
	s_nop 0
	global_load_lds_dwordx4 v[218:219], off
	v_lshl_add_u64 v[218:219], s[74:75], 0, v[204:205]
	s_add_i32 m0, s73, 0x2000
	s_nop 0
	global_load_lds_dwordx4 v[218:219], off
	v_lshl_add_u64 v[218:219], s[4:5], 0, v[208:209]
	s_mov_b32 m0, s17
	s_nop 0
	global_load_lds_dwordx4 v[218:219], off
	v_lshl_add_u64 v[218:219], s[4:5], 0, v[206:207]
	s_mov_b32 m0, s46
	s_nop 0
	global_load_lds_dwordx4 v[218:219], off
	s_waitcnt vmcnt(8)
	s_waitcnt lgkmcnt(0)
	s_barrier
	s_setprio 1
	v_mfma_f32_16x16x32_bf16 v[64:67], v[116:119], v[168:171], 0
	v_mfma_f32_16x16x32_bf16 v[60:63], v[136:139], v[168:171], 0
	v_mfma_f32_16x16x32_bf16 v[48:51], v[116:119], v[176:179], 0
	v_mfma_f32_16x16x32_bf16 v[44:47], v[136:139], v[176:179], 0
	v_mfma_f32_16x16x32_bf16 v[32:35], v[116:119], v[184:187], 0
	v_mfma_f32_16x16x32_bf16 v[28:31], v[136:139], v[184:187], 0
	v_mfma_f32_16x16x32_bf16 v[16:19], v[116:119], v[192:195], 0
	v_mfma_f32_16x16x32_bf16 v[12:15], v[136:139], v[192:195], 0
	v_mfma_f32_16x16x32_bf16 v[64:67], v[128:131], v[172:175], v[64:67]
	v_mfma_f32_16x16x32_bf16 v[60:63], v[148:151], v[172:175], v[60:63]
	v_mfma_f32_16x16x32_bf16 v[48:51], v[128:131], v[180:183], v[48:51]
	v_mfma_f32_16x16x32_bf16 v[44:47], v[148:151], v[180:183], v[44:47]
	v_mfma_f32_16x16x32_bf16 v[32:35], v[128:131], v[188:191], v[32:35]
	v_mfma_f32_16x16x32_bf16 v[28:31], v[148:151], v[188:191], v[28:31]
	v_mfma_f32_16x16x32_bf16 v[16:19], v[128:131], v[196:199], v[16:19]
	v_mfma_f32_16x16x32_bf16 v[12:15], v[148:151], v[196:199], v[12:15]
	v_mfma_f32_16x16x32_bf16 v[56:59], v[152:155], v[168:171], 0
	v_mfma_f32_16x16x32_bf16 v[52:55], v[160:163], v[168:171], 0
	v_mfma_f32_16x16x32_bf16 v[40:43], v[152:155], v[176:179], 0
	v_mfma_f32_16x16x32_bf16 v[36:39], v[160:163], v[176:179], 0
	v_mfma_f32_16x16x32_bf16 v[24:27], v[152:155], v[184:187], 0
	v_mfma_f32_16x16x32_bf16 v[20:23], v[160:163], v[184:187], 0
	v_mfma_f32_16x16x32_bf16 v[8:11], v[152:155], v[192:195], 0
	v_mfma_f32_16x16x32_bf16 v[4:7], v[160:163], v[192:195], 0
	v_mfma_f32_16x16x32_bf16 v[56:59], v[156:159], v[172:175], v[56:59]
	v_mfma_f32_16x16x32_bf16 v[52:55], v[164:167], v[172:175], v[52:55]
	v_mfma_f32_16x16x32_bf16 v[40:43], v[156:159], v[180:183], v[40:43]
	v_mfma_f32_16x16x32_bf16 v[36:39], v[164:167], v[180:183], v[36:39]
	v_mfma_f32_16x16x32_bf16 v[24:27], v[156:159], v[188:191], v[24:27]
	v_mfma_f32_16x16x32_bf16 v[20:23], v[164:167], v[188:191], v[20:23]
	v_mfma_f32_16x16x32_bf16 v[8:11], v[156:159], v[196:199], v[8:11]
	v_mfma_f32_16x16x32_bf16 v[4:7], v[164:167], v[196:199], v[4:7]
	s_setprio 0
	s_barrier
	s_add_i32 s73, 0, 0x18000
	s_add_i32 s74, 0, 0x1c000
	v_add_u32_e32 v148, s73, v203
	v_add_u32_e32 v164, s74, v203
	ds_read_b128 v[116:119], v148
	ds_read_b128 v[128:131], v148 offset:1024
	ds_read_b128 v[136:139], v148 offset:2048
	ds_read_b128 v[148:151], v148 offset:3072
	ds_read_b128 v[152:155], v164
	ds_read_b128 v[156:159], v164 offset:1024
	ds_read_b128 v[160:163], v164 offset:2048
	ds_read_b128 v[164:167], v164 offset:3072
	s_add_u32 s4, s4, 0x40000
	s_addc_u32 s5, s5, 0
	s_mov_b32 m0, s47
	v_lshl_add_u64 v[218:219], s[4:5], 0, v[208:209]
	ds_read_b128 v[168:171], v236 offset:32768
	ds_read_b128 v[172:175], v236 offset:33792
	ds_read_b128 v[176:179], v236 offset:34816
	ds_read_b128 v[180:183], v236 offset:35840
	ds_read_b128 v[184:187], v236 offset:36864
	ds_read_b128 v[188:191], v236 offset:37888
	ds_read_b128 v[192:195], v236 offset:38912
	ds_read_b128 v[196:199], v236 offset:39936
	global_load_lds_dwordx4 v[218:219], off
	v_lshl_add_u64 v[218:219], s[4:5], 0, v[206:207]
	s_mov_b32 m0, s52
	s_nop 0
	global_load_lds_dwordx4 v[218:219], off
	s_waitcnt vmcnt(8)
	s_waitcnt lgkmcnt(0)
	s_barrier
	s_setprio 1
	v_mfma_f32_16x16x32_bf16 v[144:147], v[116:119], v[168:171], v[144:147]
	v_mfma_f32_16x16x32_bf16 v[140:143], v[136:139], v[168:171], v[140:143]
	v_mfma_f32_16x16x32_bf16 v[120:123], v[116:119], v[176:179], v[120:123]
	v_mfma_f32_16x16x32_bf16 v[112:115], v[136:139], v[176:179], v[112:115]
	v_mfma_f32_16x16x32_bf16 v[96:99], v[116:119], v[184:187], v[96:99]
	v_mfma_f32_16x16x32_bf16 v[92:95], v[136:139], v[184:187], v[92:95]
	v_mfma_f32_16x16x32_bf16 v[80:83], v[116:119], v[192:195], v[80:83]
	v_mfma_f32_16x16x32_bf16 v[76:79], v[136:139], v[192:195], v[76:79]
	v_mfma_f32_16x16x32_bf16 v[144:147], v[128:131], v[172:175], v[144:147]
	v_mfma_f32_16x16x32_bf16 v[140:143], v[148:151], v[172:175], v[140:143]
	v_mfma_f32_16x16x32_bf16 v[120:123], v[128:131], v[180:183], v[120:123]
	v_mfma_f32_16x16x32_bf16 v[112:115], v[148:151], v[180:183], v[112:115]
	v_mfma_f32_16x16x32_bf16 v[96:99], v[128:131], v[188:191], v[96:99]
	v_mfma_f32_16x16x32_bf16 v[92:95], v[148:151], v[188:191], v[92:95]
	v_mfma_f32_16x16x32_bf16 v[80:83], v[128:131], v[196:199], v[80:83]
	v_mfma_f32_16x16x32_bf16 v[76:79], v[148:151], v[196:199], v[76:79]
	v_mfma_f32_16x16x32_bf16 v[132:135], v[152:155], v[168:171], v[132:135]
	v_mfma_f32_16x16x32_bf16 v[124:127], v[160:163], v[168:171], v[124:127]
	v_mfma_f32_16x16x32_bf16 v[104:107], v[152:155], v[176:179], v[104:107]
	v_mfma_f32_16x16x32_bf16 v[100:103], v[160:163], v[176:179], v[100:103]
	v_mfma_f32_16x16x32_bf16 v[88:91], v[152:155], v[184:187], v[88:91]
	v_mfma_f32_16x16x32_bf16 v[84:87], v[160:163], v[184:187], v[84:87]
	v_mfma_f32_16x16x32_bf16 v[72:75], v[152:155], v[192:195], v[72:75]
	v_mfma_f32_16x16x32_bf16 v[68:71], v[160:163], v[192:195], v[68:71]
	v_mfma_f32_16x16x32_bf16 v[132:135], v[156:159], v[172:175], v[132:135]
	v_mfma_f32_16x16x32_bf16 v[124:127], v[164:167], v[172:175], v[124:127]
	v_mfma_f32_16x16x32_bf16 v[104:107], v[156:159], v[180:183], v[104:107]
	v_mfma_f32_16x16x32_bf16 v[100:103], v[164:167], v[180:183], v[100:103]
	v_mfma_f32_16x16x32_bf16 v[88:91], v[156:159], v[188:191], v[88:91]
	v_mfma_f32_16x16x32_bf16 v[84:87], v[164:167], v[188:191], v[84:87]
	v_mfma_f32_16x16x32_bf16 v[72:75], v[156:159], v[196:199], v[72:75]
	v_mfma_f32_16x16x32_bf16 v[68:71], v[164:167], v[196:199], v[68:71]
	s_setprio 0
	s_barrier
	s_add_i32 s4, s73, s16
	v_lshl_add_u64 v[214:215], v[214:215], 0, s[34:35]
	s_mov_b32 m0, s4
	ds_read_b128 v[168:171], v236 offset:49152
	ds_read_b128 v[172:175], v236 offset:50176
	ds_read_b128 v[176:179], v236 offset:51200
	ds_read_b128 v[180:183], v236 offset:52224
	ds_read_b128 v[184:187], v236 offset:53248
	ds_read_b128 v[188:191], v236 offset:54272
	ds_read_b128 v[192:195], v236 offset:55296
	ds_read_b128 v[196:199], v236 offset:56320
	global_load_lds_dwordx4 v[214:215], off
	s_add_i32 m0, s4, 0x2000
	s_add_u32 s4, s50, 0x40080
	v_lshl_add_u64 v[214:215], v[216:217], 0, s[34:35]
	s_addc_u32 s5, s51, 0
	s_add_i32 s50, s74, s16
	global_load_lds_dwordx4 v[214:215], off
	v_lshl_add_u64 v[214:215], s[4:5], 0, v[2:3]
	s_mov_b32 m0, s50
	s_nop 0
	global_load_lds_dwordx4 v[214:215], off
	v_lshl_add_u64 v[214:215], s[4:5], 0, v[204:205]
	s_add_i32 m0, s50, 0x2000
	s_nop 0
	global_load_lds_dwordx4 v[214:215], off
	v_lshl_add_u64 v[214:215], s[12:13], 0, v[208:209]
	s_mov_b32 m0, s60
	s_nop 0
	global_load_lds_dwordx4 v[214:215], off
	v_lshl_add_u64 v[214:215], s[12:13], 0, v[206:207]
	s_mov_b32 m0, s61
	s_nop 0
	global_load_lds_dwordx4 v[214:215], off
	s_waitcnt vmcnt(8)
	s_waitcnt lgkmcnt(0)
	s_barrier
	s_setprio 1
	v_mfma_f32_16x16x32_bf16 v[64:67], v[116:119], v[168:171], v[64:67]
	v_mfma_f32_16x16x32_bf16 v[60:63], v[136:139], v[168:171], v[60:63]
	v_mfma_f32_16x16x32_bf16 v[48:51], v[116:119], v[176:179], v[48:51]
	v_mfma_f32_16x16x32_bf16 v[44:47], v[136:139], v[176:179], v[44:47]
	v_mfma_f32_16x16x32_bf16 v[32:35], v[116:119], v[184:187], v[32:35]
	v_mfma_f32_16x16x32_bf16 v[28:31], v[136:139], v[184:187], v[28:31]
	v_mfma_f32_16x16x32_bf16 v[16:19], v[116:119], v[192:195], v[16:19]
	v_mfma_f32_16x16x32_bf16 v[12:15], v[136:139], v[192:195], v[12:15]
	v_mfma_f32_16x16x32_bf16 v[64:67], v[128:131], v[172:175], v[64:67]
	v_mfma_f32_16x16x32_bf16 v[60:63], v[148:151], v[172:175], v[60:63]
	v_mfma_f32_16x16x32_bf16 v[48:51], v[128:131], v[180:183], v[48:51]
	v_mfma_f32_16x16x32_bf16 v[44:47], v[148:151], v[180:183], v[44:47]
	v_mfma_f32_16x16x32_bf16 v[32:35], v[128:131], v[188:191], v[32:35]
	v_mfma_f32_16x16x32_bf16 v[28:31], v[148:151], v[188:191], v[28:31]
	v_mfma_f32_16x16x32_bf16 v[16:19], v[128:131], v[196:199], v[16:19]
	v_mfma_f32_16x16x32_bf16 v[12:15], v[148:151], v[196:199], v[12:15]
	v_mfma_f32_16x16x32_bf16 v[56:59], v[152:155], v[168:171], v[56:59]
	v_mfma_f32_16x16x32_bf16 v[52:55], v[160:163], v[168:171], v[52:55]
	v_mfma_f32_16x16x32_bf16 v[40:43], v[152:155], v[176:179], v[40:43]
	v_mfma_f32_16x16x32_bf16 v[36:39], v[160:163], v[176:179], v[36:39]
	v_mfma_f32_16x16x32_bf16 v[24:27], v[152:155], v[184:187], v[24:27]
	v_mfma_f32_16x16x32_bf16 v[20:23], v[160:163], v[184:187], v[20:23]
	v_mfma_f32_16x16x32_bf16 v[8:11], v[152:155], v[192:195], v[8:11]
	v_mfma_f32_16x16x32_bf16 v[4:7], v[160:163], v[192:195], v[4:7]
	v_mfma_f32_16x16x32_bf16 v[56:59], v[156:159], v[172:175], v[56:59]
	v_mfma_f32_16x16x32_bf16 v[52:55], v[164:167], v[172:175], v[52:55]
	v_mfma_f32_16x16x32_bf16 v[40:43], v[156:159], v[180:183], v[40:43]
	v_mfma_f32_16x16x32_bf16 v[36:39], v[164:167], v[180:183], v[36:39]
	v_mfma_f32_16x16x32_bf16 v[24:27], v[156:159], v[188:191], v[24:27]
	v_mfma_f32_16x16x32_bf16 v[20:23], v[164:167], v[188:191], v[20:23]
	v_mfma_f32_16x16x32_bf16 v[8:11], v[156:159], v[196:199], v[8:11]
	v_mfma_f32_16x16x32_bf16 v[4:7], v[164:167], v[196:199], v[4:7]
	s_setprio 0
	s_barrier
	s_add_i32 s72, s72, 2
	s_add_u32 s48, s48, 0x100
	s_addc_u32 s49, s49, 0
	s_cmp_gt_u32 s72, 13
.LBB0_1118:
	s_add_u32 s4, s44, s48
	s_addc_u32 s5, s45, s49
	s_add_u32 s73, s4, 0x100
	s_addc_u32 s74, s5, 0
	s_add_u32 s50, s70, s48
	s_addc_u32 s51, s71, s49
	s_add_u32 s4, s4, 0x180
	s_addc_u32 s5, s5, 0
	s_add_i32 s75, 0, 0x10000
	s_add_i32 s76, 0, 0x14000
	v_add_u32_e32 v148, s75, v203
	v_add_u32_e32 v164, s76, v203
	ds_read_b128 v[116:119], v148
	ds_read_b128 v[128:131], v148 offset:1024
	ds_read_b128 v[136:139], v148 offset:2048
	ds_read_b128 v[148:151], v148 offset:3072
	ds_read_b128 v[152:155], v164
	ds_read_b128 v[156:159], v164 offset:1024
	ds_read_b128 v[160:163], v164 offset:2048
	ds_read_b128 v[164:167], v164 offset:3072
	s_cmpk_eq_i32 s48, 0x700
	s_cselect_b32 s13, s69, s5
	s_cselect_b32 s12, s68, s4
	s_cselect_b32 s51, s23, s51
	s_cselect_b32 s50, s65, s50
	s_cselect_b32 s5, s37, s74
	s_cselect_b32 s4, s64, s73
	v_lshl_add_u64 v[214:215], v[108:109], 0, s[48:49]
	s_add_i32 m0, s17, 0xc000
	ds_read_b128 v[168:171], v236
	ds_read_b128 v[172:175], v236 offset:1024
	ds_read_b128 v[176:179], v236 offset:2048
	ds_read_b128 v[180:183], v236 offset:3072
	ds_read_b128 v[184:187], v236 offset:4096
	ds_read_b128 v[188:191], v236 offset:5120
	ds_read_b128 v[192:195], v236 offset:6144
	ds_read_b128 v[196:199], v236 offset:7168
	global_load_lds_dwordx4 v[214:215], off
	v_lshl_add_u64 v[214:215], v[110:111], 0, s[48:49]
	s_add_i32 m0, s17, 0xe000
	s_nop 0
	global_load_lds_dwordx4 v[214:215], off
	s_waitcnt vmcnt(8)
	s_waitcnt lgkmcnt(0)
	s_barrier
	s_setprio 1
	v_mfma_f32_16x16x32_bf16 v[144:147], v[116:119], v[168:171], v[144:147]
	v_mfma_f32_16x16x32_bf16 v[140:143], v[136:139], v[168:171], v[140:143]
	v_mfma_f32_16x16x32_bf16 v[120:123], v[116:119], v[176:179], v[120:123]
	v_mfma_f32_16x16x32_bf16 v[112:115], v[136:139], v[176:179], v[112:115]
	v_mfma_f32_16x16x32_bf16 v[96:99], v[116:119], v[184:187], v[96:99]
	v_mfma_f32_16x16x32_bf16 v[92:95], v[136:139], v[184:187], v[92:95]
	v_mfma_f32_16x16x32_bf16 v[80:83], v[116:119], v[192:195], v[80:83]
	v_mfma_f32_16x16x32_bf16 v[76:79], v[136:139], v[192:195], v[76:79]
	v_mfma_f32_16x16x32_bf16 v[144:147], v[128:131], v[172:175], v[144:147]
	v_mfma_f32_16x16x32_bf16 v[140:143], v[148:151], v[172:175], v[140:143]
	v_mfma_f32_16x16x32_bf16 v[120:123], v[128:131], v[180:183], v[120:123]
	v_mfma_f32_16x16x32_bf16 v[112:115], v[148:151], v[180:183], v[112:115]
	v_mfma_f32_16x16x32_bf16 v[96:99], v[128:131], v[188:191], v[96:99]
	v_mfma_f32_16x16x32_bf16 v[92:95], v[148:151], v[188:191], v[92:95]
	v_mfma_f32_16x16x32_bf16 v[80:83], v[128:131], v[196:199], v[80:83]
	v_mfma_f32_16x16x32_bf16 v[76:79], v[148:151], v[196:199], v[76:79]
	v_mfma_f32_16x16x32_bf16 v[132:135], v[152:155], v[168:171], v[132:135]
	v_mfma_f32_16x16x32_bf16 v[124:127], v[160:163], v[168:171], v[124:127]
	v_mfma_f32_16x16x32_bf16 v[104:107], v[152:155], v[176:179], v[104:107]
	v_mfma_f32_16x16x32_bf16 v[100:103], v[160:163], v[176:179], v[100:103]
	v_mfma_f32_16x16x32_bf16 v[88:91], v[152:155], v[184:187], v[88:91]
	v_mfma_f32_16x16x32_bf16 v[84:87], v[160:163], v[184:187], v[84:87]
	v_mfma_f32_16x16x32_bf16 v[72:75], v[152:155], v[192:195], v[72:75]
	v_mfma_f32_16x16x32_bf16 v[68:71], v[160:163], v[192:195], v[68:71]
	v_mfma_f32_16x16x32_bf16 v[132:135], v[156:159], v[172:175], v[132:135]
	v_mfma_f32_16x16x32_bf16 v[124:127], v[164:167], v[172:175], v[124:127]
	v_mfma_f32_16x16x32_bf16 v[104:107], v[156:159], v[180:183], v[104:107]
	v_mfma_f32_16x16x32_bf16 v[100:103], v[164:167], v[180:183], v[100:103]
	v_mfma_f32_16x16x32_bf16 v[88:91], v[156:159], v[188:191], v[88:91]
	v_mfma_f32_16x16x32_bf16 v[84:87], v[164:167], v[188:191], v[84:87]
	v_mfma_f32_16x16x32_bf16 v[72:75], v[156:159], v[196:199], v[72:75]
	v_mfma_f32_16x16x32_bf16 v[68:71], v[164:167], v[196:199], v[68:71]
	s_setprio 0
	s_barrier
	s_add_i32 s73, s75, s16
	v_lshl_add_u64 v[214:215], s[50:51], 0, v[2:3]
	s_mov_b32 m0, s73
	ds_read_b128 v[168:171], v236 offset:16384
	ds_read_b128 v[172:175], v236 offset:17408
	ds_read_b128 v[176:179], v236 offset:18432
	ds_read_b128 v[180:183], v236 offset:19456
	ds_read_b128 v[184:187], v236 offset:20480
	ds_read_b128 v[188:191], v236 offset:21504
	ds_read_b128 v[192:195], v236 offset:22528
	ds_read_b128 v[196:199], v236 offset:23552
	global_load_lds_dwordx4 v[214:215], off
	s_add_i32 m0, s73, 0x2000
	s_add_u32 s74, s50, 0x40000
	v_lshl_add_u64 v[216:217], s[50:51], 0, v[204:205]
	s_addc_u32 s75, s51, 0
	s_add_i32 s73, s76, s16
	global_load_lds_dwordx4 v[216:217], off
	v_lshl_add_u64 v[218:219], s[74:75], 0, v[2:3]
	s_mov_b32 m0, s73
	s_nop 0
	global_load_lds_dwordx4 v[218:219], off
	v_lshl_add_u64 v[218:219], s[74:75], 0, v[204:205]
	s_add_i32 m0, s73, 0x2000
	s_nop 0
	global_load_lds_dwordx4 v[218:219], off
	v_lshl_add_u64 v[218:219], s[4:5], 0, v[208:209]
	s_mov_b32 m0, s17
	s_nop 0
	global_load_lds_dwordx4 v[218:219], off
	v_lshl_add_u64 v[218:219], s[4:5], 0, v[206:207]
	s_mov_b32 m0, s46
	s_nop 0
	global_load_lds_dwordx4 v[218:219], off
	s_waitcnt vmcnt(8)
	s_waitcnt lgkmcnt(0)
	s_barrier
	s_setprio 1
	v_mfma_f32_16x16x32_bf16 v[64:67], v[116:119], v[168:171], v[64:67]
	v_mfma_f32_16x16x32_bf16 v[60:63], v[136:139], v[168:171], v[60:63]
	v_mfma_f32_16x16x32_bf16 v[48:51], v[116:119], v[176:179], v[48:51]
	v_mfma_f32_16x16x32_bf16 v[44:47], v[136:139], v[176:179], v[44:47]
	v_mfma_f32_16x16x32_bf16 v[32:35], v[116:119], v[184:187], v[32:35]
	v_mfma_f32_16x16x32_bf16 v[28:31], v[136:139], v[184:187], v[28:31]
	v_mfma_f32_16x16x32_bf16 v[16:19], v[116:119], v[192:195], v[16:19]
	v_mfma_f32_16x16x32_bf16 v[12:15], v[136:139], v[192:195], v[12:15]
	v_mfma_f32_16x16x32_bf16 v[64:67], v[128:131], v[172:175], v[64:67]
	v_mfma_f32_16x16x32_bf16 v[60:63], v[148:151], v[172:175], v[60:63]
	v_mfma_f32_16x16x32_bf16 v[48:51], v[128:131], v[180:183], v[48:51]
	v_mfma_f32_16x16x32_bf16 v[44:47], v[148:151], v[180:183], v[44:47]
	v_mfma_f32_16x16x32_bf16 v[32:35], v[128:131], v[188:191], v[32:35]
	v_mfma_f32_16x16x32_bf16 v[28:31], v[148:151], v[188:191], v[28:31]
	v_mfma_f32_16x16x32_bf16 v[16:19], v[128:131], v[196:199], v[16:19]
	v_mfma_f32_16x16x32_bf16 v[12:15], v[148:151], v[196:199], v[12:15]
	v_mfma_f32_16x16x32_bf16 v[56:59], v[152:155], v[168:171], v[56:59]
	v_mfma_f32_16x16x32_bf16 v[52:55], v[160:163], v[168:171], v[52:55]
	v_mfma_f32_16x16x32_bf16 v[40:43], v[152:155], v[176:179], v[40:43]
	v_mfma_f32_16x16x32_bf16 v[36:39], v[160:163], v[176:179], v[36:39]
	v_mfma_f32_16x16x32_bf16 v[24:27], v[152:155], v[184:187], v[24:27]
	v_mfma_f32_16x16x32_bf16 v[20:23], v[160:163], v[184:187], v[20:23]
	v_mfma_f32_16x16x32_bf16 v[8:11], v[152:155], v[192:195], v[8:11]
	v_mfma_f32_16x16x32_bf16 v[4:7], v[160:163], v[192:195], v[4:7]
	v_mfma_f32_16x16x32_bf16 v[56:59], v[156:159], v[172:175], v[56:59]
	v_mfma_f32_16x16x32_bf16 v[52:55], v[164:167], v[172:175], v[52:55]
	v_mfma_f32_16x16x32_bf16 v[40:43], v[156:159], v[180:183], v[40:43]
	v_mfma_f32_16x16x32_bf16 v[36:39], v[164:167], v[180:183], v[36:39]
	v_mfma_f32_16x16x32_bf16 v[24:27], v[156:159], v[188:191], v[24:27]
	v_mfma_f32_16x16x32_bf16 v[20:23], v[164:167], v[188:191], v[20:23]
	v_mfma_f32_16x16x32_bf16 v[8:11], v[156:159], v[196:199], v[8:11]
	v_mfma_f32_16x16x32_bf16 v[4:7], v[164:167], v[196:199], v[4:7]
	s_setprio 0
	s_barrier
	s_add_i32 s73, 0, 0x18000
	s_add_i32 s74, 0, 0x1c000
	v_add_u32_e32 v148, s73, v203
	v_add_u32_e32 v164, s74, v203
	ds_read_b128 v[116:119], v148
	ds_read_b128 v[128:131], v148 offset:1024
	ds_read_b128 v[136:139], v148 offset:2048
	ds_read_b128 v[148:151], v148 offset:3072
	ds_read_b128 v[152:155], v164
	ds_read_b128 v[156:159], v164 offset:1024
	ds_read_b128 v[160:163], v164 offset:2048
	ds_read_b128 v[164:167], v164 offset:3072
	s_add_u32 s4, s4, 0x40000
	s_addc_u32 s5, s5, 0
	s_mov_b32 m0, s47
	v_lshl_add_u64 v[218:219], s[4:5], 0, v[208:209]
	ds_read_b128 v[168:171], v236 offset:32768
	ds_read_b128 v[172:175], v236 offset:33792
	ds_read_b128 v[176:179], v236 offset:34816
	ds_read_b128 v[180:183], v236 offset:35840
	ds_read_b128 v[184:187], v236 offset:36864
	ds_read_b128 v[188:191], v236 offset:37888
	ds_read_b128 v[192:195], v236 offset:38912
	ds_read_b128 v[196:199], v236 offset:39936
	global_load_lds_dwordx4 v[218:219], off
	v_lshl_add_u64 v[218:219], s[4:5], 0, v[206:207]
	s_mov_b32 m0, s52
	s_nop 0
	global_load_lds_dwordx4 v[218:219], off
	s_waitcnt vmcnt(8)
	s_waitcnt lgkmcnt(0)
	s_barrier
	s_setprio 1
	v_mfma_f32_16x16x32_bf16 v[144:147], v[116:119], v[168:171], v[144:147]
	v_mfma_f32_16x16x32_bf16 v[140:143], v[136:139], v[168:171], v[140:143]
	v_mfma_f32_16x16x32_bf16 v[120:123], v[116:119], v[176:179], v[120:123]
	v_mfma_f32_16x16x32_bf16 v[112:115], v[136:139], v[176:179], v[112:115]
	v_mfma_f32_16x16x32_bf16 v[96:99], v[116:119], v[184:187], v[96:99]
	v_mfma_f32_16x16x32_bf16 v[92:95], v[136:139], v[184:187], v[92:95]
	v_mfma_f32_16x16x32_bf16 v[80:83], v[116:119], v[192:195], v[80:83]
	v_mfma_f32_16x16x32_bf16 v[76:79], v[136:139], v[192:195], v[76:79]
	v_mfma_f32_16x16x32_bf16 v[144:147], v[128:131], v[172:175], v[144:147]
	v_mfma_f32_16x16x32_bf16 v[140:143], v[148:151], v[172:175], v[140:143]
	v_mfma_f32_16x16x32_bf16 v[120:123], v[128:131], v[180:183], v[120:123]
	v_mfma_f32_16x16x32_bf16 v[112:115], v[148:151], v[180:183], v[112:115]
	v_mfma_f32_16x16x32_bf16 v[96:99], v[128:131], v[188:191], v[96:99]
	v_mfma_f32_16x16x32_bf16 v[92:95], v[148:151], v[188:191], v[92:95]
	v_mfma_f32_16x16x32_bf16 v[80:83], v[128:131], v[196:199], v[80:83]
	v_mfma_f32_16x16x32_bf16 v[76:79], v[148:151], v[196:199], v[76:79]
	v_mfma_f32_16x16x32_bf16 v[132:135], v[152:155], v[168:171], v[132:135]
	v_mfma_f32_16x16x32_bf16 v[124:127], v[160:163], v[168:171], v[124:127]
	v_mfma_f32_16x16x32_bf16 v[104:107], v[152:155], v[176:179], v[104:107]
	v_mfma_f32_16x16x32_bf16 v[100:103], v[160:163], v[176:179], v[100:103]
	v_mfma_f32_16x16x32_bf16 v[88:91], v[152:155], v[184:187], v[88:91]
	v_mfma_f32_16x16x32_bf16 v[84:87], v[160:163], v[184:187], v[84:87]
	v_mfma_f32_16x16x32_bf16 v[72:75], v[152:155], v[192:195], v[72:75]
	v_mfma_f32_16x16x32_bf16 v[68:71], v[160:163], v[192:195], v[68:71]
	v_mfma_f32_16x16x32_bf16 v[132:135], v[156:159], v[172:175], v[132:135]
	v_mfma_f32_16x16x32_bf16 v[124:127], v[164:167], v[172:175], v[124:127]
	v_mfma_f32_16x16x32_bf16 v[104:107], v[156:159], v[180:183], v[104:107]
	v_mfma_f32_16x16x32_bf16 v[100:103], v[164:167], v[180:183], v[100:103]
	v_mfma_f32_16x16x32_bf16 v[88:91], v[156:159], v[188:191], v[88:91]
	v_mfma_f32_16x16x32_bf16 v[84:87], v[164:167], v[188:191], v[84:87]
	v_mfma_f32_16x16x32_bf16 v[72:75], v[156:159], v[196:199], v[72:75]
	v_mfma_f32_16x16x32_bf16 v[68:71], v[164:167], v[196:199], v[68:71]
	s_setprio 0
	s_barrier
	s_add_i32 s4, s73, s16
	v_lshl_add_u64 v[214:215], v[214:215], 0, s[34:35]
	s_mov_b32 m0, s4
	ds_read_b128 v[168:171], v236 offset:49152
	ds_read_b128 v[172:175], v236 offset:50176
	ds_read_b128 v[176:179], v236 offset:51200
	ds_read_b128 v[180:183], v236 offset:52224
	ds_read_b128 v[184:187], v236 offset:53248
	ds_read_b128 v[188:191], v236 offset:54272
	ds_read_b128 v[192:195], v236 offset:55296
	ds_read_b128 v[196:199], v236 offset:56320
	global_load_lds_dwordx4 v[214:215], off
	s_add_i32 m0, s4, 0x2000
	s_add_u32 s4, s50, 0x40080
	v_lshl_add_u64 v[214:215], v[216:217], 0, s[34:35]
	s_addc_u32 s5, s51, 0
	s_add_i32 s50, s74, s16
	global_load_lds_dwordx4 v[214:215], off
	v_lshl_add_u64 v[214:215], s[4:5], 0, v[2:3]
	s_mov_b32 m0, s50
	s_nop 0
	global_load_lds_dwordx4 v[214:215], off
	v_lshl_add_u64 v[214:215], s[4:5], 0, v[204:205]
	s_add_i32 m0, s50, 0x2000
	s_nop 0
	global_load_lds_dwordx4 v[214:215], off
	v_lshl_add_u64 v[214:215], s[12:13], 0, v[208:209]
	s_mov_b32 m0, s60
	s_nop 0
	global_load_lds_dwordx4 v[214:215], off
	v_lshl_add_u64 v[214:215], s[12:13], 0, v[206:207]
	s_mov_b32 m0, s61
	s_nop 0
	global_load_lds_dwordx4 v[214:215], off
	s_waitcnt vmcnt(8)
	s_waitcnt lgkmcnt(0)
	s_barrier
	s_setprio 1
	v_mfma_f32_16x16x32_bf16 v[64:67], v[116:119], v[168:171], v[64:67]
	v_mfma_f32_16x16x32_bf16 v[60:63], v[136:139], v[168:171], v[60:63]
	v_mfma_f32_16x16x32_bf16 v[48:51], v[116:119], v[176:179], v[48:51]
	v_mfma_f32_16x16x32_bf16 v[44:47], v[136:139], v[176:179], v[44:47]
	v_mfma_f32_16x16x32_bf16 v[32:35], v[116:119], v[184:187], v[32:35]
	v_mfma_f32_16x16x32_bf16 v[28:31], v[136:139], v[184:187], v[28:31]
	v_mfma_f32_16x16x32_bf16 v[16:19], v[116:119], v[192:195], v[16:19]
	v_mfma_f32_16x16x32_bf16 v[12:15], v[136:139], v[192:195], v[12:15]
	v_mfma_f32_16x16x32_bf16 v[64:67], v[128:131], v[172:175], v[64:67]
	v_mfma_f32_16x16x32_bf16 v[60:63], v[148:151], v[172:175], v[60:63]
	v_mfma_f32_16x16x32_bf16 v[48:51], v[128:131], v[180:183], v[48:51]
	v_mfma_f32_16x16x32_bf16 v[44:47], v[148:151], v[180:183], v[44:47]
	v_mfma_f32_16x16x32_bf16 v[32:35], v[128:131], v[188:191], v[32:35]
	v_mfma_f32_16x16x32_bf16 v[28:31], v[148:151], v[188:191], v[28:31]
	v_mfma_f32_16x16x32_bf16 v[16:19], v[128:131], v[196:199], v[16:19]
	v_mfma_f32_16x16x32_bf16 v[12:15], v[148:151], v[196:199], v[12:15]
	v_mfma_f32_16x16x32_bf16 v[56:59], v[152:155], v[168:171], v[56:59]
	v_mfma_f32_16x16x32_bf16 v[52:55], v[160:163], v[168:171], v[52:55]
	v_mfma_f32_16x16x32_bf16 v[40:43], v[152:155], v[176:179], v[40:43]
	v_mfma_f32_16x16x32_bf16 v[36:39], v[160:163], v[176:179], v[36:39]
	v_mfma_f32_16x16x32_bf16 v[24:27], v[152:155], v[184:187], v[24:27]
	v_mfma_f32_16x16x32_bf16 v[20:23], v[160:163], v[184:187], v[20:23]
	v_mfma_f32_16x16x32_bf16 v[8:11], v[152:155], v[192:195], v[8:11]
	v_mfma_f32_16x16x32_bf16 v[4:7], v[160:163], v[192:195], v[4:7]
	v_mfma_f32_16x16x32_bf16 v[56:59], v[156:159], v[172:175], v[56:59]
	v_mfma_f32_16x16x32_bf16 v[52:55], v[164:167], v[172:175], v[52:55]
	v_mfma_f32_16x16x32_bf16 v[40:43], v[156:159], v[180:183], v[40:43]
	v_mfma_f32_16x16x32_bf16 v[36:39], v[164:167], v[180:183], v[36:39]
	v_mfma_f32_16x16x32_bf16 v[24:27], v[156:159], v[188:191], v[24:27]
	v_mfma_f32_16x16x32_bf16 v[20:23], v[164:167], v[188:191], v[20:23]
	v_mfma_f32_16x16x32_bf16 v[8:11], v[156:159], v[196:199], v[8:11]
	v_mfma_f32_16x16x32_bf16 v[4:7], v[164:167], v[196:199], v[4:7]
	s_setprio 0
	s_barrier
	s_add_i32 s72, s72, 2
	s_add_u32 s48, s48, 0x100
	s_addc_u32 s49, s49, 0
	s_cmp_gt_u32 s72, 13
	s_cbranch_scc0 .LBB0_1118
	s_and_b64 vcc, exec, s[20:21]
	s_cbranch_vccz .LBB0_1121
	s_barrier

.LBB0_1205:
	s_ashr_i32 s37, s36, 31
	s_lshl_b64 s[4:5], s[36:37], 19
	s_add_u32 s40, s6, s4
	s_addc_u32 s41, s7, s5
	s_and_b64 s[4:5], s[38:39], exec
	s_cselect_b32 s37, s41, s23
	s_cselect_b32 s61, s40, s22
	s_ashr_i32 s21, s20, 31
	s_lshl_b64 s[4:5], s[20:21], 19
	s_add_u32 s42, s8, s4
	s_addc_u32 s43, s9, s5
	s_and_b64 s[4:5], s[38:39], exec
	s_cselect_b32 s21, s43, s45
	s_cselect_b32 s62, s42, s44
	s_add_u32 s63, s61, 0x80
	s_addc_u32 s64, s37, 0
	s_add_u32 s4, s22, 0x40080
	s_addc_u32 s5, s23, 0
	s_add_u32 s65, s44, 0x100
	v_lshl_add_u64 v[142:143], s[4:5], 0, v[138:139]
	v_lshl_add_u64 v[144:145], s[4:5], 0, v[140:141]
	s_addc_u32 s68, s45, 0
	s_mov_b32 s69, -2
	s_mov_b64 s[44:45], 0
	s_add_u32 s4, s22, s44
	s_addc_u32 s5, s23, s45
	s_add_u32 s70, s4, 0x100
	s_addc_u32 s71, s5, 0
	s_add_u32 s48, s65, s44
	s_addc_u32 s49, s68, s45
	s_add_u32 s4, s4, 0x180
	s_addc_u32 s5, s5, 0
	s_add_i32 s72, 0, 0x10000
	s_add_i32 s73, 0, 0x14000
	v_add_u32_e32 v160, s72, v146
	v_add_u32_e32 v176, s73, v146
	ds_read_b128 v[148:151], v160
	ds_read_b128 v[152:155], v160 offset:1024
	ds_read_b128 v[156:159], v160 offset:2048
	ds_read_b128 v[160:163], v160 offset:3072
	ds_read_b128 v[164:167], v176
	ds_read_b128 v[168:171], v176 offset:1024
	ds_read_b128 v[172:175], v176 offset:2048
	ds_read_b128 v[176:179], v176 offset:3072
	s_cmpk_eq_i32 s44, 0x700
	s_cselect_b32 s13, s64, s5
	s_cselect_b32 s12, s63, s4
	s_cselect_b32 s49, s21, s49
	s_cselect_b32 s48, s62, s48
	s_cselect_b32 s5, s37, s71
	s_cselect_b32 s4, s61, s70
	v_lshl_add_u64 v[216:217], v[142:143], 0, s[44:45]
	s_add_i32 m0, s17, 0xc000
	ds_read_b128 v[180:183], v147
	ds_read_b128 v[184:187], v147 offset:1024
	ds_read_b128 v[188:191], v147 offset:2048
	ds_read_b128 v[192:195], v147 offset:3072
	ds_read_b128 v[196:199], v147 offset:4096
	ds_read_b128 v[204:207], v147 offset:5120
	ds_read_b128 v[208:211], v147 offset:6144
	ds_read_b128 v[212:215], v147 offset:7168
	global_load_lds_dwordx4 v[216:217], off
	v_lshl_add_u64 v[216:217], v[144:145], 0, s[44:45]
	s_add_i32 m0, s17, 0xe000
	s_nop 0
	global_load_lds_dwordx4 v[216:217], off
	s_waitcnt vmcnt(8)
	s_waitcnt lgkmcnt(0)
	s_barrier
	s_setprio 1
	v_mfma_f32_16x16x32_bf16 v[128:131], v[148:151], v[180:183], 0
	v_mfma_f32_16x16x32_bf16 v[124:127], v[156:159], v[180:183], 0
	v_mfma_f32_16x16x32_bf16 v[120:123], v[148:151], v[188:191], 0
	v_mfma_f32_16x16x32_bf16 v[116:119], v[156:159], v[188:191], 0
	v_mfma_f32_16x16x32_bf16 v[104:107], v[148:151], v[196:199], 0
	v_mfma_f32_16x16x32_bf16 v[100:103], v[156:159], v[196:199], 0
	v_mfma_f32_16x16x32_bf16 v[88:91], v[148:151], v[208:211], 0
	v_mfma_f32_16x16x32_bf16 v[84:87], v[156:159], v[208:211], 0
	v_mfma_f32_16x16x32_bf16 v[128:131], v[152:155], v[184:187], v[128:131]
	v_mfma_f32_16x16x32_bf16 v[124:127], v[160:163], v[184:187], v[124:127]
	v_mfma_f32_16x16x32_bf16 v[120:123], v[152:155], v[192:195], v[120:123]
	v_mfma_f32_16x16x32_bf16 v[116:119], v[160:163], v[192:195], v[116:119]
	v_mfma_f32_16x16x32_bf16 v[104:107], v[152:155], v[204:207], v[104:107]
	v_mfma_f32_16x16x32_bf16 v[100:103], v[160:163], v[204:207], v[100:103]
	v_mfma_f32_16x16x32_bf16 v[88:91], v[152:155], v[212:215], v[88:91]
	v_mfma_f32_16x16x32_bf16 v[84:87], v[160:163], v[212:215], v[84:87]
	v_mfma_f32_16x16x32_bf16 v[112:115], v[164:167], v[180:183], 0
	v_mfma_f32_16x16x32_bf16 v[108:111], v[172:175], v[180:183], 0
	v_mfma_f32_16x16x32_bf16 v[96:99], v[164:167], v[188:191], 0
	v_mfma_f32_16x16x32_bf16 v[92:95], v[172:175], v[188:191], 0
	v_mfma_f32_16x16x32_bf16 v[80:83], v[164:167], v[196:199], 0
	v_mfma_f32_16x16x32_bf16 v[76:79], v[172:175], v[196:199], 0
	v_mfma_f32_16x16x32_bf16 v[72:75], v[164:167], v[208:211], 0
	v_mfma_f32_16x16x32_bf16 v[68:71], v[172:175], v[208:211], 0
	v_mfma_f32_16x16x32_bf16 v[112:115], v[168:171], v[184:187], v[112:115]
	v_mfma_f32_16x16x32_bf16 v[108:111], v[176:179], v[184:187], v[108:111]
	v_mfma_f32_16x16x32_bf16 v[96:99], v[168:171], v[192:195], v[96:99]
	v_mfma_f32_16x16x32_bf16 v[92:95], v[176:179], v[192:195], v[92:95]
	v_mfma_f32_16x16x32_bf16 v[80:83], v[168:171], v[204:207], v[80:83]
	v_mfma_f32_16x16x32_bf16 v[76:79], v[176:179], v[204:207], v[76:79]
	v_mfma_f32_16x16x32_bf16 v[72:75], v[168:171], v[212:215], v[72:75]
	v_mfma_f32_16x16x32_bf16 v[68:71], v[176:179], v[212:215], v[68:71]
	s_setprio 0
	s_barrier
	s_add_i32 s70, s72, s16
	v_lshl_add_u64 v[216:217], s[48:49], 0, v[2:3]
	s_mov_b32 m0, s70
	ds_read_b128 v[180:183], v147 offset:16384
	ds_read_b128 v[184:187], v147 offset:17408
	ds_read_b128 v[188:191], v147 offset:18432
	ds_read_b128 v[192:195], v147 offset:19456
	ds_read_b128 v[196:199], v147 offset:20480
	ds_read_b128 v[204:207], v147 offset:21504
	ds_read_b128 v[208:211], v147 offset:22528
	ds_read_b128 v[212:215], v147 offset:23552
	global_load_lds_dwordx4 v[216:217], off
	s_add_i32 m0, s70, 0x2000
	s_add_u32 s70, s48, 0x40000
	v_lshl_add_u64 v[218:219], s[48:49], 0, v[132:133]
	s_addc_u32 s71, s49, 0
	s_add_i32 s72, s73, s16
	global_load_lds_dwordx4 v[218:219], off
	v_lshl_add_u64 v[220:221], s[70:71], 0, v[2:3]
	s_mov_b32 m0, s72
	s_nop 0
	global_load_lds_dwordx4 v[220:221], off
	v_lshl_add_u64 v[220:221], s[70:71], 0, v[132:133]
	s_add_i32 m0, s72, 0x2000
	s_nop 0
	global_load_lds_dwordx4 v[220:221], off
	v_lshl_add_u64 v[220:221], s[4:5], 0, v[136:137]
	s_mov_b32 m0, s17
	s_nop 0
	global_load_lds_dwordx4 v[220:221], off
	v_lshl_add_u64 v[220:221], s[4:5], 0, v[134:135]
	s_mov_b32 m0, s46
	s_nop 0
	global_load_lds_dwordx4 v[220:221], off
	s_waitcnt vmcnt(8)
	s_waitcnt lgkmcnt(0)
	s_barrier
	s_setprio 1
	v_mfma_f32_16x16x32_bf16 v[64:67], v[148:151], v[180:183], 0
	v_mfma_f32_16x16x32_bf16 v[60:63], v[156:159], v[180:183], 0
	v_mfma_f32_16x16x32_bf16 v[56:59], v[148:151], v[188:191], 0
	v_mfma_f32_16x16x32_bf16 v[52:55], v[156:159], v[188:191], 0
	v_mfma_f32_16x16x32_bf16 v[40:43], v[148:151], v[196:199], 0
	v_mfma_f32_16x16x32_bf16 v[36:39], v[156:159], v[196:199], 0
	v_mfma_f32_16x16x32_bf16 v[24:27], v[148:151], v[208:211], 0
	v_mfma_f32_16x16x32_bf16 v[20:23], v[156:159], v[208:211], 0
	v_mfma_f32_16x16x32_bf16 v[64:67], v[152:155], v[184:187], v[64:67]
	v_mfma_f32_16x16x32_bf16 v[60:63], v[160:163], v[184:187], v[60:63]
	v_mfma_f32_16x16x32_bf16 v[56:59], v[152:155], v[192:195], v[56:59]
	v_mfma_f32_16x16x32_bf16 v[52:55], v[160:163], v[192:195], v[52:55]
	v_mfma_f32_16x16x32_bf16 v[40:43], v[152:155], v[204:207], v[40:43]
	v_mfma_f32_16x16x32_bf16 v[36:39], v[160:163], v[204:207], v[36:39]
	v_mfma_f32_16x16x32_bf16 v[24:27], v[152:155], v[212:215], v[24:27]
	v_mfma_f32_16x16x32_bf16 v[20:23], v[160:163], v[212:215], v[20:23]
	v_mfma_f32_16x16x32_bf16 v[48:51], v[164:167], v[180:183], 0
	v_mfma_f32_16x16x32_bf16 v[44:47], v[172:175], v[180:183], 0
	v_mfma_f32_16x16x32_bf16 v[32:35], v[164:167], v[188:191], 0
	v_mfma_f32_16x16x32_bf16 v[28:31], v[172:175], v[188:191], 0
	v_mfma_f32_16x16x32_bf16 v[16:19], v[164:167], v[196:199], 0
	v_mfma_f32_16x16x32_bf16 v[12:15], v[172:175], v[196:199], 0
	v_mfma_f32_16x16x32_bf16 v[8:11], v[164:167], v[208:211], 0
	v_mfma_f32_16x16x32_bf16 v[4:7], v[172:175], v[208:211], 0
	v_mfma_f32_16x16x32_bf16 v[48:51], v[168:171], v[184:187], v[48:51]
	v_mfma_f32_16x16x32_bf16 v[44:47], v[176:179], v[184:187], v[44:47]
	v_mfma_f32_16x16x32_bf16 v[32:35], v[168:171], v[192:195], v[32:35]
	v_mfma_f32_16x16x32_bf16 v[28:31], v[176:179], v[192:195], v[28:31]
	v_mfma_f32_16x16x32_bf16 v[16:19], v[168:171], v[204:207], v[16:19]
	v_mfma_f32_16x16x32_bf16 v[12:15], v[176:179], v[204:207], v[12:15]
	v_mfma_f32_16x16x32_bf16 v[8:11], v[168:171], v[212:215], v[8:11]
	v_mfma_f32_16x16x32_bf16 v[4:7], v[176:179], v[212:215], v[4:7]
	s_setprio 0
	s_barrier
	s_add_i32 s70, 0, 0x18000
	s_add_i32 s71, 0, 0x1c000
	v_add_u32_e32 v160, s70, v146
	v_add_u32_e32 v176, s71, v146
	ds_read_b128 v[148:151], v160
	ds_read_b128 v[152:155], v160 offset:1024
	ds_read_b128 v[156:159], v160 offset:2048
	ds_read_b128 v[160:163], v160 offset:3072
	ds_read_b128 v[164:167], v176
	ds_read_b128 v[168:171], v176 offset:1024
	ds_read_b128 v[172:175], v176 offset:2048
	ds_read_b128 v[176:179], v176 offset:3072
	s_add_u32 s4, s4, 0x40000
	s_addc_u32 s5, s5, 0
	s_mov_b32 m0, s47
	v_lshl_add_u64 v[220:221], s[4:5], 0, v[136:137]
	ds_read_b128 v[180:183], v147 offset:32768
	ds_read_b128 v[184:187], v147 offset:33792
	ds_read_b128 v[188:191], v147 offset:34816
	ds_read_b128 v[192:195], v147 offset:35840
	ds_read_b128 v[196:199], v147 offset:36864
	ds_read_b128 v[204:207], v147 offset:37888
	ds_read_b128 v[208:211], v147 offset:38912
	ds_read_b128 v[212:215], v147 offset:39936
	global_load_lds_dwordx4 v[220:221], off
	v_lshl_add_u64 v[220:221], s[4:5], 0, v[134:135]
	s_mov_b32 m0, s50
	s_nop 0
	global_load_lds_dwordx4 v[220:221], off
	s_waitcnt vmcnt(8)
	s_waitcnt lgkmcnt(0)
	s_barrier
	s_setprio 1
	v_mfma_f32_16x16x32_bf16 v[128:131], v[148:151], v[180:183], v[128:131]
	v_mfma_f32_16x16x32_bf16 v[124:127], v[156:159], v[180:183], v[124:127]
	v_mfma_f32_16x16x32_bf16 v[120:123], v[148:151], v[188:191], v[120:123]
	v_mfma_f32_16x16x32_bf16 v[116:119], v[156:159], v[188:191], v[116:119]
	v_mfma_f32_16x16x32_bf16 v[104:107], v[148:151], v[196:199], v[104:107]
	v_mfma_f32_16x16x32_bf16 v[100:103], v[156:159], v[196:199], v[100:103]
	v_mfma_f32_16x16x32_bf16 v[88:91], v[148:151], v[208:211], v[88:91]
	v_mfma_f32_16x16x32_bf16 v[84:87], v[156:159], v[208:211], v[84:87]
	v_mfma_f32_16x16x32_bf16 v[128:131], v[152:155], v[184:187], v[128:131]
	v_mfma_f32_16x16x32_bf16 v[124:127], v[160:163], v[184:187], v[124:127]
	v_mfma_f32_16x16x32_bf16 v[120:123], v[152:155], v[192:195], v[120:123]
	v_mfma_f32_16x16x32_bf16 v[116:119], v[160:163], v[192:195], v[116:119]
	v_mfma_f32_16x16x32_bf16 v[104:107], v[152:155], v[204:207], v[104:107]
	v_mfma_f32_16x16x32_bf16 v[100:103], v[160:163], v[204:207], v[100:103]
	v_mfma_f32_16x16x32_bf16 v[88:91], v[152:155], v[212:215], v[88:91]
	v_mfma_f32_16x16x32_bf16 v[84:87], v[160:163], v[212:215], v[84:87]
	v_mfma_f32_16x16x32_bf16 v[112:115], v[164:167], v[180:183], v[112:115]
	v_mfma_f32_16x16x32_bf16 v[108:111], v[172:175], v[180:183], v[108:111]
	v_mfma_f32_16x16x32_bf16 v[96:99], v[164:167], v[188:191], v[96:99]
	v_mfma_f32_16x16x32_bf16 v[92:95], v[172:175], v[188:191], v[92:95]
	v_mfma_f32_16x16x32_bf16 v[80:83], v[164:167], v[196:199], v[80:83]
	v_mfma_f32_16x16x32_bf16 v[76:79], v[172:175], v[196:199], v[76:79]
	v_mfma_f32_16x16x32_bf16 v[72:75], v[164:167], v[208:211], v[72:75]
	v_mfma_f32_16x16x32_bf16 v[68:71], v[172:175], v[208:211], v[68:71]
	v_mfma_f32_16x16x32_bf16 v[112:115], v[168:171], v[184:187], v[112:115]
	v_mfma_f32_16x16x32_bf16 v[108:111], v[176:179], v[184:187], v[108:111]
	v_mfma_f32_16x16x32_bf16 v[96:99], v[168:171], v[192:195], v[96:99]
	v_mfma_f32_16x16x32_bf16 v[92:95], v[176:179], v[192:195], v[92:95]
	v_mfma_f32_16x16x32_bf16 v[80:83], v[168:171], v[204:207], v[80:83]
	v_mfma_f32_16x16x32_bf16 v[76:79], v[176:179], v[204:207], v[76:79]
	v_mfma_f32_16x16x32_bf16 v[72:75], v[168:171], v[212:215], v[72:75]
	v_mfma_f32_16x16x32_bf16 v[68:71], v[176:179], v[212:215], v[68:71]
	s_setprio 0
	s_barrier
	s_add_i32 s4, s70, s16
	v_lshl_add_u64 v[216:217], v[216:217], 0, s[34:35]
	s_mov_b32 m0, s4
	ds_read_b128 v[180:183], v147 offset:49152
	ds_read_b128 v[184:187], v147 offset:50176
	ds_read_b128 v[188:191], v147 offset:51200
	ds_read_b128 v[192:195], v147 offset:52224
	ds_read_b128 v[196:199], v147 offset:53248
	ds_read_b128 v[204:207], v147 offset:54272
	ds_read_b128 v[208:211], v147 offset:55296
	ds_read_b128 v[212:215], v147 offset:56320
	global_load_lds_dwordx4 v[216:217], off
	s_add_i32 m0, s4, 0x2000
	s_add_u32 s4, s48, 0x40080
	v_lshl_add_u64 v[216:217], v[218:219], 0, s[34:35]
	s_addc_u32 s5, s49, 0
	s_add_i32 s48, s71, s16
	global_load_lds_dwordx4 v[216:217], off
	v_lshl_add_u64 v[216:217], s[4:5], 0, v[2:3]
	s_mov_b32 m0, s48
	s_nop 0
	global_load_lds_dwordx4 v[216:217], off
	v_lshl_add_u64 v[216:217], s[4:5], 0, v[132:133]
	s_add_i32 m0, s48, 0x2000
	s_nop 0
	global_load_lds_dwordx4 v[216:217], off
	v_lshl_add_u64 v[216:217], s[12:13], 0, v[136:137]
	s_mov_b32 m0, s53
	s_nop 0
	global_load_lds_dwordx4 v[216:217], off
	v_lshl_add_u64 v[216:217], s[12:13], 0, v[134:135]
	s_mov_b32 m0, s56
	s_nop 0
	global_load_lds_dwordx4 v[216:217], off
	s_waitcnt vmcnt(8)
	s_waitcnt lgkmcnt(0)
	s_barrier
	s_setprio 1
	v_mfma_f32_16x16x32_bf16 v[64:67], v[148:151], v[180:183], v[64:67]
	v_mfma_f32_16x16x32_bf16 v[60:63], v[156:159], v[180:183], v[60:63]
	v_mfma_f32_16x16x32_bf16 v[56:59], v[148:151], v[188:191], v[56:59]
	v_mfma_f32_16x16x32_bf16 v[52:55], v[156:159], v[188:191], v[52:55]
	v_mfma_f32_16x16x32_bf16 v[40:43], v[148:151], v[196:199], v[40:43]
	v_mfma_f32_16x16x32_bf16 v[36:39], v[156:159], v[196:199], v[36:39]
	v_mfma_f32_16x16x32_bf16 v[24:27], v[148:151], v[208:211], v[24:27]
	v_mfma_f32_16x16x32_bf16 v[20:23], v[156:159], v[208:211], v[20:23]
	v_mfma_f32_16x16x32_bf16 v[64:67], v[152:155], v[184:187], v[64:67]
	v_mfma_f32_16x16x32_bf16 v[60:63], v[160:163], v[184:187], v[60:63]
	v_mfma_f32_16x16x32_bf16 v[56:59], v[152:155], v[192:195], v[56:59]
	v_mfma_f32_16x16x32_bf16 v[52:55], v[160:163], v[192:195], v[52:55]
	v_mfma_f32_16x16x32_bf16 v[40:43], v[152:155], v[204:207], v[40:43]
	v_mfma_f32_16x16x32_bf16 v[36:39], v[160:163], v[204:207], v[36:39]
	v_mfma_f32_16x16x32_bf16 v[24:27], v[152:155], v[212:215], v[24:27]
	v_mfma_f32_16x16x32_bf16 v[20:23], v[160:163], v[212:215], v[20:23]
	v_mfma_f32_16x16x32_bf16 v[48:51], v[164:167], v[180:183], v[48:51]
	v_mfma_f32_16x16x32_bf16 v[44:47], v[172:175], v[180:183], v[44:47]
	v_mfma_f32_16x16x32_bf16 v[32:35], v[164:167], v[188:191], v[32:35]
	v_mfma_f32_16x16x32_bf16 v[28:31], v[172:175], v[188:191], v[28:31]
	v_mfma_f32_16x16x32_bf16 v[16:19], v[164:167], v[196:199], v[16:19]
	v_mfma_f32_16x16x32_bf16 v[12:15], v[172:175], v[196:199], v[12:15]
	v_mfma_f32_16x16x32_bf16 v[8:11], v[164:167], v[208:211], v[8:11]
	v_mfma_f32_16x16x32_bf16 v[4:7], v[172:175], v[208:211], v[4:7]
	v_mfma_f32_16x16x32_bf16 v[48:51], v[168:171], v[184:187], v[48:51]
	v_mfma_f32_16x16x32_bf16 v[44:47], v[176:179], v[184:187], v[44:47]
	v_mfma_f32_16x16x32_bf16 v[32:35], v[168:171], v[192:195], v[32:35]
	v_mfma_f32_16x16x32_bf16 v[28:31], v[176:179], v[192:195], v[28:31]
	v_mfma_f32_16x16x32_bf16 v[16:19], v[168:171], v[204:207], v[16:19]
	v_mfma_f32_16x16x32_bf16 v[12:15], v[176:179], v[204:207], v[12:15]
	v_mfma_f32_16x16x32_bf16 v[8:11], v[168:171], v[212:215], v[8:11]
	v_mfma_f32_16x16x32_bf16 v[4:7], v[176:179], v[212:215], v[4:7]
	s_setprio 0
	s_barrier
	s_add_i32 s69, s69, 2
	s_add_u32 s44, s44, 0x100
	s_addc_u32 s45, s45, 0
	s_cmp_gt_u32 s69, 13
.LBB0_1206:
	s_add_u32 s4, s22, s44
	s_addc_u32 s5, s23, s45
	s_add_u32 s70, s4, 0x100
	s_addc_u32 s71, s5, 0
	s_add_u32 s48, s65, s44
	s_addc_u32 s49, s68, s45
	s_add_u32 s4, s4, 0x180
	s_addc_u32 s5, s5, 0
	s_add_i32 s72, 0, 0x10000
	s_add_i32 s73, 0, 0x14000
	v_add_u32_e32 v160, s72, v146
	v_add_u32_e32 v176, s73, v146
	ds_read_b128 v[148:151], v160
	ds_read_b128 v[152:155], v160 offset:1024
	ds_read_b128 v[156:159], v160 offset:2048
	ds_read_b128 v[160:163], v160 offset:3072
	ds_read_b128 v[164:167], v176
	ds_read_b128 v[168:171], v176 offset:1024
	ds_read_b128 v[172:175], v176 offset:2048
	ds_read_b128 v[176:179], v176 offset:3072
	s_cmpk_eq_i32 s44, 0x700
	s_cselect_b32 s13, s64, s5
	s_cselect_b32 s12, s63, s4
	s_cselect_b32 s49, s21, s49
	s_cselect_b32 s48, s62, s48
	s_cselect_b32 s5, s37, s71
	s_cselect_b32 s4, s61, s70
	v_lshl_add_u64 v[216:217], v[142:143], 0, s[44:45]
	s_add_i32 m0, s17, 0xc000
	ds_read_b128 v[180:183], v147
	ds_read_b128 v[184:187], v147 offset:1024
	ds_read_b128 v[188:191], v147 offset:2048
	ds_read_b128 v[192:195], v147 offset:3072
	ds_read_b128 v[196:199], v147 offset:4096
	ds_read_b128 v[204:207], v147 offset:5120
	ds_read_b128 v[208:211], v147 offset:6144
	ds_read_b128 v[212:215], v147 offset:7168
	global_load_lds_dwordx4 v[216:217], off
	v_lshl_add_u64 v[216:217], v[144:145], 0, s[44:45]
	s_add_i32 m0, s17, 0xe000
	s_nop 0
	global_load_lds_dwordx4 v[216:217], off
	s_waitcnt vmcnt(8)
	s_waitcnt lgkmcnt(0)
	s_barrier
	s_setprio 1
	v_mfma_f32_16x16x32_bf16 v[128:131], v[148:151], v[180:183], v[128:131]
	v_mfma_f32_16x16x32_bf16 v[124:127], v[156:159], v[180:183], v[124:127]
	v_mfma_f32_16x16x32_bf16 v[120:123], v[148:151], v[188:191], v[120:123]
	v_mfma_f32_16x16x32_bf16 v[116:119], v[156:159], v[188:191], v[116:119]
	v_mfma_f32_16x16x32_bf16 v[104:107], v[148:151], v[196:199], v[104:107]
	v_mfma_f32_16x16x32_bf16 v[100:103], v[156:159], v[196:199], v[100:103]
	v_mfma_f32_16x16x32_bf16 v[88:91], v[148:151], v[208:211], v[88:91]
	v_mfma_f32_16x16x32_bf16 v[84:87], v[156:159], v[208:211], v[84:87]
	v_mfma_f32_16x16x32_bf16 v[128:131], v[152:155], v[184:187], v[128:131]
	v_mfma_f32_16x16x32_bf16 v[124:127], v[160:163], v[184:187], v[124:127]
	v_mfma_f32_16x16x32_bf16 v[120:123], v[152:155], v[192:195], v[120:123]
	v_mfma_f32_16x16x32_bf16 v[116:119], v[160:163], v[192:195], v[116:119]
	v_mfma_f32_16x16x32_bf16 v[104:107], v[152:155], v[204:207], v[104:107]
	v_mfma_f32_16x16x32_bf16 v[100:103], v[160:163], v[204:207], v[100:103]
	v_mfma_f32_16x16x32_bf16 v[88:91], v[152:155], v[212:215], v[88:91]
	v_mfma_f32_16x16x32_bf16 v[84:87], v[160:163], v[212:215], v[84:87]
	v_mfma_f32_16x16x32_bf16 v[112:115], v[164:167], v[180:183], v[112:115]
	v_mfma_f32_16x16x32_bf16 v[108:111], v[172:175], v[180:183], v[108:111]
	v_mfma_f32_16x16x32_bf16 v[96:99], v[164:167], v[188:191], v[96:99]
	v_mfma_f32_16x16x32_bf16 v[92:95], v[172:175], v[188:191], v[92:95]
	v_mfma_f32_16x16x32_bf16 v[80:83], v[164:167], v[196:199], v[80:83]
	v_mfma_f32_16x16x32_bf16 v[76:79], v[172:175], v[196:199], v[76:79]
	v_mfma_f32_16x16x32_bf16 v[72:75], v[164:167], v[208:211], v[72:75]
	v_mfma_f32_16x16x32_bf16 v[68:71], v[172:175], v[208:211], v[68:71]
	v_mfma_f32_16x16x32_bf16 v[112:115], v[168:171], v[184:187], v[112:115]
	v_mfma_f32_16x16x32_bf16 v[108:111], v[176:179], v[184:187], v[108:111]
	v_mfma_f32_16x16x32_bf16 v[96:99], v[168:171], v[192:195], v[96:99]
	v_mfma_f32_16x16x32_bf16 v[92:95], v[176:179], v[192:195], v[92:95]
	v_mfma_f32_16x16x32_bf16 v[80:83], v[168:171], v[204:207], v[80:83]
	v_mfma_f32_16x16x32_bf16 v[76:79], v[176:179], v[204:207], v[76:79]
	v_mfma_f32_16x16x32_bf16 v[72:75], v[168:171], v[212:215], v[72:75]
	v_mfma_f32_16x16x32_bf16 v[68:71], v[176:179], v[212:215], v[68:71]
	s_setprio 0
	s_barrier
	s_add_i32 s70, s72, s16
	v_lshl_add_u64 v[216:217], s[48:49], 0, v[2:3]
	s_mov_b32 m0, s70
	ds_read_b128 v[180:183], v147 offset:16384
	ds_read_b128 v[184:187], v147 offset:17408
	ds_read_b128 v[188:191], v147 offset:18432
	ds_read_b128 v[192:195], v147 offset:19456
	ds_read_b128 v[196:199], v147 offset:20480
	ds_read_b128 v[204:207], v147 offset:21504
	ds_read_b128 v[208:211], v147 offset:22528
	ds_read_b128 v[212:215], v147 offset:23552
	global_load_lds_dwordx4 v[216:217], off
	s_add_i32 m0, s70, 0x2000
	s_add_u32 s70, s48, 0x40000
	v_lshl_add_u64 v[218:219], s[48:49], 0, v[132:133]
	s_addc_u32 s71, s49, 0
	s_add_i32 s72, s73, s16
	global_load_lds_dwordx4 v[218:219], off
	v_lshl_add_u64 v[220:221], s[70:71], 0, v[2:3]
	s_mov_b32 m0, s72
	s_nop 0
	global_load_lds_dwordx4 v[220:221], off
	v_lshl_add_u64 v[220:221], s[70:71], 0, v[132:133]
	s_add_i32 m0, s72, 0x2000
	s_nop 0
	global_load_lds_dwordx4 v[220:221], off
	v_lshl_add_u64 v[220:221], s[4:5], 0, v[136:137]
	s_mov_b32 m0, s17
	s_nop 0
	global_load_lds_dwordx4 v[220:221], off
	v_lshl_add_u64 v[220:221], s[4:5], 0, v[134:135]
	s_mov_b32 m0, s46
	s_nop 0
	global_load_lds_dwordx4 v[220:221], off
	s_waitcnt vmcnt(8)
	s_waitcnt lgkmcnt(0)
	s_barrier
	s_setprio 1
	v_mfma_f32_16x16x32_bf16 v[64:67], v[148:151], v[180:183], v[64:67]
	v_mfma_f32_16x16x32_bf16 v[60:63], v[156:159], v[180:183], v[60:63]
	v_mfma_f32_16x16x32_bf16 v[56:59], v[148:151], v[188:191], v[56:59]
	v_mfma_f32_16x16x32_bf16 v[52:55], v[156:159], v[188:191], v[52:55]
	v_mfma_f32_16x16x32_bf16 v[40:43], v[148:151], v[196:199], v[40:43]
	v_mfma_f32_16x16x32_bf16 v[36:39], v[156:159], v[196:199], v[36:39]
	v_mfma_f32_16x16x32_bf16 v[24:27], v[148:151], v[208:211], v[24:27]
	v_mfma_f32_16x16x32_bf16 v[20:23], v[156:159], v[208:211], v[20:23]
	v_mfma_f32_16x16x32_bf16 v[64:67], v[152:155], v[184:187], v[64:67]
	v_mfma_f32_16x16x32_bf16 v[60:63], v[160:163], v[184:187], v[60:63]
	v_mfma_f32_16x16x32_bf16 v[56:59], v[152:155], v[192:195], v[56:59]
	v_mfma_f32_16x16x32_bf16 v[52:55], v[160:163], v[192:195], v[52:55]
	v_mfma_f32_16x16x32_bf16 v[40:43], v[152:155], v[204:207], v[40:43]
	v_mfma_f32_16x16x32_bf16 v[36:39], v[160:163], v[204:207], v[36:39]
	v_mfma_f32_16x16x32_bf16 v[24:27], v[152:155], v[212:215], v[24:27]
	v_mfma_f32_16x16x32_bf16 v[20:23], v[160:163], v[212:215], v[20:23]
	v_mfma_f32_16x16x32_bf16 v[48:51], v[164:167], v[180:183], v[48:51]
	v_mfma_f32_16x16x32_bf16 v[44:47], v[172:175], v[180:183], v[44:47]
	v_mfma_f32_16x16x32_bf16 v[32:35], v[164:167], v[188:191], v[32:35]
	v_mfma_f32_16x16x32_bf16 v[28:31], v[172:175], v[188:191], v[28:31]
	v_mfma_f32_16x16x32_bf16 v[16:19], v[164:167], v[196:199], v[16:19]
	v_mfma_f32_16x16x32_bf16 v[12:15], v[172:175], v[196:199], v[12:15]
	v_mfma_f32_16x16x32_bf16 v[8:11], v[164:167], v[208:211], v[8:11]
	v_mfma_f32_16x16x32_bf16 v[4:7], v[172:175], v[208:211], v[4:7]
	v_mfma_f32_16x16x32_bf16 v[48:51], v[168:171], v[184:187], v[48:51]
	v_mfma_f32_16x16x32_bf16 v[44:47], v[176:179], v[184:187], v[44:47]
	v_mfma_f32_16x16x32_bf16 v[32:35], v[168:171], v[192:195], v[32:35]
	v_mfma_f32_16x16x32_bf16 v[28:31], v[176:179], v[192:195], v[28:31]
	v_mfma_f32_16x16x32_bf16 v[16:19], v[168:171], v[204:207], v[16:19]
	v_mfma_f32_16x16x32_bf16 v[12:15], v[176:179], v[204:207], v[12:15]
	v_mfma_f32_16x16x32_bf16 v[8:11], v[168:171], v[212:215], v[8:11]
	v_mfma_f32_16x16x32_bf16 v[4:7], v[176:179], v[212:215], v[4:7]
	s_setprio 0
	s_barrier
	s_add_i32 s70, 0, 0x18000
	s_add_i32 s71, 0, 0x1c000
	v_add_u32_e32 v160, s70, v146
	v_add_u32_e32 v176, s71, v146
	ds_read_b128 v[148:151], v160
	ds_read_b128 v[152:155], v160 offset:1024
	ds_read_b128 v[156:159], v160 offset:2048
	ds_read_b128 v[160:163], v160 offset:3072
	ds_read_b128 v[164:167], v176
	ds_read_b128 v[168:171], v176 offset:1024
	ds_read_b128 v[172:175], v176 offset:2048
	ds_read_b128 v[176:179], v176 offset:3072
	s_add_u32 s4, s4, 0x40000
	s_addc_u32 s5, s5, 0
	s_mov_b32 m0, s47
	v_lshl_add_u64 v[220:221], s[4:5], 0, v[136:137]
	ds_read_b128 v[180:183], v147 offset:32768
	ds_read_b128 v[184:187], v147 offset:33792
	ds_read_b128 v[188:191], v147 offset:34816
	ds_read_b128 v[192:195], v147 offset:35840
	ds_read_b128 v[196:199], v147 offset:36864
	ds_read_b128 v[204:207], v147 offset:37888
	ds_read_b128 v[208:211], v147 offset:38912
	ds_read_b128 v[212:215], v147 offset:39936
	global_load_lds_dwordx4 v[220:221], off
	v_lshl_add_u64 v[220:221], s[4:5], 0, v[134:135]
	s_mov_b32 m0, s50
	s_nop 0
	global_load_lds_dwordx4 v[220:221], off
	s_waitcnt vmcnt(8)
	s_waitcnt lgkmcnt(0)
	s_barrier
	s_setprio 1
	v_mfma_f32_16x16x32_bf16 v[128:131], v[148:151], v[180:183], v[128:131]
	v_mfma_f32_16x16x32_bf16 v[124:127], v[156:159], v[180:183], v[124:127]
	v_mfma_f32_16x16x32_bf16 v[120:123], v[148:151], v[188:191], v[120:123]
	v_mfma_f32_16x16x32_bf16 v[116:119], v[156:159], v[188:191], v[116:119]
	v_mfma_f32_16x16x32_bf16 v[104:107], v[148:151], v[196:199], v[104:107]
	v_mfma_f32_16x16x32_bf16 v[100:103], v[156:159], v[196:199], v[100:103]
	v_mfma_f32_16x16x32_bf16 v[88:91], v[148:151], v[208:211], v[88:91]
	v_mfma_f32_16x16x32_bf16 v[84:87], v[156:159], v[208:211], v[84:87]
	v_mfma_f32_16x16x32_bf16 v[128:131], v[152:155], v[184:187], v[128:131]
	v_mfma_f32_16x16x32_bf16 v[124:127], v[160:163], v[184:187], v[124:127]
	v_mfma_f32_16x16x32_bf16 v[120:123], v[152:155], v[192:195], v[120:123]
	v_mfma_f32_16x16x32_bf16 v[116:119], v[160:163], v[192:195], v[116:119]
	v_mfma_f32_16x16x32_bf16 v[104:107], v[152:155], v[204:207], v[104:107]
	v_mfma_f32_16x16x32_bf16 v[100:103], v[160:163], v[204:207], v[100:103]
	v_mfma_f32_16x16x32_bf16 v[88:91], v[152:155], v[212:215], v[88:91]
	v_mfma_f32_16x16x32_bf16 v[84:87], v[160:163], v[212:215], v[84:87]
	v_mfma_f32_16x16x32_bf16 v[112:115], v[164:167], v[180:183], v[112:115]
	v_mfma_f32_16x16x32_bf16 v[108:111], v[172:175], v[180:183], v[108:111]
	v_mfma_f32_16x16x32_bf16 v[96:99], v[164:167], v[188:191], v[96:99]
	v_mfma_f32_16x16x32_bf16 v[92:95], v[172:175], v[188:191], v[92:95]
	v_mfma_f32_16x16x32_bf16 v[80:83], v[164:167], v[196:199], v[80:83]
	v_mfma_f32_16x16x32_bf16 v[76:79], v[172:175], v[196:199], v[76:79]
	v_mfma_f32_16x16x32_bf16 v[72:75], v[164:167], v[208:211], v[72:75]
	v_mfma_f32_16x16x32_bf16 v[68:71], v[172:175], v[208:211], v[68:71]
	v_mfma_f32_16x16x32_bf16 v[112:115], v[168:171], v[184:187], v[112:115]
	v_mfma_f32_16x16x32_bf16 v[108:111], v[176:179], v[184:187], v[108:111]
	v_mfma_f32_16x16x32_bf16 v[96:99], v[168:171], v[192:195], v[96:99]
	v_mfma_f32_16x16x32_bf16 v[92:95], v[176:179], v[192:195], v[92:95]
	v_mfma_f32_16x16x32_bf16 v[80:83], v[168:171], v[204:207], v[80:83]
	v_mfma_f32_16x16x32_bf16 v[76:79], v[176:179], v[204:207], v[76:79]
	v_mfma_f32_16x16x32_bf16 v[72:75], v[168:171], v[212:215], v[72:75]
	v_mfma_f32_16x16x32_bf16 v[68:71], v[176:179], v[212:215], v[68:71]
	s_setprio 0
	s_barrier
	s_add_i32 s4, s70, s16
	v_lshl_add_u64 v[216:217], v[216:217], 0, s[34:35]
	s_mov_b32 m0, s4
	ds_read_b128 v[180:183], v147 offset:49152
	ds_read_b128 v[184:187], v147 offset:50176
	ds_read_b128 v[188:191], v147 offset:51200
	ds_read_b128 v[192:195], v147 offset:52224
	ds_read_b128 v[196:199], v147 offset:53248
	ds_read_b128 v[204:207], v147 offset:54272
	ds_read_b128 v[208:211], v147 offset:55296
	ds_read_b128 v[212:215], v147 offset:56320
	global_load_lds_dwordx4 v[216:217], off
	s_add_i32 m0, s4, 0x2000
	s_add_u32 s4, s48, 0x40080
	v_lshl_add_u64 v[216:217], v[218:219], 0, s[34:35]
	s_addc_u32 s5, s49, 0
	s_add_i32 s48, s71, s16
	global_load_lds_dwordx4 v[216:217], off
	v_lshl_add_u64 v[216:217], s[4:5], 0, v[2:3]
	s_mov_b32 m0, s48
	s_nop 0
	global_load_lds_dwordx4 v[216:217], off
	v_lshl_add_u64 v[216:217], s[4:5], 0, v[132:133]
	s_add_i32 m0, s48, 0x2000
	s_nop 0
	global_load_lds_dwordx4 v[216:217], off
	v_lshl_add_u64 v[216:217], s[12:13], 0, v[136:137]
	s_mov_b32 m0, s53
	s_nop 0
	global_load_lds_dwordx4 v[216:217], off
	v_lshl_add_u64 v[216:217], s[12:13], 0, v[134:135]
	s_mov_b32 m0, s56
	s_nop 0
	global_load_lds_dwordx4 v[216:217], off
	s_waitcnt vmcnt(8)
	s_waitcnt lgkmcnt(0)
	s_barrier
	s_setprio 1
	v_mfma_f32_16x16x32_bf16 v[64:67], v[148:151], v[180:183], v[64:67]
	v_mfma_f32_16x16x32_bf16 v[60:63], v[156:159], v[180:183], v[60:63]
	v_mfma_f32_16x16x32_bf16 v[56:59], v[148:151], v[188:191], v[56:59]
	v_mfma_f32_16x16x32_bf16 v[52:55], v[156:159], v[188:191], v[52:55]
	v_mfma_f32_16x16x32_bf16 v[40:43], v[148:151], v[196:199], v[40:43]
	v_mfma_f32_16x16x32_bf16 v[36:39], v[156:159], v[196:199], v[36:39]
	v_mfma_f32_16x16x32_bf16 v[24:27], v[148:151], v[208:211], v[24:27]
	v_mfma_f32_16x16x32_bf16 v[20:23], v[156:159], v[208:211], v[20:23]
	v_mfma_f32_16x16x32_bf16 v[64:67], v[152:155], v[184:187], v[64:67]
	v_mfma_f32_16x16x32_bf16 v[60:63], v[160:163], v[184:187], v[60:63]
	v_mfma_f32_16x16x32_bf16 v[56:59], v[152:155], v[192:195], v[56:59]
	v_mfma_f32_16x16x32_bf16 v[52:55], v[160:163], v[192:195], v[52:55]
	v_mfma_f32_16x16x32_bf16 v[40:43], v[152:155], v[204:207], v[40:43]
	v_mfma_f32_16x16x32_bf16 v[36:39], v[160:163], v[204:207], v[36:39]
	v_mfma_f32_16x16x32_bf16 v[24:27], v[152:155], v[212:215], v[24:27]
	v_mfma_f32_16x16x32_bf16 v[20:23], v[160:163], v[212:215], v[20:23]
	v_mfma_f32_16x16x32_bf16 v[48:51], v[164:167], v[180:183], v[48:51]
	v_mfma_f32_16x16x32_bf16 v[44:47], v[172:175], v[180:183], v[44:47]
	v_mfma_f32_16x16x32_bf16 v[32:35], v[164:167], v[188:191], v[32:35]
	v_mfma_f32_16x16x32_bf16 v[28:31], v[172:175], v[188:191], v[28:31]
	v_mfma_f32_16x16x32_bf16 v[16:19], v[164:167], v[196:199], v[16:19]
	v_mfma_f32_16x16x32_bf16 v[12:15], v[172:175], v[196:199], v[12:15]
	v_mfma_f32_16x16x32_bf16 v[8:11], v[164:167], v[208:211], v[8:11]
	v_mfma_f32_16x16x32_bf16 v[4:7], v[172:175], v[208:211], v[4:7]
	v_mfma_f32_16x16x32_bf16 v[48:51], v[168:171], v[184:187], v[48:51]
	v_mfma_f32_16x16x32_bf16 v[44:47], v[176:179], v[184:187], v[44:47]
	v_mfma_f32_16x16x32_bf16 v[32:35], v[168:171], v[192:195], v[32:35]
	v_mfma_f32_16x16x32_bf16 v[28:31], v[176:179], v[192:195], v[28:31]
	v_mfma_f32_16x16x32_bf16 v[16:19], v[168:171], v[204:207], v[16:19]
	v_mfma_f32_16x16x32_bf16 v[12:15], v[176:179], v[204:207], v[12:15]
	v_mfma_f32_16x16x32_bf16 v[8:11], v[168:171], v[212:215], v[8:11]
	v_mfma_f32_16x16x32_bf16 v[4:7], v[176:179], v[212:215], v[4:7]
	s_setprio 0
	s_barrier
	s_add_i32 s69, s69, 2
	s_add_u32 s44, s44, 0x100
	s_addc_u32 s45, s45, 0
	s_cmp_gt_u32 s69, 13
	s_cbranch_scc0 .LBB0_1206
	s_and_b64 vcc, exec, s[18:19]
	s_mov_b32 s62, 0x18000
	s_mov_b32 s63, 0x1a000
	s_cbranch_vccz .LBB0_1209
	s_barrier

.LBB0_1379:
	s_ashr_i32 s43, s42, 31
	s_lshl_b64 s[4:5], s[42:43], 19
	s_add_u32 s44, s6, s4
	s_addc_u32 s45, s7, s5
	s_and_b64 s[4:5], s[38:39], exec
	s_cselect_b32 s43, s45, s41
	s_cselect_b32 s68, s44, s40
	s_ashr_i32 s37, s36, 31
	s_lshl_b64 s[4:5], s[36:37], 19
	s_add_u32 s48, s8, s4
	s_addc_u32 s49, s9, s5
	s_and_b64 s[4:5], s[38:39], exec
	s_cselect_b32 s37, s49, s51
	s_cselect_b32 s69, s48, s50
	s_add_u32 s70, s68, 0x80
	s_addc_u32 s71, s43, 0
	s_add_u32 s4, s40, 0x40080
	s_addc_u32 s5, s41, 0
	s_add_u32 s72, s50, 0x100
	v_lshl_add_u64 v[144:145], s[4:5], 0, v[140:141]
	v_lshl_add_u64 v[146:147], s[4:5], 0, v[142:143]
	s_addc_u32 s73, s51, 0
	s_mov_b32 s74, -2
	s_mov_b64 s[50:51], 0
	s_waitcnt vmcnt(0)
	s_add_u32 s4, s40, s50
	s_addc_u32 s5, s41, s51
	s_add_u32 s75, s4, 0x100
	s_addc_u32 s76, s5, 0
	s_add_u32 s52, s72, s50
	s_addc_u32 s53, s73, s51
	s_add_u32 s4, s4, 0x180
	s_addc_u32 s5, s5, 0
	s_add_i32 s77, 0, 0x10000
	s_add_i32 s78, 0, 0x14000
	v_add_u32_e32 v2, s77, v160
	ds_read_b128 v[148:151], v2
	ds_read_b128 v[152:155], v2 offset:1024
	ds_read_b128 v[156:159], v2 offset:2048
	ds_read_b128 v[162:165], v2 offset:3072
	v_add_u32_e32 v2, s78, v160
	ds_read_b128 v[166:169], v2
	s_waitcnt lgkmcnt(0)
	ds_read_b128 v[170:173], v2 offset:1024
	ds_read_b128 v[174:177], v2 offset:2048
	ds_read_b128 v[178:181], v2 offset:3072
	s_cmpk_eq_i32 s50, 0x700
	s_cselect_b32 s13, s71, s5
	s_cselect_b32 s12, s70, s4
	s_cselect_b32 s53, s37, s53
	s_cselect_b32 s52, s69, s52
	s_cselect_b32 s5, s43, s76
	s_cselect_b32 s4, s68, s75
	v_lshl_add_u64 v[198:199], v[144:145], 0, s[50:51]
	s_add_i32 m0, s17, 0xc000
	ds_read_b128 v[182:185], v161
	ds_read_b128 v[186:189], v161 offset:1024
	ds_read_b128 v[190:193], v161 offset:2048
	ds_read_b128 v[194:197], v161 offset:3072
	ds_read_b128 v[204:207], v161 offset:4096
	ds_read_b128 v[208:211], v161 offset:5120
	ds_read_b128 v[212:215], v161 offset:6144
	ds_read_b128 v[216:219], v161 offset:7168
	global_load_lds_dwordx4 v[198:199], off
	v_lshl_add_u64 v[198:199], v[146:147], 0, s[50:51]
	s_add_i32 m0, s17, 0xe000
	s_nop 0
	global_load_lds_dwordx4 v[198:199], off
	s_waitcnt vmcnt(8)
	s_waitcnt lgkmcnt(0)
	s_barrier
	s_setprio 1
	v_mfma_f32_16x16x32_bf16 v[128:131], v[148:151], v[182:185], 0
	v_mfma_f32_16x16x32_bf16 v[124:127], v[156:159], v[182:185], 0
	v_mfma_f32_16x16x32_bf16 v[112:115], v[148:151], v[190:193], 0
	v_mfma_f32_16x16x32_bf16 v[108:111], v[156:159], v[190:193], 0
	v_mfma_f32_16x16x32_bf16 v[96:99], v[148:151], v[204:207], 0
	v_mfma_f32_16x16x32_bf16 v[92:95], v[156:159], v[204:207], 0
	v_mfma_f32_16x16x32_bf16 v[80:83], v[148:151], v[212:215], 0
	v_mfma_f32_16x16x32_bf16 v[76:79], v[156:159], v[212:215], 0
	v_mfma_f32_16x16x32_bf16 v[128:131], v[152:155], v[186:189], v[128:131]
	v_mfma_f32_16x16x32_bf16 v[124:127], v[162:165], v[186:189], v[124:127]
	v_mfma_f32_16x16x32_bf16 v[112:115], v[152:155], v[194:197], v[112:115]
	v_mfma_f32_16x16x32_bf16 v[108:111], v[162:165], v[194:197], v[108:111]
	v_mfma_f32_16x16x32_bf16 v[96:99], v[152:155], v[208:211], v[96:99]
	v_mfma_f32_16x16x32_bf16 v[92:95], v[162:165], v[208:211], v[92:95]
	v_mfma_f32_16x16x32_bf16 v[80:83], v[152:155], v[216:219], v[80:83]
	v_mfma_f32_16x16x32_bf16 v[76:79], v[162:165], v[216:219], v[76:79]
	v_mfma_f32_16x16x32_bf16 v[120:123], v[166:169], v[182:185], 0
	v_mfma_f32_16x16x32_bf16 v[116:119], v[174:177], v[182:185], 0
	v_mfma_f32_16x16x32_bf16 v[104:107], v[166:169], v[190:193], 0
	v_mfma_f32_16x16x32_bf16 v[100:103], v[174:177], v[190:193], 0
	v_mfma_f32_16x16x32_bf16 v[88:91], v[166:169], v[204:207], 0
	v_mfma_f32_16x16x32_bf16 v[84:87], v[174:177], v[204:207], 0
	v_mfma_f32_16x16x32_bf16 v[72:75], v[166:169], v[212:215], 0
	v_mfma_f32_16x16x32_bf16 v[68:71], v[174:177], v[212:215], 0
	v_mfma_f32_16x16x32_bf16 v[120:123], v[170:173], v[186:189], v[120:123]
	v_mfma_f32_16x16x32_bf16 v[116:119], v[178:181], v[186:189], v[116:119]
	v_mfma_f32_16x16x32_bf16 v[104:107], v[170:173], v[194:197], v[104:107]
	v_mfma_f32_16x16x32_bf16 v[100:103], v[178:181], v[194:197], v[100:103]
	v_mfma_f32_16x16x32_bf16 v[88:91], v[170:173], v[208:211], v[88:91]
	v_mfma_f32_16x16x32_bf16 v[84:87], v[178:181], v[208:211], v[84:87]
	v_mfma_f32_16x16x32_bf16 v[72:75], v[170:173], v[216:219], v[72:75]
	v_mfma_f32_16x16x32_bf16 v[68:71], v[178:181], v[216:219], v[68:71]
	s_setprio 0
	s_barrier
	s_add_i32 s75, s77, s16
	v_lshl_add_u64 v[198:199], s[52:53], 0, v[136:137]
	s_mov_b32 m0, s75
	ds_read_b128 v[182:185], v161 offset:16384
	ds_read_b128 v[186:189], v161 offset:17408
	ds_read_b128 v[190:193], v161 offset:18432
	ds_read_b128 v[194:197], v161 offset:19456
	ds_read_b128 v[204:207], v161 offset:20480
	ds_read_b128 v[208:211], v161 offset:21504
	ds_read_b128 v[212:215], v161 offset:22528
	ds_read_b128 v[216:219], v161 offset:23552
	global_load_lds_dwordx4 v[198:199], off
	s_add_i32 m0, s75, 0x2000
	s_add_u32 s76, s52, 0x40000
	v_lshl_add_u64 v[220:221], s[52:53], 0, v[132:133]
	s_addc_u32 s77, s53, 0
	s_add_i32 s75, s78, s16
	global_load_lds_dwordx4 v[220:221], off
	v_lshl_add_u64 v[222:223], s[76:77], 0, v[136:137]
	s_mov_b32 m0, s75
	s_nop 0
	global_load_lds_dwordx4 v[222:223], off
	v_lshl_add_u64 v[222:223], s[76:77], 0, v[132:133]
	s_add_i32 m0, s75, 0x2000
	s_nop 0
	global_load_lds_dwordx4 v[222:223], off
	v_lshl_add_u64 v[222:223], s[4:5], 0, v[138:139]
	s_mov_b32 m0, s17
	s_nop 0
	global_load_lds_dwordx4 v[222:223], off
	v_lshl_add_u64 v[222:223], s[4:5], 0, v[134:135]
	s_mov_b32 m0, s46
	s_nop 0
	global_load_lds_dwordx4 v[222:223], off
	s_waitcnt vmcnt(8)
	s_waitcnt lgkmcnt(0)
	s_barrier
	s_setprio 1
	v_mfma_f32_16x16x32_bf16 v[64:67], v[148:151], v[182:185], 0
	v_mfma_f32_16x16x32_bf16 v[60:63], v[156:159], v[182:185], 0
	v_mfma_f32_16x16x32_bf16 v[48:51], v[148:151], v[190:193], 0
	v_mfma_f32_16x16x32_bf16 v[44:47], v[156:159], v[190:193], 0
	v_mfma_f32_16x16x32_bf16 v[32:35], v[148:151], v[204:207], 0
	v_mfma_f32_16x16x32_bf16 v[28:31], v[156:159], v[204:207], 0
	v_mfma_f32_16x16x32_bf16 v[16:19], v[148:151], v[212:215], 0
	v_mfma_f32_16x16x32_bf16 v[12:15], v[156:159], v[212:215], 0
	v_mfma_f32_16x16x32_bf16 v[64:67], v[152:155], v[186:189], v[64:67]
	v_mfma_f32_16x16x32_bf16 v[60:63], v[162:165], v[186:189], v[60:63]
	v_mfma_f32_16x16x32_bf16 v[48:51], v[152:155], v[194:197], v[48:51]
	v_mfma_f32_16x16x32_bf16 v[44:47], v[162:165], v[194:197], v[44:47]
	v_mfma_f32_16x16x32_bf16 v[32:35], v[152:155], v[208:211], v[32:35]
	v_mfma_f32_16x16x32_bf16 v[28:31], v[162:165], v[208:211], v[28:31]
	v_mfma_f32_16x16x32_bf16 v[16:19], v[152:155], v[216:219], v[16:19]
	v_mfma_f32_16x16x32_bf16 v[12:15], v[162:165], v[216:219], v[12:15]
	v_mfma_f32_16x16x32_bf16 v[56:59], v[166:169], v[182:185], 0
	v_mfma_f32_16x16x32_bf16 v[52:55], v[174:177], v[182:185], 0
	v_mfma_f32_16x16x32_bf16 v[40:43], v[166:169], v[190:193], 0
	v_mfma_f32_16x16x32_bf16 v[36:39], v[174:177], v[190:193], 0
	v_mfma_f32_16x16x32_bf16 v[24:27], v[166:169], v[204:207], 0
	v_mfma_f32_16x16x32_bf16 v[20:23], v[174:177], v[204:207], 0
	v_mfma_f32_16x16x32_bf16 v[8:11], v[166:169], v[212:215], 0
	v_mfma_f32_16x16x32_bf16 v[4:7], v[174:177], v[212:215], 0
	v_mfma_f32_16x16x32_bf16 v[56:59], v[170:173], v[186:189], v[56:59]
	v_mfma_f32_16x16x32_bf16 v[52:55], v[178:181], v[186:189], v[52:55]
	v_mfma_f32_16x16x32_bf16 v[40:43], v[170:173], v[194:197], v[40:43]
	v_mfma_f32_16x16x32_bf16 v[36:39], v[178:181], v[194:197], v[36:39]
	v_mfma_f32_16x16x32_bf16 v[24:27], v[170:173], v[208:211], v[24:27]
	v_mfma_f32_16x16x32_bf16 v[20:23], v[178:181], v[208:211], v[20:23]
	v_mfma_f32_16x16x32_bf16 v[8:11], v[170:173], v[216:219], v[8:11]
	v_mfma_f32_16x16x32_bf16 v[4:7], v[178:181], v[216:219], v[4:7]
	s_setprio 0
	s_barrier
	s_add_i32 s75, 0, 0x18000
	v_add_u32_e32 v2, s75, v160
	s_add_i32 s76, 0, 0x1c000
	ds_read_b128 v[148:151], v2
	ds_read_b128 v[152:155], v2 offset:1024
	ds_read_b128 v[156:159], v2 offset:2048
	ds_read_b128 v[162:165], v2 offset:3072
	v_add_u32_e32 v2, s76, v160
	ds_read_b128 v[166:169], v2
	ds_read_b128 v[170:173], v2 offset:1024
	ds_read_b128 v[174:177], v2 offset:2048
	ds_read_b128 v[178:181], v2 offset:3072
	s_add_u32 s4, s4, 0x40000
	s_addc_u32 s5, s5, 0
	s_mov_b32 m0, s47
	v_lshl_add_u64 v[222:223], s[4:5], 0, v[138:139]
	ds_read_b128 v[182:185], v161 offset:32768
	ds_read_b128 v[186:189], v161 offset:33792
	ds_read_b128 v[190:193], v161 offset:34816
	ds_read_b128 v[194:197], v161 offset:35840
	ds_read_b128 v[204:207], v161 offset:36864
	ds_read_b128 v[208:211], v161 offset:37888
	ds_read_b128 v[212:215], v161 offset:38912
	ds_read_b128 v[216:219], v161 offset:39936
	global_load_lds_dwordx4 v[222:223], off
	v_lshl_add_u64 v[222:223], s[4:5], 0, v[134:135]
	s_mov_b32 m0, s56
	s_nop 0
	global_load_lds_dwordx4 v[222:223], off
	s_waitcnt vmcnt(8)
	s_waitcnt lgkmcnt(0)
	s_barrier
	s_setprio 1
	v_mfma_f32_16x16x32_bf16 v[128:131], v[148:151], v[182:185], v[128:131]
	v_mfma_f32_16x16x32_bf16 v[124:127], v[156:159], v[182:185], v[124:127]
	v_mfma_f32_16x16x32_bf16 v[112:115], v[148:151], v[190:193], v[112:115]
	v_mfma_f32_16x16x32_bf16 v[108:111], v[156:159], v[190:193], v[108:111]
	v_mfma_f32_16x16x32_bf16 v[96:99], v[148:151], v[204:207], v[96:99]
	v_mfma_f32_16x16x32_bf16 v[92:95], v[156:159], v[204:207], v[92:95]
	v_mfma_f32_16x16x32_bf16 v[80:83], v[148:151], v[212:215], v[80:83]
	v_mfma_f32_16x16x32_bf16 v[76:79], v[156:159], v[212:215], v[76:79]
	v_mfma_f32_16x16x32_bf16 v[128:131], v[152:155], v[186:189], v[128:131]
	v_mfma_f32_16x16x32_bf16 v[124:127], v[162:165], v[186:189], v[124:127]
	v_mfma_f32_16x16x32_bf16 v[112:115], v[152:155], v[194:197], v[112:115]
	v_mfma_f32_16x16x32_bf16 v[108:111], v[162:165], v[194:197], v[108:111]
	v_mfma_f32_16x16x32_bf16 v[96:99], v[152:155], v[208:211], v[96:99]
	v_mfma_f32_16x16x32_bf16 v[92:95], v[162:165], v[208:211], v[92:95]
	v_mfma_f32_16x16x32_bf16 v[80:83], v[152:155], v[216:219], v[80:83]
	v_mfma_f32_16x16x32_bf16 v[76:79], v[162:165], v[216:219], v[76:79]
	v_mfma_f32_16x16x32_bf16 v[120:123], v[166:169], v[182:185], v[120:123]
	v_mfma_f32_16x16x32_bf16 v[116:119], v[174:177], v[182:185], v[116:119]
	v_mfma_f32_16x16x32_bf16 v[104:107], v[166:169], v[190:193], v[104:107]
	v_mfma_f32_16x16x32_bf16 v[100:103], v[174:177], v[190:193], v[100:103]
	v_mfma_f32_16x16x32_bf16 v[88:91], v[166:169], v[204:207], v[88:91]
	v_mfma_f32_16x16x32_bf16 v[84:87], v[174:177], v[204:207], v[84:87]
	v_mfma_f32_16x16x32_bf16 v[72:75], v[166:169], v[212:215], v[72:75]
	v_mfma_f32_16x16x32_bf16 v[68:71], v[174:177], v[212:215], v[68:71]
	v_mfma_f32_16x16x32_bf16 v[120:123], v[170:173], v[186:189], v[120:123]
	v_mfma_f32_16x16x32_bf16 v[116:119], v[178:181], v[186:189], v[116:119]
	v_mfma_f32_16x16x32_bf16 v[104:107], v[170:173], v[194:197], v[104:107]
	v_mfma_f32_16x16x32_bf16 v[100:103], v[178:181], v[194:197], v[100:103]
	v_mfma_f32_16x16x32_bf16 v[88:91], v[170:173], v[208:211], v[88:91]
	v_mfma_f32_16x16x32_bf16 v[84:87], v[178:181], v[208:211], v[84:87]
	v_mfma_f32_16x16x32_bf16 v[72:75], v[170:173], v[216:219], v[72:75]
	v_mfma_f32_16x16x32_bf16 v[68:71], v[178:181], v[216:219], v[68:71]
	s_setprio 0
	s_barrier
	s_add_i32 s4, s75, s16
	v_lshl_add_u64 v[198:199], v[198:199], 0, s[34:35]
	s_mov_b32 m0, s4
	ds_read_b128 v[182:185], v161 offset:49152
	ds_read_b128 v[186:189], v161 offset:50176
	ds_read_b128 v[190:193], v161 offset:51200
	ds_read_b128 v[194:197], v161 offset:52224
	ds_read_b128 v[204:207], v161 offset:53248
	ds_read_b128 v[208:211], v161 offset:54272
	ds_read_b128 v[212:215], v161 offset:55296
	ds_read_b128 v[216:219], v161 offset:56320
	global_load_lds_dwordx4 v[198:199], off
	s_add_i32 m0, s4, 0x2000
	s_add_u32 s4, s52, 0x40080
	v_lshl_add_u64 v[198:199], v[220:221], 0, s[34:35]
	s_addc_u32 s5, s53, 0
	s_add_i32 s52, s76, s16
	global_load_lds_dwordx4 v[198:199], off
	v_lshl_add_u64 v[198:199], s[4:5], 0, v[136:137]
	s_mov_b32 m0, s52
	s_nop 0
	global_load_lds_dwordx4 v[198:199], off
	v_lshl_add_u64 v[198:199], s[4:5], 0, v[132:133]
	s_add_i32 m0, s52, 0x2000
	s_nop 0
	global_load_lds_dwordx4 v[198:199], off
	v_lshl_add_u64 v[198:199], s[12:13], 0, v[138:139]
	s_mov_b32 m0, s61
	s_nop 0
	global_load_lds_dwordx4 v[198:199], off
	v_lshl_add_u64 v[198:199], s[12:13], 0, v[134:135]
	s_mov_b32 m0, s62
	s_nop 0
	global_load_lds_dwordx4 v[198:199], off
	s_waitcnt vmcnt(8)
	s_waitcnt lgkmcnt(0)
	s_barrier
	s_setprio 1
	v_mfma_f32_16x16x32_bf16 v[64:67], v[148:151], v[182:185], v[64:67]
	v_mfma_f32_16x16x32_bf16 v[60:63], v[156:159], v[182:185], v[60:63]
	v_mfma_f32_16x16x32_bf16 v[48:51], v[148:151], v[190:193], v[48:51]
	v_mfma_f32_16x16x32_bf16 v[44:47], v[156:159], v[190:193], v[44:47]
	v_mfma_f32_16x16x32_bf16 v[32:35], v[148:151], v[204:207], v[32:35]
	v_mfma_f32_16x16x32_bf16 v[28:31], v[156:159], v[204:207], v[28:31]
	v_mfma_f32_16x16x32_bf16 v[16:19], v[148:151], v[212:215], v[16:19]
	v_mfma_f32_16x16x32_bf16 v[12:15], v[156:159], v[212:215], v[12:15]
	v_mfma_f32_16x16x32_bf16 v[64:67], v[152:155], v[186:189], v[64:67]
	v_mfma_f32_16x16x32_bf16 v[60:63], v[162:165], v[186:189], v[60:63]
	v_mfma_f32_16x16x32_bf16 v[48:51], v[152:155], v[194:197], v[48:51]
	v_mfma_f32_16x16x32_bf16 v[44:47], v[162:165], v[194:197], v[44:47]
	v_mfma_f32_16x16x32_bf16 v[32:35], v[152:155], v[208:211], v[32:35]
	v_mfma_f32_16x16x32_bf16 v[28:31], v[162:165], v[208:211], v[28:31]
	v_mfma_f32_16x16x32_bf16 v[16:19], v[152:155], v[216:219], v[16:19]
	v_mfma_f32_16x16x32_bf16 v[12:15], v[162:165], v[216:219], v[12:15]
	v_mfma_f32_16x16x32_bf16 v[56:59], v[166:169], v[182:185], v[56:59]
	v_mfma_f32_16x16x32_bf16 v[52:55], v[174:177], v[182:185], v[52:55]
	v_mfma_f32_16x16x32_bf16 v[40:43], v[166:169], v[190:193], v[40:43]
	v_mfma_f32_16x16x32_bf16 v[36:39], v[174:177], v[190:193], v[36:39]
	v_mfma_f32_16x16x32_bf16 v[24:27], v[166:169], v[204:207], v[24:27]
	v_mfma_f32_16x16x32_bf16 v[20:23], v[174:177], v[204:207], v[20:23]
	v_mfma_f32_16x16x32_bf16 v[8:11], v[166:169], v[212:215], v[8:11]
	v_mfma_f32_16x16x32_bf16 v[4:7], v[174:177], v[212:215], v[4:7]
	v_mfma_f32_16x16x32_bf16 v[56:59], v[170:173], v[186:189], v[56:59]
	v_mfma_f32_16x16x32_bf16 v[52:55], v[178:181], v[186:189], v[52:55]
	v_mfma_f32_16x16x32_bf16 v[40:43], v[170:173], v[194:197], v[40:43]
	v_mfma_f32_16x16x32_bf16 v[36:39], v[178:181], v[194:197], v[36:39]
	v_mfma_f32_16x16x32_bf16 v[24:27], v[170:173], v[208:211], v[24:27]
	v_mfma_f32_16x16x32_bf16 v[20:23], v[178:181], v[208:211], v[20:23]
	v_mfma_f32_16x16x32_bf16 v[8:11], v[170:173], v[216:219], v[8:11]
	v_mfma_f32_16x16x32_bf16 v[4:7], v[178:181], v[216:219], v[4:7]
	s_setprio 0
	s_barrier
	s_add_i32 s74, s74, 2
	s_add_u32 s50, s50, 0x100
	s_addc_u32 s51, s51, 0
	s_cmp_gt_u32 s74, 13
.LBB0_1380:
	s_add_u32 s4, s40, s50
	s_addc_u32 s5, s41, s51
	s_add_u32 s75, s4, 0x100
	s_addc_u32 s76, s5, 0
	s_add_u32 s52, s72, s50
	s_addc_u32 s53, s73, s51
	s_add_u32 s4, s4, 0x180
	s_addc_u32 s5, s5, 0
	s_add_i32 s77, 0, 0x10000
	s_add_i32 s78, 0, 0x14000
	v_add_u32_e32 v2, s77, v160
	ds_read_b128 v[148:151], v2
	ds_read_b128 v[152:155], v2 offset:1024
	ds_read_b128 v[156:159], v2 offset:2048
	ds_read_b128 v[162:165], v2 offset:3072
	v_add_u32_e32 v2, s78, v160
	ds_read_b128 v[166:169], v2
	s_waitcnt lgkmcnt(0)
	ds_read_b128 v[170:173], v2 offset:1024
	ds_read_b128 v[174:177], v2 offset:2048
	ds_read_b128 v[178:181], v2 offset:3072
	s_cmpk_eq_i32 s50, 0x700
	s_cselect_b32 s13, s71, s5
	s_cselect_b32 s12, s70, s4
	s_cselect_b32 s53, s37, s53
	s_cselect_b32 s52, s69, s52
	s_cselect_b32 s5, s43, s76
	s_cselect_b32 s4, s68, s75
	v_lshl_add_u64 v[198:199], v[144:145], 0, s[50:51]
	s_add_i32 m0, s17, 0xc000
	ds_read_b128 v[182:185], v161
	ds_read_b128 v[186:189], v161 offset:1024
	ds_read_b128 v[190:193], v161 offset:2048
	ds_read_b128 v[194:197], v161 offset:3072
	ds_read_b128 v[204:207], v161 offset:4096
	ds_read_b128 v[208:211], v161 offset:5120
	ds_read_b128 v[212:215], v161 offset:6144
	ds_read_b128 v[216:219], v161 offset:7168
	global_load_lds_dwordx4 v[198:199], off
	v_lshl_add_u64 v[198:199], v[146:147], 0, s[50:51]
	s_add_i32 m0, s17, 0xe000
	s_nop 0
	global_load_lds_dwordx4 v[198:199], off
	s_waitcnt vmcnt(8)
	s_waitcnt lgkmcnt(0)
	s_barrier
	s_setprio 1
	v_mfma_f32_16x16x32_bf16 v[128:131], v[148:151], v[182:185], v[128:131]
	v_mfma_f32_16x16x32_bf16 v[124:127], v[156:159], v[182:185], v[124:127]
	v_mfma_f32_16x16x32_bf16 v[112:115], v[148:151], v[190:193], v[112:115]
	v_mfma_f32_16x16x32_bf16 v[108:111], v[156:159], v[190:193], v[108:111]
	v_mfma_f32_16x16x32_bf16 v[96:99], v[148:151], v[204:207], v[96:99]
	v_mfma_f32_16x16x32_bf16 v[92:95], v[156:159], v[204:207], v[92:95]
	v_mfma_f32_16x16x32_bf16 v[80:83], v[148:151], v[212:215], v[80:83]
	v_mfma_f32_16x16x32_bf16 v[76:79], v[156:159], v[212:215], v[76:79]
	v_mfma_f32_16x16x32_bf16 v[128:131], v[152:155], v[186:189], v[128:131]
	v_mfma_f32_16x16x32_bf16 v[124:127], v[162:165], v[186:189], v[124:127]
	v_mfma_f32_16x16x32_bf16 v[112:115], v[152:155], v[194:197], v[112:115]
	v_mfma_f32_16x16x32_bf16 v[108:111], v[162:165], v[194:197], v[108:111]
	v_mfma_f32_16x16x32_bf16 v[96:99], v[152:155], v[208:211], v[96:99]
	v_mfma_f32_16x16x32_bf16 v[92:95], v[162:165], v[208:211], v[92:95]
	v_mfma_f32_16x16x32_bf16 v[80:83], v[152:155], v[216:219], v[80:83]
	v_mfma_f32_16x16x32_bf16 v[76:79], v[162:165], v[216:219], v[76:79]
	v_mfma_f32_16x16x32_bf16 v[120:123], v[166:169], v[182:185], v[120:123]
	v_mfma_f32_16x16x32_bf16 v[116:119], v[174:177], v[182:185], v[116:119]
	v_mfma_f32_16x16x32_bf16 v[104:107], v[166:169], v[190:193], v[104:107]
	v_mfma_f32_16x16x32_bf16 v[100:103], v[174:177], v[190:193], v[100:103]
	v_mfma_f32_16x16x32_bf16 v[88:91], v[166:169], v[204:207], v[88:91]
	v_mfma_f32_16x16x32_bf16 v[84:87], v[174:177], v[204:207], v[84:87]
	v_mfma_f32_16x16x32_bf16 v[72:75], v[166:169], v[212:215], v[72:75]
	v_mfma_f32_16x16x32_bf16 v[68:71], v[174:177], v[212:215], v[68:71]
	v_mfma_f32_16x16x32_bf16 v[120:123], v[170:173], v[186:189], v[120:123]
	v_mfma_f32_16x16x32_bf16 v[116:119], v[178:181], v[186:189], v[116:119]
	v_mfma_f32_16x16x32_bf16 v[104:107], v[170:173], v[194:197], v[104:107]
	v_mfma_f32_16x16x32_bf16 v[100:103], v[178:181], v[194:197], v[100:103]
	v_mfma_f32_16x16x32_bf16 v[88:91], v[170:173], v[208:211], v[88:91]
	v_mfma_f32_16x16x32_bf16 v[84:87], v[178:181], v[208:211], v[84:87]
	v_mfma_f32_16x16x32_bf16 v[72:75], v[170:173], v[216:219], v[72:75]
	v_mfma_f32_16x16x32_bf16 v[68:71], v[178:181], v[216:219], v[68:71]
	s_setprio 0
	s_barrier
	s_add_i32 s75, s77, s16
	v_lshl_add_u64 v[198:199], s[52:53], 0, v[136:137]
	s_mov_b32 m0, s75
	ds_read_b128 v[182:185], v161 offset:16384
	ds_read_b128 v[186:189], v161 offset:17408
	ds_read_b128 v[190:193], v161 offset:18432
	ds_read_b128 v[194:197], v161 offset:19456
	ds_read_b128 v[204:207], v161 offset:20480
	ds_read_b128 v[208:211], v161 offset:21504
	ds_read_b128 v[212:215], v161 offset:22528
	ds_read_b128 v[216:219], v161 offset:23552
	global_load_lds_dwordx4 v[198:199], off
	s_add_i32 m0, s75, 0x2000
	s_add_u32 s76, s52, 0x40000
	v_lshl_add_u64 v[220:221], s[52:53], 0, v[132:133]
	s_addc_u32 s77, s53, 0
	s_add_i32 s75, s78, s16
	global_load_lds_dwordx4 v[220:221], off
	v_lshl_add_u64 v[222:223], s[76:77], 0, v[136:137]
	s_mov_b32 m0, s75
	s_nop 0
	global_load_lds_dwordx4 v[222:223], off
	v_lshl_add_u64 v[222:223], s[76:77], 0, v[132:133]
	s_add_i32 m0, s75, 0x2000
	s_nop 0
	global_load_lds_dwordx4 v[222:223], off
	v_lshl_add_u64 v[222:223], s[4:5], 0, v[138:139]
	s_mov_b32 m0, s17
	s_nop 0
	global_load_lds_dwordx4 v[222:223], off
	v_lshl_add_u64 v[222:223], s[4:5], 0, v[134:135]
	s_mov_b32 m0, s46
	s_nop 0
	global_load_lds_dwordx4 v[222:223], off
	s_waitcnt vmcnt(8)
	s_waitcnt lgkmcnt(0)
	s_barrier
	s_setprio 1
	v_mfma_f32_16x16x32_bf16 v[64:67], v[148:151], v[182:185], v[64:67]
	v_mfma_f32_16x16x32_bf16 v[60:63], v[156:159], v[182:185], v[60:63]
	v_mfma_f32_16x16x32_bf16 v[48:51], v[148:151], v[190:193], v[48:51]
	v_mfma_f32_16x16x32_bf16 v[44:47], v[156:159], v[190:193], v[44:47]
	v_mfma_f32_16x16x32_bf16 v[32:35], v[148:151], v[204:207], v[32:35]
	v_mfma_f32_16x16x32_bf16 v[28:31], v[156:159], v[204:207], v[28:31]
	v_mfma_f32_16x16x32_bf16 v[16:19], v[148:151], v[212:215], v[16:19]
	v_mfma_f32_16x16x32_bf16 v[12:15], v[156:159], v[212:215], v[12:15]
	v_mfma_f32_16x16x32_bf16 v[64:67], v[152:155], v[186:189], v[64:67]
	v_mfma_f32_16x16x32_bf16 v[60:63], v[162:165], v[186:189], v[60:63]
	v_mfma_f32_16x16x32_bf16 v[48:51], v[152:155], v[194:197], v[48:51]
	v_mfma_f32_16x16x32_bf16 v[44:47], v[162:165], v[194:197], v[44:47]
	v_mfma_f32_16x16x32_bf16 v[32:35], v[152:155], v[208:211], v[32:35]
	v_mfma_f32_16x16x32_bf16 v[28:31], v[162:165], v[208:211], v[28:31]
	v_mfma_f32_16x16x32_bf16 v[16:19], v[152:155], v[216:219], v[16:19]
	v_mfma_f32_16x16x32_bf16 v[12:15], v[162:165], v[216:219], v[12:15]
	v_mfma_f32_16x16x32_bf16 v[56:59], v[166:169], v[182:185], v[56:59]
	v_mfma_f32_16x16x32_bf16 v[52:55], v[174:177], v[182:185], v[52:55]
	v_mfma_f32_16x16x32_bf16 v[40:43], v[166:169], v[190:193], v[40:43]
	v_mfma_f32_16x16x32_bf16 v[36:39], v[174:177], v[190:193], v[36:39]
	v_mfma_f32_16x16x32_bf16 v[24:27], v[166:169], v[204:207], v[24:27]
	v_mfma_f32_16x16x32_bf16 v[20:23], v[174:177], v[204:207], v[20:23]
	v_mfma_f32_16x16x32_bf16 v[8:11], v[166:169], v[212:215], v[8:11]
	v_mfma_f32_16x16x32_bf16 v[4:7], v[174:177], v[212:215], v[4:7]
	v_mfma_f32_16x16x32_bf16 v[56:59], v[170:173], v[186:189], v[56:59]
	v_mfma_f32_16x16x32_bf16 v[52:55], v[178:181], v[186:189], v[52:55]
	v_mfma_f32_16x16x32_bf16 v[40:43], v[170:173], v[194:197], v[40:43]
	v_mfma_f32_16x16x32_bf16 v[36:39], v[178:181], v[194:197], v[36:39]
	v_mfma_f32_16x16x32_bf16 v[24:27], v[170:173], v[208:211], v[24:27]
	v_mfma_f32_16x16x32_bf16 v[20:23], v[178:181], v[208:211], v[20:23]
	v_mfma_f32_16x16x32_bf16 v[8:11], v[170:173], v[216:219], v[8:11]
	v_mfma_f32_16x16x32_bf16 v[4:7], v[178:181], v[216:219], v[4:7]
	s_setprio 0
	s_barrier
	s_add_i32 s75, 0, 0x18000
	v_add_u32_e32 v2, s75, v160
	s_add_i32 s76, 0, 0x1c000
	ds_read_b128 v[148:151], v2
	ds_read_b128 v[152:155], v2 offset:1024
	ds_read_b128 v[156:159], v2 offset:2048
	ds_read_b128 v[162:165], v2 offset:3072
	v_add_u32_e32 v2, s76, v160
	ds_read_b128 v[166:169], v2
	ds_read_b128 v[170:173], v2 offset:1024
	ds_read_b128 v[174:177], v2 offset:2048
	ds_read_b128 v[178:181], v2 offset:3072
	s_add_u32 s4, s4, 0x40000
	s_addc_u32 s5, s5, 0
	s_mov_b32 m0, s47
	v_lshl_add_u64 v[222:223], s[4:5], 0, v[138:139]
	ds_read_b128 v[182:185], v161 offset:32768
	ds_read_b128 v[186:189], v161 offset:33792
	ds_read_b128 v[190:193], v161 offset:34816
	ds_read_b128 v[194:197], v161 offset:35840
	ds_read_b128 v[204:207], v161 offset:36864
	ds_read_b128 v[208:211], v161 offset:37888
	ds_read_b128 v[212:215], v161 offset:38912
	ds_read_b128 v[216:219], v161 offset:39936
	global_load_lds_dwordx4 v[222:223], off
	v_lshl_add_u64 v[222:223], s[4:5], 0, v[134:135]
	s_mov_b32 m0, s56
	s_nop 0
	global_load_lds_dwordx4 v[222:223], off
	s_waitcnt vmcnt(8)
	s_waitcnt lgkmcnt(0)
	s_barrier
	s_setprio 1
	v_mfma_f32_16x16x32_bf16 v[128:131], v[148:151], v[182:185], v[128:131]
	v_mfma_f32_16x16x32_bf16 v[124:127], v[156:159], v[182:185], v[124:127]
	v_mfma_f32_16x16x32_bf16 v[112:115], v[148:151], v[190:193], v[112:115]
	v_mfma_f32_16x16x32_bf16 v[108:111], v[156:159], v[190:193], v[108:111]
	v_mfma_f32_16x16x32_bf16 v[96:99], v[148:151], v[204:207], v[96:99]
	v_mfma_f32_16x16x32_bf16 v[92:95], v[156:159], v[204:207], v[92:95]
	v_mfma_f32_16x16x32_bf16 v[80:83], v[148:151], v[212:215], v[80:83]
	v_mfma_f32_16x16x32_bf16 v[76:79], v[156:159], v[212:215], v[76:79]
	v_mfma_f32_16x16x32_bf16 v[128:131], v[152:155], v[186:189], v[128:131]
	v_mfma_f32_16x16x32_bf16 v[124:127], v[162:165], v[186:189], v[124:127]
	v_mfma_f32_16x16x32_bf16 v[112:115], v[152:155], v[194:197], v[112:115]
	v_mfma_f32_16x16x32_bf16 v[108:111], v[162:165], v[194:197], v[108:111]
	v_mfma_f32_16x16x32_bf16 v[96:99], v[152:155], v[208:211], v[96:99]
	v_mfma_f32_16x16x32_bf16 v[92:95], v[162:165], v[208:211], v[92:95]
	v_mfma_f32_16x16x32_bf16 v[80:83], v[152:155], v[216:219], v[80:83]
	v_mfma_f32_16x16x32_bf16 v[76:79], v[162:165], v[216:219], v[76:79]
	v_mfma_f32_16x16x32_bf16 v[120:123], v[166:169], v[182:185], v[120:123]
	v_mfma_f32_16x16x32_bf16 v[116:119], v[174:177], v[182:185], v[116:119]
	v_mfma_f32_16x16x32_bf16 v[104:107], v[166:169], v[190:193], v[104:107]
	v_mfma_f32_16x16x32_bf16 v[100:103], v[174:177], v[190:193], v[100:103]
	v_mfma_f32_16x16x32_bf16 v[88:91], v[166:169], v[204:207], v[88:91]
	v_mfma_f32_16x16x32_bf16 v[84:87], v[174:177], v[204:207], v[84:87]
	v_mfma_f32_16x16x32_bf16 v[72:75], v[166:169], v[212:215], v[72:75]
	v_mfma_f32_16x16x32_bf16 v[68:71], v[174:177], v[212:215], v[68:71]
	v_mfma_f32_16x16x32_bf16 v[120:123], v[170:173], v[186:189], v[120:123]
	v_mfma_f32_16x16x32_bf16 v[116:119], v[178:181], v[186:189], v[116:119]
	v_mfma_f32_16x16x32_bf16 v[104:107], v[170:173], v[194:197], v[104:107]
	v_mfma_f32_16x16x32_bf16 v[100:103], v[178:181], v[194:197], v[100:103]
	v_mfma_f32_16x16x32_bf16 v[88:91], v[170:173], v[208:211], v[88:91]
	v_mfma_f32_16x16x32_bf16 v[84:87], v[178:181], v[208:211], v[84:87]
	v_mfma_f32_16x16x32_bf16 v[72:75], v[170:173], v[216:219], v[72:75]
	v_mfma_f32_16x16x32_bf16 v[68:71], v[178:181], v[216:219], v[68:71]
	s_setprio 0
	s_barrier
	s_add_i32 s4, s75, s16
	v_lshl_add_u64 v[198:199], v[198:199], 0, s[34:35]
	s_mov_b32 m0, s4
	ds_read_b128 v[182:185], v161 offset:49152
	ds_read_b128 v[186:189], v161 offset:50176
	ds_read_b128 v[190:193], v161 offset:51200
	ds_read_b128 v[194:197], v161 offset:52224
	ds_read_b128 v[204:207], v161 offset:53248
	ds_read_b128 v[208:211], v161 offset:54272
	ds_read_b128 v[212:215], v161 offset:55296
	ds_read_b128 v[216:219], v161 offset:56320
	global_load_lds_dwordx4 v[198:199], off
	s_add_i32 m0, s4, 0x2000
	s_add_u32 s4, s52, 0x40080
	v_lshl_add_u64 v[198:199], v[220:221], 0, s[34:35]
	s_addc_u32 s5, s53, 0
	s_add_i32 s52, s76, s16
	global_load_lds_dwordx4 v[198:199], off
	v_lshl_add_u64 v[198:199], s[4:5], 0, v[136:137]
	s_mov_b32 m0, s52
	s_nop 0
	global_load_lds_dwordx4 v[198:199], off
	v_lshl_add_u64 v[198:199], s[4:5], 0, v[132:133]
	s_add_i32 m0, s52, 0x2000
	s_nop 0
	global_load_lds_dwordx4 v[198:199], off
	v_lshl_add_u64 v[198:199], s[12:13], 0, v[138:139]
	s_mov_b32 m0, s61
	s_nop 0
	global_load_lds_dwordx4 v[198:199], off
	v_lshl_add_u64 v[198:199], s[12:13], 0, v[134:135]
	s_mov_b32 m0, s62
	s_nop 0
	global_load_lds_dwordx4 v[198:199], off
	s_waitcnt vmcnt(8)
	s_waitcnt lgkmcnt(0)
	s_barrier
	s_setprio 1
	v_mfma_f32_16x16x32_bf16 v[64:67], v[148:151], v[182:185], v[64:67]
	v_mfma_f32_16x16x32_bf16 v[60:63], v[156:159], v[182:185], v[60:63]
	v_mfma_f32_16x16x32_bf16 v[48:51], v[148:151], v[190:193], v[48:51]
	v_mfma_f32_16x16x32_bf16 v[44:47], v[156:159], v[190:193], v[44:47]
	v_mfma_f32_16x16x32_bf16 v[32:35], v[148:151], v[204:207], v[32:35]
	v_mfma_f32_16x16x32_bf16 v[28:31], v[156:159], v[204:207], v[28:31]
	v_mfma_f32_16x16x32_bf16 v[16:19], v[148:151], v[212:215], v[16:19]
	v_mfma_f32_16x16x32_bf16 v[12:15], v[156:159], v[212:215], v[12:15]
	v_mfma_f32_16x16x32_bf16 v[64:67], v[152:155], v[186:189], v[64:67]
	v_mfma_f32_16x16x32_bf16 v[60:63], v[162:165], v[186:189], v[60:63]
	v_mfma_f32_16x16x32_bf16 v[48:51], v[152:155], v[194:197], v[48:51]
	v_mfma_f32_16x16x32_bf16 v[44:47], v[162:165], v[194:197], v[44:47]
	v_mfma_f32_16x16x32_bf16 v[32:35], v[152:155], v[208:211], v[32:35]
	v_mfma_f32_16x16x32_bf16 v[28:31], v[162:165], v[208:211], v[28:31]
	v_mfma_f32_16x16x32_bf16 v[16:19], v[152:155], v[216:219], v[16:19]
	v_mfma_f32_16x16x32_bf16 v[12:15], v[162:165], v[216:219], v[12:15]
	v_mfma_f32_16x16x32_bf16 v[56:59], v[166:169], v[182:185], v[56:59]
	v_mfma_f32_16x16x32_bf16 v[52:55], v[174:177], v[182:185], v[52:55]
	v_mfma_f32_16x16x32_bf16 v[40:43], v[166:169], v[190:193], v[40:43]
	v_mfma_f32_16x16x32_bf16 v[36:39], v[174:177], v[190:193], v[36:39]
	v_mfma_f32_16x16x32_bf16 v[24:27], v[166:169], v[204:207], v[24:27]
	v_mfma_f32_16x16x32_bf16 v[20:23], v[174:177], v[204:207], v[20:23]
	v_mfma_f32_16x16x32_bf16 v[8:11], v[166:169], v[212:215], v[8:11]
	v_mfma_f32_16x16x32_bf16 v[4:7], v[174:177], v[212:215], v[4:7]
	v_mfma_f32_16x16x32_bf16 v[56:59], v[170:173], v[186:189], v[56:59]
	v_mfma_f32_16x16x32_bf16 v[52:55], v[178:181], v[186:189], v[52:55]
	v_mfma_f32_16x16x32_bf16 v[40:43], v[170:173], v[194:197], v[40:43]
	v_mfma_f32_16x16x32_bf16 v[36:39], v[178:181], v[194:197], v[36:39]
	v_mfma_f32_16x16x32_bf16 v[24:27], v[170:173], v[208:211], v[24:27]
	v_mfma_f32_16x16x32_bf16 v[20:23], v[178:181], v[208:211], v[20:23]
	v_mfma_f32_16x16x32_bf16 v[8:11], v[170:173], v[216:219], v[8:11]
	v_mfma_f32_16x16x32_bf16 v[4:7], v[178:181], v[216:219], v[4:7]
	s_setprio 0
	s_barrier
	s_add_i32 s74, s74, 2
	s_add_u32 s50, s50, 0x100
	s_addc_u32 s51, s51, 0
	s_cmp_gt_u32 s74, 13
	s_cbranch_scc0 .LBB0_1380
	s_and_b64 vcc, exec, s[22:23]
	s_cbranch_vccz .LBB0_1383
	s_barrier

.LBB0_1458:
	s_ashr_i32 s41, s40, 31
	s_lshl_b64 s[4:5], s[40:41], 21
	s_add_u32 s42, s6, s4
	s_addc_u32 s43, s7, s5
	s_and_b64 s[4:5], s[38:39], exec
	s_cselect_b32 s41, s43, s49
	s_cselect_b32 s68, s42, s48
	s_ashr_i32 s37, s36, 31
	s_lshl_b64 s[4:5], s[36:37], 21
	s_add_u32 s44, s8, s4
	s_addc_u32 s45, s9, s5
	s_and_b64 s[4:5], s[38:39], exec
	s_cselect_b32 s37, s45, s51
	s_cselect_b32 s69, s44, s50
	s_add_u32 s70, s68, 0x80
	s_addc_u32 s71, s41, 0
	s_add_u32 s72, s50, 0x100
	s_addc_u32 s73, s51, 0
	s_add_u32 s4, s48, 0x100080
	s_addc_u32 s5, s49, 0
	v_lshl_add_u64 v[112:113], s[4:5], 0, v[210:211]
	v_lshl_add_u64 v[114:115], s[4:5], 0, v[212:213]
	s_mov_b32 s74, -2
	s_mov_b64 s[50:51], 0
	s_waitcnt lgkmcnt(0)
	s_waitcnt vmcnt(0)
	s_add_u32 s4, s48, s50
	s_addc_u32 s5, s49, s51
	s_add_u32 s75, s4, 0x100
	s_addc_u32 s76, s5, 0
	s_add_u32 s52, s72, s50
	s_addc_u32 s53, s73, s51
	s_add_u32 s4, s4, 0x180
	s_addc_u32 s5, s5, 0
	s_add_i32 s77, 0, 0x10000
	s_add_i32 s78, 0, 0x14000
	v_add_u32_e32 v148, s77, v203
	v_add_u32_e32 v164, s78, v203
	ds_read_b128 v[120:123], v148
	ds_read_b128 v[132:135], v148 offset:1024
	ds_read_b128 v[144:147], v148 offset:2048
	ds_read_b128 v[148:151], v148 offset:3072
	ds_read_b128 v[152:155], v164
	ds_read_b128 v[156:159], v164 offset:1024
	ds_read_b128 v[160:163], v164 offset:2048
	ds_read_b128 v[164:167], v164 offset:3072
	s_cmpk_eq_i32 s50, 0x1f00
	s_cselect_b32 s13, s71, s5
	s_cselect_b32 s12, s70, s4
	s_cselect_b32 s53, s37, s53
	s_cselect_b32 s52, s69, s52
	s_cselect_b32 s5, s41, s76
	s_cselect_b32 s4, s68, s75
	v_lshl_add_u64 v[214:215], v[112:113], 0, s[50:51]
	s_add_i32 m0, s17, 0xc000
	ds_read_b128 v[168:171], v233
	ds_read_b128 v[172:175], v233 offset:1024
	ds_read_b128 v[176:179], v233 offset:2048
	ds_read_b128 v[180:183], v233 offset:3072
	ds_read_b128 v[184:187], v233 offset:4096
	ds_read_b128 v[188:191], v233 offset:5120
	ds_read_b128 v[192:195], v233 offset:6144
	ds_read_b128 v[196:199], v233 offset:7168
	global_load_lds_dwordx4 v[214:215], off
	v_lshl_add_u64 v[214:215], v[114:115], 0, s[50:51]
	s_add_i32 m0, s17, 0xe000
	s_nop 0
	global_load_lds_dwordx4 v[214:215], off
	s_waitcnt vmcnt(8)
	s_waitcnt lgkmcnt(0)
	s_barrier
	s_setprio 1
	v_mfma_f32_16x16x32_bf16 v[140:143], v[120:123], v[168:171], 0
	v_mfma_f32_16x16x32_bf16 v[136:139], v[144:147], v[168:171], 0
	v_mfma_f32_16x16x32_bf16 v[116:119], v[120:123], v[176:179], 0
	v_mfma_f32_16x16x32_bf16 v[108:111], v[144:147], v[176:179], 0
	v_mfma_f32_16x16x32_bf16 v[96:99], v[120:123], v[184:187], 0
	v_mfma_f32_16x16x32_bf16 v[92:95], v[144:147], v[184:187], 0
	v_mfma_f32_16x16x32_bf16 v[80:83], v[120:123], v[192:195], 0
	v_mfma_f32_16x16x32_bf16 v[76:79], v[144:147], v[192:195], 0
	v_mfma_f32_16x16x32_bf16 v[140:143], v[132:135], v[172:175], v[140:143]
	v_mfma_f32_16x16x32_bf16 v[136:139], v[148:151], v[172:175], v[136:139]
	v_mfma_f32_16x16x32_bf16 v[116:119], v[132:135], v[180:183], v[116:119]
	v_mfma_f32_16x16x32_bf16 v[108:111], v[148:151], v[180:183], v[108:111]
	v_mfma_f32_16x16x32_bf16 v[96:99], v[132:135], v[188:191], v[96:99]
	v_mfma_f32_16x16x32_bf16 v[92:95], v[148:151], v[188:191], v[92:95]
	v_mfma_f32_16x16x32_bf16 v[80:83], v[132:135], v[196:199], v[80:83]
	v_mfma_f32_16x16x32_bf16 v[76:79], v[148:151], v[196:199], v[76:79]
	v_mfma_f32_16x16x32_bf16 v[128:131], v[152:155], v[168:171], 0
	v_mfma_f32_16x16x32_bf16 v[124:127], v[160:163], v[168:171], 0
	v_mfma_f32_16x16x32_bf16 v[104:107], v[152:155], v[176:179], 0
	v_mfma_f32_16x16x32_bf16 v[100:103], v[160:163], v[176:179], 0
	v_mfma_f32_16x16x32_bf16 v[88:91], v[152:155], v[184:187], 0
	v_mfma_f32_16x16x32_bf16 v[84:87], v[160:163], v[184:187], 0
	v_mfma_f32_16x16x32_bf16 v[72:75], v[152:155], v[192:195], 0
	v_mfma_f32_16x16x32_bf16 v[68:71], v[160:163], v[192:195], 0
	v_mfma_f32_16x16x32_bf16 v[128:131], v[156:159], v[172:175], v[128:131]
	v_mfma_f32_16x16x32_bf16 v[124:127], v[164:167], v[172:175], v[124:127]
	v_mfma_f32_16x16x32_bf16 v[104:107], v[156:159], v[180:183], v[104:107]
	v_mfma_f32_16x16x32_bf16 v[100:103], v[164:167], v[180:183], v[100:103]
	v_mfma_f32_16x16x32_bf16 v[88:91], v[156:159], v[188:191], v[88:91]
	v_mfma_f32_16x16x32_bf16 v[84:87], v[164:167], v[188:191], v[84:87]
	v_mfma_f32_16x16x32_bf16 v[72:75], v[156:159], v[196:199], v[72:75]
	v_mfma_f32_16x16x32_bf16 v[68:71], v[164:167], v[196:199], v[68:71]
	s_setprio 0
	s_barrier
	s_add_i32 s75, s77, s16
	v_lshl_add_u64 v[214:215], s[52:53], 0, v[2:3]
	s_mov_b32 m0, s75
	ds_read_b128 v[168:171], v233 offset:16384
	ds_read_b128 v[172:175], v233 offset:17408
	ds_read_b128 v[176:179], v233 offset:18432
	ds_read_b128 v[180:183], v233 offset:19456
	ds_read_b128 v[184:187], v233 offset:20480
	ds_read_b128 v[188:191], v233 offset:21504
	ds_read_b128 v[192:195], v233 offset:22528
	ds_read_b128 v[196:199], v233 offset:23552
	global_load_lds_dwordx4 v[214:215], off
	s_add_i32 m0, s75, 0x2000
	s_add_u32 s76, s52, 0x100000
	v_lshl_add_u64 v[216:217], s[52:53], 0, v[204:205]
	s_addc_u32 s77, s53, 0
	s_add_i32 s75, s78, s16
	global_load_lds_dwordx4 v[216:217], off
	v_lshl_add_u64 v[218:219], s[76:77], 0, v[2:3]
	s_mov_b32 m0, s75
	s_nop 0
	global_load_lds_dwordx4 v[218:219], off
	v_lshl_add_u64 v[218:219], s[76:77], 0, v[204:205]
	s_add_i32 m0, s75, 0x2000
	s_nop 0
	global_load_lds_dwordx4 v[218:219], off
	v_lshl_add_u64 v[218:219], s[4:5], 0, v[208:209]
	s_mov_b32 m0, s17
	s_nop 0
	global_load_lds_dwordx4 v[218:219], off
	v_lshl_add_u64 v[218:219], s[4:5], 0, v[206:207]
	s_mov_b32 m0, s46
	s_nop 0
	global_load_lds_dwordx4 v[218:219], off
	s_waitcnt vmcnt(8)
	s_waitcnt lgkmcnt(0)
	s_barrier
	s_setprio 1
	v_mfma_f32_16x16x32_bf16 v[64:67], v[120:123], v[168:171], 0
	v_mfma_f32_16x16x32_bf16 v[60:63], v[144:147], v[168:171], 0
	v_mfma_f32_16x16x32_bf16 v[48:51], v[120:123], v[176:179], 0
	v_mfma_f32_16x16x32_bf16 v[44:47], v[144:147], v[176:179], 0
	v_mfma_f32_16x16x32_bf16 v[32:35], v[120:123], v[184:187], 0
	v_mfma_f32_16x16x32_bf16 v[28:31], v[144:147], v[184:187], 0
	v_mfma_f32_16x16x32_bf16 v[16:19], v[120:123], v[192:195], 0
	v_mfma_f32_16x16x32_bf16 v[12:15], v[144:147], v[192:195], 0
	v_mfma_f32_16x16x32_bf16 v[64:67], v[132:135], v[172:175], v[64:67]
	v_mfma_f32_16x16x32_bf16 v[60:63], v[148:151], v[172:175], v[60:63]
	v_mfma_f32_16x16x32_bf16 v[48:51], v[132:135], v[180:183], v[48:51]
	v_mfma_f32_16x16x32_bf16 v[44:47], v[148:151], v[180:183], v[44:47]
	v_mfma_f32_16x16x32_bf16 v[32:35], v[132:135], v[188:191], v[32:35]
	v_mfma_f32_16x16x32_bf16 v[28:31], v[148:151], v[188:191], v[28:31]
	v_mfma_f32_16x16x32_bf16 v[16:19], v[132:135], v[196:199], v[16:19]
	v_mfma_f32_16x16x32_bf16 v[12:15], v[148:151], v[196:199], v[12:15]
	v_mfma_f32_16x16x32_bf16 v[56:59], v[152:155], v[168:171], 0
	v_mfma_f32_16x16x32_bf16 v[52:55], v[160:163], v[168:171], 0
	v_mfma_f32_16x16x32_bf16 v[40:43], v[152:155], v[176:179], 0
	v_mfma_f32_16x16x32_bf16 v[36:39], v[160:163], v[176:179], 0
	v_mfma_f32_16x16x32_bf16 v[24:27], v[152:155], v[184:187], 0
	v_mfma_f32_16x16x32_bf16 v[20:23], v[160:163], v[184:187], 0
	v_mfma_f32_16x16x32_bf16 v[8:11], v[152:155], v[192:195], 0
	v_mfma_f32_16x16x32_bf16 v[4:7], v[160:163], v[192:195], 0
	v_mfma_f32_16x16x32_bf16 v[56:59], v[156:159], v[172:175], v[56:59]
	v_mfma_f32_16x16x32_bf16 v[52:55], v[164:167], v[172:175], v[52:55]
	v_mfma_f32_16x16x32_bf16 v[40:43], v[156:159], v[180:183], v[40:43]
	v_mfma_f32_16x16x32_bf16 v[36:39], v[164:167], v[180:183], v[36:39]
	v_mfma_f32_16x16x32_bf16 v[24:27], v[156:159], v[188:191], v[24:27]
	v_mfma_f32_16x16x32_bf16 v[20:23], v[164:167], v[188:191], v[20:23]
	v_mfma_f32_16x16x32_bf16 v[8:11], v[156:159], v[196:199], v[8:11]
	v_mfma_f32_16x16x32_bf16 v[4:7], v[164:167], v[196:199], v[4:7]
	s_setprio 0
	s_barrier
	s_add_i32 s75, 0, 0x18000
	s_add_i32 s76, 0, 0x1c000
	v_add_u32_e32 v148, s75, v203
	v_add_u32_e32 v164, s76, v203
	ds_read_b128 v[120:123], v148
	ds_read_b128 v[132:135], v148 offset:1024
	ds_read_b128 v[144:147], v148 offset:2048
	ds_read_b128 v[148:151], v148 offset:3072
	ds_read_b128 v[152:155], v164
	ds_read_b128 v[156:159], v164 offset:1024
	ds_read_b128 v[160:163], v164 offset:2048
	ds_read_b128 v[164:167], v164 offset:3072
	s_add_u32 s4, s4, 0x100000
	s_addc_u32 s5, s5, 0
	s_mov_b32 m0, s47
	v_lshl_add_u64 v[218:219], s[4:5], 0, v[208:209]
	ds_read_b128 v[168:171], v233 offset:32768
	ds_read_b128 v[172:175], v233 offset:33792
	ds_read_b128 v[176:179], v233 offset:34816
	ds_read_b128 v[180:183], v233 offset:35840
	ds_read_b128 v[184:187], v233 offset:36864
	ds_read_b128 v[188:191], v233 offset:37888
	ds_read_b128 v[192:195], v233 offset:38912
	ds_read_b128 v[196:199], v233 offset:39936
	global_load_lds_dwordx4 v[218:219], off
	v_lshl_add_u64 v[218:219], s[4:5], 0, v[206:207]
	s_mov_b32 m0, s58
	s_nop 0
	global_load_lds_dwordx4 v[218:219], off
	s_waitcnt vmcnt(8)
	s_waitcnt lgkmcnt(0)
	s_barrier
	s_setprio 1
	v_mfma_f32_16x16x32_bf16 v[140:143], v[120:123], v[168:171], v[140:143]
	v_mfma_f32_16x16x32_bf16 v[136:139], v[144:147], v[168:171], v[136:139]
	v_mfma_f32_16x16x32_bf16 v[116:119], v[120:123], v[176:179], v[116:119]
	v_mfma_f32_16x16x32_bf16 v[108:111], v[144:147], v[176:179], v[108:111]
	v_mfma_f32_16x16x32_bf16 v[96:99], v[120:123], v[184:187], v[96:99]
	v_mfma_f32_16x16x32_bf16 v[92:95], v[144:147], v[184:187], v[92:95]
	v_mfma_f32_16x16x32_bf16 v[80:83], v[120:123], v[192:195], v[80:83]
	v_mfma_f32_16x16x32_bf16 v[76:79], v[144:147], v[192:195], v[76:79]
	v_mfma_f32_16x16x32_bf16 v[140:143], v[132:135], v[172:175], v[140:143]
	v_mfma_f32_16x16x32_bf16 v[136:139], v[148:151], v[172:175], v[136:139]
	v_mfma_f32_16x16x32_bf16 v[116:119], v[132:135], v[180:183], v[116:119]
	v_mfma_f32_16x16x32_bf16 v[108:111], v[148:151], v[180:183], v[108:111]
	v_mfma_f32_16x16x32_bf16 v[96:99], v[132:135], v[188:191], v[96:99]
	v_mfma_f32_16x16x32_bf16 v[92:95], v[148:151], v[188:191], v[92:95]
	v_mfma_f32_16x16x32_bf16 v[80:83], v[132:135], v[196:199], v[80:83]
	v_mfma_f32_16x16x32_bf16 v[76:79], v[148:151], v[196:199], v[76:79]
	v_mfma_f32_16x16x32_bf16 v[128:131], v[152:155], v[168:171], v[128:131]
	v_mfma_f32_16x16x32_bf16 v[124:127], v[160:163], v[168:171], v[124:127]
	v_mfma_f32_16x16x32_bf16 v[104:107], v[152:155], v[176:179], v[104:107]
	v_mfma_f32_16x16x32_bf16 v[100:103], v[160:163], v[176:179], v[100:103]
	v_mfma_f32_16x16x32_bf16 v[88:91], v[152:155], v[184:187], v[88:91]
	v_mfma_f32_16x16x32_bf16 v[84:87], v[160:163], v[184:187], v[84:87]
	v_mfma_f32_16x16x32_bf16 v[72:75], v[152:155], v[192:195], v[72:75]
	v_mfma_f32_16x16x32_bf16 v[68:71], v[160:163], v[192:195], v[68:71]
	v_mfma_f32_16x16x32_bf16 v[128:131], v[156:159], v[172:175], v[128:131]
	v_mfma_f32_16x16x32_bf16 v[124:127], v[164:167], v[172:175], v[124:127]
	v_mfma_f32_16x16x32_bf16 v[104:107], v[156:159], v[180:183], v[104:107]
	v_mfma_f32_16x16x32_bf16 v[100:103], v[164:167], v[180:183], v[100:103]
	v_mfma_f32_16x16x32_bf16 v[88:91], v[156:159], v[188:191], v[88:91]
	v_mfma_f32_16x16x32_bf16 v[84:87], v[164:167], v[188:191], v[84:87]
	v_mfma_f32_16x16x32_bf16 v[72:75], v[156:159], v[196:199], v[72:75]
	v_mfma_f32_16x16x32_bf16 v[68:71], v[164:167], v[196:199], v[68:71]
	s_setprio 0
	s_barrier
	s_add_i32 s4, s75, s16
	v_lshl_add_u64 v[214:215], v[214:215], 0, s[34:35]
	s_mov_b32 m0, s4
	ds_read_b128 v[168:171], v233 offset:49152
	ds_read_b128 v[172:175], v233 offset:50176
	ds_read_b128 v[176:179], v233 offset:51200
	ds_read_b128 v[180:183], v233 offset:52224
	ds_read_b128 v[184:187], v233 offset:53248
	ds_read_b128 v[188:191], v233 offset:54272
	ds_read_b128 v[192:195], v233 offset:55296
	ds_read_b128 v[196:199], v233 offset:56320
	global_load_lds_dwordx4 v[214:215], off
	s_add_i32 m0, s4, 0x2000
	s_add_u32 s4, s52, 0x100080
	v_lshl_add_u64 v[214:215], v[216:217], 0, s[34:35]
	s_addc_u32 s5, s53, 0
	s_add_i32 s52, s76, s16
	global_load_lds_dwordx4 v[214:215], off
	v_lshl_add_u64 v[214:215], s[4:5], 0, v[2:3]
	s_mov_b32 m0, s52
	s_nop 0
	global_load_lds_dwordx4 v[214:215], off
	v_lshl_add_u64 v[214:215], s[4:5], 0, v[204:205]
	s_add_i32 m0, s52, 0x2000
	s_nop 0
	global_load_lds_dwordx4 v[214:215], off
	v_lshl_add_u64 v[214:215], s[12:13], 0, v[208:209]
	s_mov_b32 m0, s62
	s_nop 0
	global_load_lds_dwordx4 v[214:215], off
	v_lshl_add_u64 v[214:215], s[12:13], 0, v[206:207]
	s_mov_b32 m0, s63
	s_nop 0
	global_load_lds_dwordx4 v[214:215], off
	s_waitcnt vmcnt(8)
	s_waitcnt lgkmcnt(0)
	s_barrier
	s_setprio 1
	v_mfma_f32_16x16x32_bf16 v[64:67], v[120:123], v[168:171], v[64:67]
	v_mfma_f32_16x16x32_bf16 v[60:63], v[144:147], v[168:171], v[60:63]
	v_mfma_f32_16x16x32_bf16 v[48:51], v[120:123], v[176:179], v[48:51]
	v_mfma_f32_16x16x32_bf16 v[44:47], v[144:147], v[176:179], v[44:47]
	v_mfma_f32_16x16x32_bf16 v[32:35], v[120:123], v[184:187], v[32:35]
	v_mfma_f32_16x16x32_bf16 v[28:31], v[144:147], v[184:187], v[28:31]
	v_mfma_f32_16x16x32_bf16 v[16:19], v[120:123], v[192:195], v[16:19]
	v_mfma_f32_16x16x32_bf16 v[12:15], v[144:147], v[192:195], v[12:15]
	v_mfma_f32_16x16x32_bf16 v[64:67], v[132:135], v[172:175], v[64:67]
	v_mfma_f32_16x16x32_bf16 v[60:63], v[148:151], v[172:175], v[60:63]
	v_mfma_f32_16x16x32_bf16 v[48:51], v[132:135], v[180:183], v[48:51]
	v_mfma_f32_16x16x32_bf16 v[44:47], v[148:151], v[180:183], v[44:47]
	v_mfma_f32_16x16x32_bf16 v[32:35], v[132:135], v[188:191], v[32:35]
	v_mfma_f32_16x16x32_bf16 v[28:31], v[148:151], v[188:191], v[28:31]
	v_mfma_f32_16x16x32_bf16 v[16:19], v[132:135], v[196:199], v[16:19]
	v_mfma_f32_16x16x32_bf16 v[12:15], v[148:151], v[196:199], v[12:15]
	v_mfma_f32_16x16x32_bf16 v[56:59], v[152:155], v[168:171], v[56:59]
	v_mfma_f32_16x16x32_bf16 v[52:55], v[160:163], v[168:171], v[52:55]
	v_mfma_f32_16x16x32_bf16 v[40:43], v[152:155], v[176:179], v[40:43]
	v_mfma_f32_16x16x32_bf16 v[36:39], v[160:163], v[176:179], v[36:39]
	v_mfma_f32_16x16x32_bf16 v[24:27], v[152:155], v[184:187], v[24:27]
	v_mfma_f32_16x16x32_bf16 v[20:23], v[160:163], v[184:187], v[20:23]
	v_mfma_f32_16x16x32_bf16 v[8:11], v[152:155], v[192:195], v[8:11]
	v_mfma_f32_16x16x32_bf16 v[4:7], v[160:163], v[192:195], v[4:7]
	v_mfma_f32_16x16x32_bf16 v[56:59], v[156:159], v[172:175], v[56:59]
	v_mfma_f32_16x16x32_bf16 v[52:55], v[164:167], v[172:175], v[52:55]
	v_mfma_f32_16x16x32_bf16 v[40:43], v[156:159], v[180:183], v[40:43]
	v_mfma_f32_16x16x32_bf16 v[36:39], v[164:167], v[180:183], v[36:39]
	v_mfma_f32_16x16x32_bf16 v[24:27], v[156:159], v[188:191], v[24:27]
	v_mfma_f32_16x16x32_bf16 v[20:23], v[164:167], v[188:191], v[20:23]
	v_mfma_f32_16x16x32_bf16 v[8:11], v[156:159], v[196:199], v[8:11]
	v_mfma_f32_16x16x32_bf16 v[4:7], v[164:167], v[196:199], v[4:7]
	s_setprio 0
	s_barrier
	s_add_i32 s74, s74, 2
	s_add_u32 s50, s50, 0x100
	s_addc_u32 s51, s51, 0
	s_cmp_gt_u32 s74, 61
.LBB0_1459:
	s_add_u32 s4, s48, s50
	s_addc_u32 s5, s49, s51
	s_add_u32 s75, s4, 0x100
	s_addc_u32 s76, s5, 0
	s_add_u32 s52, s72, s50
	s_addc_u32 s53, s73, s51
	s_add_u32 s4, s4, 0x180
	s_addc_u32 s5, s5, 0
	s_add_i32 s77, 0, 0x10000
	s_add_i32 s78, 0, 0x14000
	v_add_u32_e32 v148, s77, v203
	v_add_u32_e32 v164, s78, v203
	ds_read_b128 v[120:123], v148
	ds_read_b128 v[132:135], v148 offset:1024
	ds_read_b128 v[144:147], v148 offset:2048
	ds_read_b128 v[148:151], v148 offset:3072
	ds_read_b128 v[152:155], v164
	ds_read_b128 v[156:159], v164 offset:1024
	ds_read_b128 v[160:163], v164 offset:2048
	ds_read_b128 v[164:167], v164 offset:3072
	s_cmpk_eq_i32 s50, 0x1f00
	s_cselect_b32 s13, s71, s5
	s_cselect_b32 s12, s70, s4
	s_cselect_b32 s53, s37, s53
	s_cselect_b32 s52, s69, s52
	s_cselect_b32 s5, s41, s76
	s_cselect_b32 s4, s68, s75
	v_lshl_add_u64 v[214:215], v[112:113], 0, s[50:51]
	s_add_i32 m0, s17, 0xc000
	ds_read_b128 v[168:171], v233
	ds_read_b128 v[172:175], v233 offset:1024
	ds_read_b128 v[176:179], v233 offset:2048
	ds_read_b128 v[180:183], v233 offset:3072
	ds_read_b128 v[184:187], v233 offset:4096
	ds_read_b128 v[188:191], v233 offset:5120
	ds_read_b128 v[192:195], v233 offset:6144
	ds_read_b128 v[196:199], v233 offset:7168
	global_load_lds_dwordx4 v[214:215], off
	v_lshl_add_u64 v[214:215], v[114:115], 0, s[50:51]
	s_add_i32 m0, s17, 0xe000
	s_nop 0
	global_load_lds_dwordx4 v[214:215], off
	s_waitcnt vmcnt(8)
	s_waitcnt lgkmcnt(0)
	s_barrier
	s_setprio 1
	v_mfma_f32_16x16x32_bf16 v[140:143], v[120:123], v[168:171], v[140:143]
	v_mfma_f32_16x16x32_bf16 v[136:139], v[144:147], v[168:171], v[136:139]
	v_mfma_f32_16x16x32_bf16 v[116:119], v[120:123], v[176:179], v[116:119]
	v_mfma_f32_16x16x32_bf16 v[108:111], v[144:147], v[176:179], v[108:111]
	v_mfma_f32_16x16x32_bf16 v[96:99], v[120:123], v[184:187], v[96:99]
	v_mfma_f32_16x16x32_bf16 v[92:95], v[144:147], v[184:187], v[92:95]
	v_mfma_f32_16x16x32_bf16 v[80:83], v[120:123], v[192:195], v[80:83]
	v_mfma_f32_16x16x32_bf16 v[76:79], v[144:147], v[192:195], v[76:79]
	v_mfma_f32_16x16x32_bf16 v[140:143], v[132:135], v[172:175], v[140:143]
	v_mfma_f32_16x16x32_bf16 v[136:139], v[148:151], v[172:175], v[136:139]
	v_mfma_f32_16x16x32_bf16 v[116:119], v[132:135], v[180:183], v[116:119]
	v_mfma_f32_16x16x32_bf16 v[108:111], v[148:151], v[180:183], v[108:111]
	v_mfma_f32_16x16x32_bf16 v[96:99], v[132:135], v[188:191], v[96:99]
	v_mfma_f32_16x16x32_bf16 v[92:95], v[148:151], v[188:191], v[92:95]
	v_mfma_f32_16x16x32_bf16 v[80:83], v[132:135], v[196:199], v[80:83]
	v_mfma_f32_16x16x32_bf16 v[76:79], v[148:151], v[196:199], v[76:79]
	v_mfma_f32_16x16x32_bf16 v[128:131], v[152:155], v[168:171], v[128:131]
	v_mfma_f32_16x16x32_bf16 v[124:127], v[160:163], v[168:171], v[124:127]
	v_mfma_f32_16x16x32_bf16 v[104:107], v[152:155], v[176:179], v[104:107]
	v_mfma_f32_16x16x32_bf16 v[100:103], v[160:163], v[176:179], v[100:103]
	v_mfma_f32_16x16x32_bf16 v[88:91], v[152:155], v[184:187], v[88:91]
	v_mfma_f32_16x16x32_bf16 v[84:87], v[160:163], v[184:187], v[84:87]
	v_mfma_f32_16x16x32_bf16 v[72:75], v[152:155], v[192:195], v[72:75]
	v_mfma_f32_16x16x32_bf16 v[68:71], v[160:163], v[192:195], v[68:71]
	v_mfma_f32_16x16x32_bf16 v[128:131], v[156:159], v[172:175], v[128:131]
	v_mfma_f32_16x16x32_bf16 v[124:127], v[164:167], v[172:175], v[124:127]
	v_mfma_f32_16x16x32_bf16 v[104:107], v[156:159], v[180:183], v[104:107]
	v_mfma_f32_16x16x32_bf16 v[100:103], v[164:167], v[180:183], v[100:103]
	v_mfma_f32_16x16x32_bf16 v[88:91], v[156:159], v[188:191], v[88:91]
	v_mfma_f32_16x16x32_bf16 v[84:87], v[164:167], v[188:191], v[84:87]
	v_mfma_f32_16x16x32_bf16 v[72:75], v[156:159], v[196:199], v[72:75]
	v_mfma_f32_16x16x32_bf16 v[68:71], v[164:167], v[196:199], v[68:71]
	s_setprio 0
	s_barrier
	s_add_i32 s75, s77, s16
	v_lshl_add_u64 v[214:215], s[52:53], 0, v[2:3]
	s_mov_b32 m0, s75
	ds_read_b128 v[168:171], v233 offset:16384
	ds_read_b128 v[172:175], v233 offset:17408
	ds_read_b128 v[176:179], v233 offset:18432
	ds_read_b128 v[180:183], v233 offset:19456
	ds_read_b128 v[184:187], v233 offset:20480
	ds_read_b128 v[188:191], v233 offset:21504
	ds_read_b128 v[192:195], v233 offset:22528
	ds_read_b128 v[196:199], v233 offset:23552
	global_load_lds_dwordx4 v[214:215], off
	s_add_i32 m0, s75, 0x2000
	s_add_u32 s76, s52, 0x100000
	v_lshl_add_u64 v[216:217], s[52:53], 0, v[204:205]
	s_addc_u32 s77, s53, 0
	s_add_i32 s75, s78, s16
	global_load_lds_dwordx4 v[216:217], off
	v_lshl_add_u64 v[218:219], s[76:77], 0, v[2:3]
	s_mov_b32 m0, s75
	s_nop 0
	global_load_lds_dwordx4 v[218:219], off
	v_lshl_add_u64 v[218:219], s[76:77], 0, v[204:205]
	s_add_i32 m0, s75, 0x2000
	s_nop 0
	global_load_lds_dwordx4 v[218:219], off
	v_lshl_add_u64 v[218:219], s[4:5], 0, v[208:209]
	s_mov_b32 m0, s17
	s_nop 0
	global_load_lds_dwordx4 v[218:219], off
	v_lshl_add_u64 v[218:219], s[4:5], 0, v[206:207]
	s_mov_b32 m0, s46
	s_nop 0
	global_load_lds_dwordx4 v[218:219], off
	s_waitcnt vmcnt(8)
	s_waitcnt lgkmcnt(0)
	s_barrier
	s_setprio 1
	v_mfma_f32_16x16x32_bf16 v[64:67], v[120:123], v[168:171], v[64:67]
	v_mfma_f32_16x16x32_bf16 v[60:63], v[144:147], v[168:171], v[60:63]
	v_mfma_f32_16x16x32_bf16 v[48:51], v[120:123], v[176:179], v[48:51]
	v_mfma_f32_16x16x32_bf16 v[44:47], v[144:147], v[176:179], v[44:47]
	v_mfma_f32_16x16x32_bf16 v[32:35], v[120:123], v[184:187], v[32:35]
	v_mfma_f32_16x16x32_bf16 v[28:31], v[144:147], v[184:187], v[28:31]
	v_mfma_f32_16x16x32_bf16 v[16:19], v[120:123], v[192:195], v[16:19]
	v_mfma_f32_16x16x32_bf16 v[12:15], v[144:147], v[192:195], v[12:15]
	v_mfma_f32_16x16x32_bf16 v[64:67], v[132:135], v[172:175], v[64:67]
	v_mfma_f32_16x16x32_bf16 v[60:63], v[148:151], v[172:175], v[60:63]
	v_mfma_f32_16x16x32_bf16 v[48:51], v[132:135], v[180:183], v[48:51]
	v_mfma_f32_16x16x32_bf16 v[44:47], v[148:151], v[180:183], v[44:47]
	v_mfma_f32_16x16x32_bf16 v[32:35], v[132:135], v[188:191], v[32:35]
	v_mfma_f32_16x16x32_bf16 v[28:31], v[148:151], v[188:191], v[28:31]
	v_mfma_f32_16x16x32_bf16 v[16:19], v[132:135], v[196:199], v[16:19]
	v_mfma_f32_16x16x32_bf16 v[12:15], v[148:151], v[196:199], v[12:15]
	v_mfma_f32_16x16x32_bf16 v[56:59], v[152:155], v[168:171], v[56:59]
	v_mfma_f32_16x16x32_bf16 v[52:55], v[160:163], v[168:171], v[52:55]
	v_mfma_f32_16x16x32_bf16 v[40:43], v[152:155], v[176:179], v[40:43]
	v_mfma_f32_16x16x32_bf16 v[36:39], v[160:163], v[176:179], v[36:39]
	v_mfma_f32_16x16x32_bf16 v[24:27], v[152:155], v[184:187], v[24:27]
	v_mfma_f32_16x16x32_bf16 v[20:23], v[160:163], v[184:187], v[20:23]
	v_mfma_f32_16x16x32_bf16 v[8:11], v[152:155], v[192:195], v[8:11]
	v_mfma_f32_16x16x32_bf16 v[4:7], v[160:163], v[192:195], v[4:7]
	v_mfma_f32_16x16x32_bf16 v[56:59], v[156:159], v[172:175], v[56:59]
	v_mfma_f32_16x16x32_bf16 v[52:55], v[164:167], v[172:175], v[52:55]
	v_mfma_f32_16x16x32_bf16 v[40:43], v[156:159], v[180:183], v[40:43]
	v_mfma_f32_16x16x32_bf16 v[36:39], v[164:167], v[180:183], v[36:39]
	v_mfma_f32_16x16x32_bf16 v[24:27], v[156:159], v[188:191], v[24:27]
	v_mfma_f32_16x16x32_bf16 v[20:23], v[164:167], v[188:191], v[20:23]
	v_mfma_f32_16x16x32_bf16 v[8:11], v[156:159], v[196:199], v[8:11]
	v_mfma_f32_16x16x32_bf16 v[4:7], v[164:167], v[196:199], v[4:7]
	s_setprio 0
	s_barrier
	s_add_i32 s75, 0, 0x18000
	s_add_i32 s76, 0, 0x1c000
	v_add_u32_e32 v148, s75, v203
	v_add_u32_e32 v164, s76, v203
	ds_read_b128 v[120:123], v148
	ds_read_b128 v[132:135], v148 offset:1024
	ds_read_b128 v[144:147], v148 offset:2048
	ds_read_b128 v[148:151], v148 offset:3072
	ds_read_b128 v[152:155], v164
	ds_read_b128 v[156:159], v164 offset:1024
	ds_read_b128 v[160:163], v164 offset:2048
	ds_read_b128 v[164:167], v164 offset:3072
	s_add_u32 s4, s4, 0x100000
	s_addc_u32 s5, s5, 0
	s_mov_b32 m0, s47
	v_lshl_add_u64 v[218:219], s[4:5], 0, v[208:209]
	ds_read_b128 v[168:171], v233 offset:32768
	ds_read_b128 v[172:175], v233 offset:33792
	ds_read_b128 v[176:179], v233 offset:34816
	ds_read_b128 v[180:183], v233 offset:35840
	ds_read_b128 v[184:187], v233 offset:36864
	ds_read_b128 v[188:191], v233 offset:37888
	ds_read_b128 v[192:195], v233 offset:38912
	ds_read_b128 v[196:199], v233 offset:39936
	global_load_lds_dwordx4 v[218:219], off
	v_lshl_add_u64 v[218:219], s[4:5], 0, v[206:207]
	s_mov_b32 m0, s58
	s_nop 0
	global_load_lds_dwordx4 v[218:219], off
	s_waitcnt vmcnt(8)
	s_waitcnt lgkmcnt(0)
	s_barrier
	s_setprio 1
	v_mfma_f32_16x16x32_bf16 v[140:143], v[120:123], v[168:171], v[140:143]
	v_mfma_f32_16x16x32_bf16 v[136:139], v[144:147], v[168:171], v[136:139]
	v_mfma_f32_16x16x32_bf16 v[116:119], v[120:123], v[176:179], v[116:119]
	v_mfma_f32_16x16x32_bf16 v[108:111], v[144:147], v[176:179], v[108:111]
	v_mfma_f32_16x16x32_bf16 v[96:99], v[120:123], v[184:187], v[96:99]
	v_mfma_f32_16x16x32_bf16 v[92:95], v[144:147], v[184:187], v[92:95]
	v_mfma_f32_16x16x32_bf16 v[80:83], v[120:123], v[192:195], v[80:83]
	v_mfma_f32_16x16x32_bf16 v[76:79], v[144:147], v[192:195], v[76:79]
	v_mfma_f32_16x16x32_bf16 v[140:143], v[132:135], v[172:175], v[140:143]
	v_mfma_f32_16x16x32_bf16 v[136:139], v[148:151], v[172:175], v[136:139]
	v_mfma_f32_16x16x32_bf16 v[116:119], v[132:135], v[180:183], v[116:119]
	v_mfma_f32_16x16x32_bf16 v[108:111], v[148:151], v[180:183], v[108:111]
	v_mfma_f32_16x16x32_bf16 v[96:99], v[132:135], v[188:191], v[96:99]
	v_mfma_f32_16x16x32_bf16 v[92:95], v[148:151], v[188:191], v[92:95]
	v_mfma_f32_16x16x32_bf16 v[80:83], v[132:135], v[196:199], v[80:83]
	v_mfma_f32_16x16x32_bf16 v[76:79], v[148:151], v[196:199], v[76:79]
	v_mfma_f32_16x16x32_bf16 v[128:131], v[152:155], v[168:171], v[128:131]
	v_mfma_f32_16x16x32_bf16 v[124:127], v[160:163], v[168:171], v[124:127]
	v_mfma_f32_16x16x32_bf16 v[104:107], v[152:155], v[176:179], v[104:107]
	v_mfma_f32_16x16x32_bf16 v[100:103], v[160:163], v[176:179], v[100:103]
	v_mfma_f32_16x16x32_bf16 v[88:91], v[152:155], v[184:187], v[88:91]
	v_mfma_f32_16x16x32_bf16 v[84:87], v[160:163], v[184:187], v[84:87]
	v_mfma_f32_16x16x32_bf16 v[72:75], v[152:155], v[192:195], v[72:75]
	v_mfma_f32_16x16x32_bf16 v[68:71], v[160:163], v[192:195], v[68:71]
	v_mfma_f32_16x16x32_bf16 v[128:131], v[156:159], v[172:175], v[128:131]
	v_mfma_f32_16x16x32_bf16 v[124:127], v[164:167], v[172:175], v[124:127]
	v_mfma_f32_16x16x32_bf16 v[104:107], v[156:159], v[180:183], v[104:107]
	v_mfma_f32_16x16x32_bf16 v[100:103], v[164:167], v[180:183], v[100:103]
	v_mfma_f32_16x16x32_bf16 v[88:91], v[156:159], v[188:191], v[88:91]
	v_mfma_f32_16x16x32_bf16 v[84:87], v[164:167], v[188:191], v[84:87]
	v_mfma_f32_16x16x32_bf16 v[72:75], v[156:159], v[196:199], v[72:75]
	v_mfma_f32_16x16x32_bf16 v[68:71], v[164:167], v[196:199], v[68:71]
	s_setprio 0
	s_barrier
	s_add_i32 s4, s75, s16
	v_lshl_add_u64 v[214:215], v[214:215], 0, s[34:35]
	s_mov_b32 m0, s4
	ds_read_b128 v[168:171], v233 offset:49152
	ds_read_b128 v[172:175], v233 offset:50176
	ds_read_b128 v[176:179], v233 offset:51200
	ds_read_b128 v[180:183], v233 offset:52224
	ds_read_b128 v[184:187], v233 offset:53248
	ds_read_b128 v[188:191], v233 offset:54272
	ds_read_b128 v[192:195], v233 offset:55296
	ds_read_b128 v[196:199], v233 offset:56320
	global_load_lds_dwordx4 v[214:215], off
	s_add_i32 m0, s4, 0x2000
	s_add_u32 s4, s52, 0x100080
	v_lshl_add_u64 v[214:215], v[216:217], 0, s[34:35]
	s_addc_u32 s5, s53, 0
	s_add_i32 s52, s76, s16
	global_load_lds_dwordx4 v[214:215], off
	v_lshl_add_u64 v[214:215], s[4:5], 0, v[2:3]
	s_mov_b32 m0, s52
	s_nop 0
	global_load_lds_dwordx4 v[214:215], off
	v_lshl_add_u64 v[214:215], s[4:5], 0, v[204:205]
	s_add_i32 m0, s52, 0x2000
	s_nop 0
	global_load_lds_dwordx4 v[214:215], off
	v_lshl_add_u64 v[214:215], s[12:13], 0, v[208:209]
	s_mov_b32 m0, s62
	s_nop 0
	global_load_lds_dwordx4 v[214:215], off
	v_lshl_add_u64 v[214:215], s[12:13], 0, v[206:207]
	s_mov_b32 m0, s63
	s_nop 0
	global_load_lds_dwordx4 v[214:215], off
	s_waitcnt vmcnt(8)
	s_waitcnt lgkmcnt(0)
	s_barrier
	s_setprio 1
	v_mfma_f32_16x16x32_bf16 v[64:67], v[120:123], v[168:171], v[64:67]
	v_mfma_f32_16x16x32_bf16 v[60:63], v[144:147], v[168:171], v[60:63]
	v_mfma_f32_16x16x32_bf16 v[48:51], v[120:123], v[176:179], v[48:51]
	v_mfma_f32_16x16x32_bf16 v[44:47], v[144:147], v[176:179], v[44:47]
	v_mfma_f32_16x16x32_bf16 v[32:35], v[120:123], v[184:187], v[32:35]
	v_mfma_f32_16x16x32_bf16 v[28:31], v[144:147], v[184:187], v[28:31]
	v_mfma_f32_16x16x32_bf16 v[16:19], v[120:123], v[192:195], v[16:19]
	v_mfma_f32_16x16x32_bf16 v[12:15], v[144:147], v[192:195], v[12:15]
	v_mfma_f32_16x16x32_bf16 v[64:67], v[132:135], v[172:175], v[64:67]
	v_mfma_f32_16x16x32_bf16 v[60:63], v[148:151], v[172:175], v[60:63]
	v_mfma_f32_16x16x32_bf16 v[48:51], v[132:135], v[180:183], v[48:51]
	v_mfma_f32_16x16x32_bf16 v[44:47], v[148:151], v[180:183], v[44:47]
	v_mfma_f32_16x16x32_bf16 v[32:35], v[132:135], v[188:191], v[32:35]
	v_mfma_f32_16x16x32_bf16 v[28:31], v[148:151], v[188:191], v[28:31]
	v_mfma_f32_16x16x32_bf16 v[16:19], v[132:135], v[196:199], v[16:19]
	v_mfma_f32_16x16x32_bf16 v[12:15], v[148:151], v[196:199], v[12:15]
	v_mfma_f32_16x16x32_bf16 v[56:59], v[152:155], v[168:171], v[56:59]
	v_mfma_f32_16x16x32_bf16 v[52:55], v[160:163], v[168:171], v[52:55]
	v_mfma_f32_16x16x32_bf16 v[40:43], v[152:155], v[176:179], v[40:43]
	v_mfma_f32_16x16x32_bf16 v[36:39], v[160:163], v[176:179], v[36:39]
	v_mfma_f32_16x16x32_bf16 v[24:27], v[152:155], v[184:187], v[24:27]
	v_mfma_f32_16x16x32_bf16 v[20:23], v[160:163], v[184:187], v[20:23]
	v_mfma_f32_16x16x32_bf16 v[8:11], v[152:155], v[192:195], v[8:11]
	v_mfma_f32_16x16x32_bf16 v[4:7], v[160:163], v[192:195], v[4:7]
	v_mfma_f32_16x16x32_bf16 v[56:59], v[156:159], v[172:175], v[56:59]
	v_mfma_f32_16x16x32_bf16 v[52:55], v[164:167], v[172:175], v[52:55]
	v_mfma_f32_16x16x32_bf16 v[40:43], v[156:159], v[180:183], v[40:43]
	v_mfma_f32_16x16x32_bf16 v[36:39], v[164:167], v[180:183], v[36:39]
	v_mfma_f32_16x16x32_bf16 v[24:27], v[156:159], v[188:191], v[24:27]
	v_mfma_f32_16x16x32_bf16 v[20:23], v[164:167], v[188:191], v[20:23]
	v_mfma_f32_16x16x32_bf16 v[8:11], v[156:159], v[196:199], v[8:11]
	v_mfma_f32_16x16x32_bf16 v[4:7], v[164:167], v[196:199], v[4:7]
	s_setprio 0
	s_barrier
	s_add_i32 s74, s74, 2
	s_add_u32 s50, s50, 0x100
	s_addc_u32 s51, s51, 0
	s_cmp_gt_u32 s74, 61
	s_cbranch_scc0 .LBB0_1459
	s_and_b64 vcc, exec, s[22:23]
	s_cbranch_vccz .LBB0_1462
	s_barrier
